# stack: P12 adjacent column-tile pairs per XCD + P13 reuses P12 block table + hand-written 3-deep down-weight conversion + hand-written S5 Kd stage, on top of previous best
# speedup vs baseline: 1.1584x; 1.0017x over previous
; __device__ __forceinline__ void s5_setup(int g, LAS unsigned char* lds, const float* lam_re, const float* lam_im, const float* log_dt, const float* b_re, const float* b_im,
;                                          const float* c_re, const float* c_im, bf16* BTY, bf16* BTS, float* AP32, int tid) {
;     ...
;     for (int idx = tid; idx < 32 * 256; idx += NTHR) { const int d = idx >> 8, co = (idx >> 4) & 15, ci = idx & 15; float a = 0.f;
;         for (int p = 0; p < 64; ++p) { const float cr = ccr[co * 64 + p], cm = cci[co * 64 + p], ar = apr[d * 64 + p], ai = api[d * 64 + p];
;             const float car = cr * ar - cm * ai, cai = cr * ai + cm * ar; a += car * bbr[p * 16 + ci] - cai * bbi[p * 16 + ci]; }
;         Kd[idx] = a; }
.LBB0_58:
	s_or_b64 exec, exec, s[4:5]
	s_movk_i32 s0, 0x2000
	v_cmp_gt_i32_e32 vcc, s0, v132
	s_waitcnt lgkmcnt(0)
	s_barrier
	s_and_saveexec_b64 s[4:5], vcc
	s_cbranch_execz .LBB0_63
	v_bfe_u32 v222, v132, 4, 4
	v_lshlrev_b32_e32 v222, 8, v222
	v_and_b32_e32 v223, 15, v132
	v_lshlrev_b32_e32 v223, 2, v223
	v_add_u32_e32 v224, 0x4200, v223
	v_add_u32_e32 v228, 0x5200, v223
	v_add_u32_e32 v225, 0x4600, v223
	v_add_u32_e32 v229, 0x5600, v223
	v_add_u32_e32 v226, 0x4a00, v223
	v_add_u32_e32 v230, 0x5a00, v223
	v_add_u32_e32 v227, 0x4e00, v223
	v_add_u32_e32 v231, 0x5e00, v223
	s_lshr_b32 s1, s89, 2
	s_lshl_b32 s1, s1, 8
	v_mov_b32_e32 v220, s1
	v_lshlrev_b32_e32 v221, 2, v132
	ds_read_b128 v[200:203], v222 offset:25088
	ds_read_b128 v[204:207], v222 offset:29184
	ds_read2_b32 v[208:209], v224 offset0:0 offset1:16
	ds_read2_b32 v[210:211], v224 offset0:32 offset1:48
	ds_read2_b32 v[212:213], v228 offset0:0 offset1:16
	ds_read2_b32 v[214:215], v228 offset0:32 offset1:48
	s_waitcnt lgkmcnt(0)
	v_mul_f32_e32 v16, v200, v208
	v_mul_f32_e64 v136, -v200, v212
	v_fma_f32 v16, -v204, v212, v16
	v_fma_f32 v136, -v204, v208, v136
	v_mul_f32_e32 v17, v201, v209
	v_mul_f32_e64 v137, -v201, v213
	v_fma_f32 v17, -v205, v213, v17
	v_fma_f32 v137, -v205, v209, v137
	v_mul_f32_e32 v18, v202, v210
	v_mul_f32_e64 v138, -v202, v214
	v_fma_f32 v18, -v206, v214, v18
	v_fma_f32 v138, -v206, v210, v138
	v_mul_f32_e32 v19, v203, v211
	v_mul_f32_e64 v139, -v203, v215
	v_fma_f32 v19, -v207, v215, v19
	v_fma_f32 v139, -v207, v211, v139
	ds_read_b128 v[200:203], v222 offset:25104
	ds_read_b128 v[204:207], v222 offset:29200
	ds_read2_b32 v[208:209], v224 offset0:64 offset1:80
	ds_read2_b32 v[210:211], v224 offset0:96 offset1:112
	ds_read2_b32 v[212:213], v228 offset0:64 offset1:80
	ds_read2_b32 v[214:215], v228 offset0:96 offset1:112
	s_waitcnt lgkmcnt(0)
	v_mul_f32_e32 v20, v200, v208
	v_mul_f32_e64 v140, -v200, v212
	v_fma_f32 v20, -v204, v212, v20
	v_fma_f32 v140, -v204, v208, v140
	v_mul_f32_e32 v21, v201, v209
	v_mul_f32_e64 v141, -v201, v213
	v_fma_f32 v21, -v205, v213, v21
	v_fma_f32 v141, -v205, v209, v141
	v_mul_f32_e32 v22, v202, v210
	v_mul_f32_e64 v142, -v202, v214
	v_fma_f32 v22, -v206, v214, v22
	v_fma_f32 v142, -v206, v210, v142
	v_mul_f32_e32 v23, v203, v211
	v_mul_f32_e64 v143, -v203, v215
	v_fma_f32 v23, -v207, v215, v23
	v_fma_f32 v143, -v207, v211, v143
	ds_read_b128 v[200:203], v222 offset:25120
	ds_read_b128 v[204:207], v222 offset:29216
	ds_read2_b32 v[208:209], v224 offset0:128 offset1:144
	ds_read2_b32 v[210:211], v224 offset0:160 offset1:176
	ds_read2_b32 v[212:213], v228 offset0:128 offset1:144
	ds_read2_b32 v[214:215], v228 offset0:160 offset1:176
	s_waitcnt lgkmcnt(0)
	v_mul_f32_e32 v24, v200, v208
	v_mul_f32_e64 v144, -v200, v212
	v_fma_f32 v24, -v204, v212, v24
	v_fma_f32 v144, -v204, v208, v144
	v_mul_f32_e32 v25, v201, v209
	v_mul_f32_e64 v145, -v201, v213
	v_fma_f32 v25, -v205, v213, v25
	v_fma_f32 v145, -v205, v209, v145
	v_mul_f32_e32 v26, v202, v210
	v_mul_f32_e64 v146, -v202, v214
	v_fma_f32 v26, -v206, v214, v26
	v_fma_f32 v146, -v206, v210, v146
	v_mul_f32_e32 v27, v203, v211
	v_mul_f32_e64 v147, -v203, v215
	v_fma_f32 v27, -v207, v215, v27
	v_fma_f32 v147, -v207, v211, v147
	ds_read_b128 v[200:203], v222 offset:25136
	ds_read_b128 v[204:207], v222 offset:29232
	ds_read2_b32 v[208:209], v224 offset0:192 offset1:208
	ds_read2_b32 v[210:211], v224 offset0:224 offset1:240
	ds_read2_b32 v[212:213], v228 offset0:192 offset1:208
	ds_read2_b32 v[214:215], v228 offset0:224 offset1:240
	s_waitcnt lgkmcnt(0)
	v_mul_f32_e32 v28, v200, v208
	v_mul_f32_e64 v148, -v200, v212
	v_fma_f32 v28, -v204, v212, v28
	v_fma_f32 v148, -v204, v208, v148
	v_mul_f32_e32 v29, v201, v209
	v_mul_f32_e64 v149, -v201, v213
	v_fma_f32 v29, -v205, v213, v29
	v_fma_f32 v149, -v205, v209, v149
	v_mul_f32_e32 v30, v202, v210
	v_mul_f32_e64 v150, -v202, v214
	v_fma_f32 v30, -v206, v214, v30
	v_fma_f32 v150, -v206, v210, v150
	v_mul_f32_e32 v31, v203, v211
	v_mul_f32_e64 v151, -v203, v215
	v_fma_f32 v31, -v207, v215, v31
	v_fma_f32 v151, -v207, v211, v151
	ds_read_b128 v[200:203], v222 offset:25152
	ds_read_b128 v[204:207], v222 offset:29248
	ds_read2_b32 v[208:209], v225 offset0:0 offset1:16
	ds_read2_b32 v[210:211], v225 offset0:32 offset1:48
	ds_read2_b32 v[212:213], v229 offset0:0 offset1:16
	ds_read2_b32 v[214:215], v229 offset0:32 offset1:48
	s_waitcnt lgkmcnt(0)
	v_mul_f32_e32 v32, v200, v208
	v_mul_f32_e64 v152, -v200, v212
	v_fma_f32 v32, -v204, v212, v32
	v_fma_f32 v152, -v204, v208, v152
	v_mul_f32_e32 v33, v201, v209
	v_mul_f32_e64 v153, -v201, v213
	v_fma_f32 v33, -v205, v213, v33
	v_fma_f32 v153, -v205, v209, v153
	v_mul_f32_e32 v34, v202, v210
	v_mul_f32_e64 v154, -v202, v214
	v_fma_f32 v34, -v206, v214, v34
	v_fma_f32 v154, -v206, v210, v154
	v_mul_f32_e32 v35, v203, v211
	v_mul_f32_e64 v155, -v203, v215
	v_fma_f32 v35, -v207, v215, v35
	v_fma_f32 v155, -v207, v211, v155
	ds_read_b128 v[200:203], v222 offset:25168
	ds_read_b128 v[204:207], v222 offset:29264
	ds_read2_b32 v[208:209], v225 offset0:64 offset1:80
	ds_read2_b32 v[210:211], v225 offset0:96 offset1:112
	ds_read2_b32 v[212:213], v229 offset0:64 offset1:80
	ds_read2_b32 v[214:215], v229 offset0:96 offset1:112
	s_waitcnt lgkmcnt(0)
; __device__ __forceinline__ void s5_setup(int g, LAS unsigned char* lds, const float* lam_re, const float* lam_im, const float* log_dt, const float* b_re, const float* b_im,
;                                          const float* c_re, const float* c_im, bf16* BTY, bf16* BTS, float* AP32, int tid) {
;     ...
;     for (int idx = tid; idx < 32 * 256; idx += NTHR) { const int d = idx >> 8, co = (idx >> 4) & 15, ci = idx & 15; float a = 0.f;
;         for (int p = 0; p < 64; ++p) { const float cr = ccr[co * 64 + p], cm = cci[co * 64 + p], ar = apr[d * 64 + p], ai = api[d * 64 + p];
;             const float car = cr * ar - cm * ai, cai = cr * ai + cm * ar; a += car * bbr[p * 16 + ci] - cai * bbi[p * 16 + ci]; }
;         Kd[idx] = a; }
	v_mul_f32_e32 v36, v200, v208
	v_mul_f32_e64 v156, -v200, v212
	v_fma_f32 v36, -v204, v212, v36
	v_fma_f32 v156, -v204, v208, v156
	v_mul_f32_e32 v37, v201, v209
	v_mul_f32_e64 v157, -v201, v213
	v_fma_f32 v37, -v205, v213, v37
	v_fma_f32 v157, -v205, v209, v157
	v_mul_f32_e32 v38, v202, v210
	v_mul_f32_e64 v158, -v202, v214
	v_fma_f32 v38, -v206, v214, v38
	v_fma_f32 v158, -v206, v210, v158
	v_mul_f32_e32 v39, v203, v211
	v_mul_f32_e64 v159, -v203, v215
	v_fma_f32 v39, -v207, v215, v39
	v_fma_f32 v159, -v207, v211, v159
	ds_read_b128 v[200:203], v222 offset:25184
	ds_read_b128 v[204:207], v222 offset:29280
	ds_read2_b32 v[208:209], v225 offset0:128 offset1:144
	ds_read2_b32 v[210:211], v225 offset0:160 offset1:176
	ds_read2_b32 v[212:213], v229 offset0:128 offset1:144
	ds_read2_b32 v[214:215], v229 offset0:160 offset1:176
	s_waitcnt lgkmcnt(0)
	v_mul_f32_e32 v40, v200, v208
	v_mul_f32_e64 v160, -v200, v212
	v_fma_f32 v40, -v204, v212, v40
	v_fma_f32 v160, -v204, v208, v160
	v_mul_f32_e32 v41, v201, v209
	v_mul_f32_e64 v161, -v201, v213
	v_fma_f32 v41, -v205, v213, v41
	v_fma_f32 v161, -v205, v209, v161
	v_mul_f32_e32 v42, v202, v210
	v_mul_f32_e64 v162, -v202, v214
	v_fma_f32 v42, -v206, v214, v42
	v_fma_f32 v162, -v206, v210, v162
	v_mul_f32_e32 v43, v203, v211
	v_mul_f32_e64 v163, -v203, v215
	v_fma_f32 v43, -v207, v215, v43
	v_fma_f32 v163, -v207, v211, v163
	ds_read_b128 v[200:203], v222 offset:25200
	ds_read_b128 v[204:207], v222 offset:29296
	ds_read2_b32 v[208:209], v225 offset0:192 offset1:208
	ds_read2_b32 v[210:211], v225 offset0:224 offset1:240
	ds_read2_b32 v[212:213], v229 offset0:192 offset1:208
	ds_read2_b32 v[214:215], v229 offset0:224 offset1:240
	s_waitcnt lgkmcnt(0)
	v_mul_f32_e32 v44, v200, v208
	v_mul_f32_e64 v164, -v200, v212
	v_fma_f32 v44, -v204, v212, v44
	v_fma_f32 v164, -v204, v208, v164
	v_mul_f32_e32 v45, v201, v209
	v_mul_f32_e64 v165, -v201, v213
	v_fma_f32 v45, -v205, v213, v45
	v_fma_f32 v165, -v205, v209, v165
	v_mul_f32_e32 v46, v202, v210
	v_mul_f32_e64 v166, -v202, v214
	v_fma_f32 v46, -v206, v214, v46
	v_fma_f32 v166, -v206, v210, v166
	v_mul_f32_e32 v47, v203, v211
	v_mul_f32_e64 v167, -v203, v215
	v_fma_f32 v47, -v207, v215, v47
	v_fma_f32 v167, -v207, v211, v167
	ds_read_b128 v[200:203], v222 offset:25216
	ds_read_b128 v[204:207], v222 offset:29312
	ds_read2_b32 v[208:209], v226 offset0:0 offset1:16
	ds_read2_b32 v[210:211], v226 offset0:32 offset1:48
	ds_read2_b32 v[212:213], v230 offset0:0 offset1:16
	ds_read2_b32 v[214:215], v230 offset0:32 offset1:48
	s_waitcnt lgkmcnt(0)
	v_mul_f32_e32 v48, v200, v208
	v_mul_f32_e64 v168, -v200, v212
	v_fma_f32 v48, -v204, v212, v48
	v_fma_f32 v168, -v204, v208, v168
	v_mul_f32_e32 v49, v201, v209
	v_mul_f32_e64 v169, -v201, v213
	v_fma_f32 v49, -v205, v213, v49
	v_fma_f32 v169, -v205, v209, v169
	v_mul_f32_e32 v50, v202, v210
	v_mul_f32_e64 v170, -v202, v214
	v_fma_f32 v50, -v206, v214, v50
	v_fma_f32 v170, -v206, v210, v170
	v_mul_f32_e32 v51, v203, v211
	v_mul_f32_e64 v171, -v203, v215
	v_fma_f32 v51, -v207, v215, v51
	v_fma_f32 v171, -v207, v211, v171
	ds_read_b128 v[200:203], v222 offset:25232
	ds_read_b128 v[204:207], v222 offset:29328
	ds_read2_b32 v[208:209], v226 offset0:64 offset1:80
	ds_read2_b32 v[210:211], v226 offset0:96 offset1:112
	ds_read2_b32 v[212:213], v230 offset0:64 offset1:80
	ds_read2_b32 v[214:215], v230 offset0:96 offset1:112
	s_waitcnt lgkmcnt(0)
	v_mul_f32_e32 v52, v200, v208
	v_mul_f32_e64 v172, -v200, v212
	v_fma_f32 v52, -v204, v212, v52
	v_fma_f32 v172, -v204, v208, v172
	v_mul_f32_e32 v53, v201, v209
	v_mul_f32_e64 v173, -v201, v213
	v_fma_f32 v53, -v205, v213, v53
	v_fma_f32 v173, -v205, v209, v173
	v_mul_f32_e32 v54, v202, v210
	v_mul_f32_e64 v174, -v202, v214
	v_fma_f32 v54, -v206, v214, v54
	v_fma_f32 v174, -v206, v210, v174
	v_mul_f32_e32 v55, v203, v211
	v_mul_f32_e64 v175, -v203, v215
	v_fma_f32 v55, -v207, v215, v55
	v_fma_f32 v175, -v207, v211, v175
	ds_read_b128 v[200:203], v222 offset:25248
	ds_read_b128 v[204:207], v222 offset:29344
	ds_read2_b32 v[208:209], v226 offset0:128 offset1:144
	ds_read2_b32 v[210:211], v226 offset0:160 offset1:176
	ds_read2_b32 v[212:213], v230 offset0:128 offset1:144
	ds_read2_b32 v[214:215], v230 offset0:160 offset1:176
	s_waitcnt lgkmcnt(0)
	v_mul_f32_e32 v56, v200, v208
	v_mul_f32_e64 v176, -v200, v212
	v_fma_f32 v56, -v204, v212, v56
	v_fma_f32 v176, -v204, v208, v176
	v_mul_f32_e32 v57, v201, v209
	v_mul_f32_e64 v177, -v201, v213
	v_fma_f32 v57, -v205, v213, v57
	v_fma_f32 v177, -v205, v209, v177
	v_mul_f32_e32 v58, v202, v210
	v_mul_f32_e64 v178, -v202, v214
	v_fma_f32 v58, -v206, v214, v58
	v_fma_f32 v178, -v206, v210, v178
	v_mul_f32_e32 v59, v203, v211
	v_mul_f32_e64 v179, -v203, v215
	v_fma_f32 v59, -v207, v215, v59
	v_fma_f32 v179, -v207, v211, v179
	ds_read_b128 v[200:203], v222 offset:25264
	ds_read_b128 v[204:207], v222 offset:29360
	ds_read2_b32 v[208:209], v226 offset0:192 offset1:208
	ds_read2_b32 v[210:211], v226 offset0:224 offset1:240
	ds_read2_b32 v[212:213], v230 offset0:192 offset1:208
	ds_read2_b32 v[214:215], v230 offset0:224 offset1:240
	s_waitcnt lgkmcnt(0)
	v_mul_f32_e32 v60, v200, v208
	v_mul_f32_e64 v180, -v200, v212
	v_fma_f32 v60, -v204, v212, v60
	v_fma_f32 v180, -v204, v208, v180
	v_mul_f32_e32 v61, v201, v209
	v_mul_f32_e64 v181, -v201, v213
	v_fma_f32 v61, -v205, v213, v61
	v_fma_f32 v181, -v205, v209, v181
	v_mul_f32_e32 v62, v202, v210
	v_mul_f32_e64 v182, -v202, v214
	v_fma_f32 v62, -v206, v214, v62
	v_fma_f32 v182, -v206, v210, v182
	v_mul_f32_e32 v63, v203, v211
	v_mul_f32_e64 v183, -v203, v215
	v_fma_f32 v63, -v207, v215, v63
	v_fma_f32 v183, -v207, v211, v183
	ds_read_b128 v[200:203], v222 offset:25280
	ds_read_b128 v[204:207], v222 offset:29376
	ds_read2_b32 v[208:209], v227 offset0:0 offset1:16
	ds_read2_b32 v[210:211], v227 offset0:32 offset1:48
	ds_read2_b32 v[212:213], v231 offset0:0 offset1:16
	ds_read2_b32 v[214:215], v231 offset0:32 offset1:48
	s_waitcnt lgkmcnt(0)
; __device__ __forceinline__ void s5_setup(int g, LAS unsigned char* lds, const float* lam_re, const float* lam_im, const float* log_dt, const float* b_re, const float* b_im,
;                                          const float* c_re, const float* c_im, bf16* BTY, bf16* BTS, float* AP32, int tid) {
;     ...
;     for (int idx = tid; idx < 32 * 256; idx += NTHR) { const int d = idx >> 8, co = (idx >> 4) & 15, ci = idx & 15; float a = 0.f;
;         for (int p = 0; p < 64; ++p) { const float cr = ccr[co * 64 + p], cm = cci[co * 64 + p], ar = apr[d * 64 + p], ai = api[d * 64 + p];
;             const float car = cr * ar - cm * ai, cai = cr * ai + cm * ar; a += car * bbr[p * 16 + ci] - cai * bbi[p * 16 + ci]; }
;         Kd[idx] = a; }
	v_mul_f32_e32 v64, v200, v208
	v_mul_f32_e64 v184, -v200, v212
	v_fma_f32 v64, -v204, v212, v64
	v_fma_f32 v184, -v204, v208, v184
	v_mul_f32_e32 v65, v201, v209
	v_mul_f32_e64 v185, -v201, v213
	v_fma_f32 v65, -v205, v213, v65
	v_fma_f32 v185, -v205, v209, v185
	v_mul_f32_e32 v66, v202, v210
	v_mul_f32_e64 v186, -v202, v214
	v_fma_f32 v66, -v206, v214, v66
	v_fma_f32 v186, -v206, v210, v186
	v_mul_f32_e32 v67, v203, v211
	v_mul_f32_e64 v187, -v203, v215
	v_fma_f32 v67, -v207, v215, v67
	v_fma_f32 v187, -v207, v211, v187
	ds_read_b128 v[200:203], v222 offset:25296
	ds_read_b128 v[204:207], v222 offset:29392
	ds_read2_b32 v[208:209], v227 offset0:64 offset1:80
	ds_read2_b32 v[210:211], v227 offset0:96 offset1:112
	ds_read2_b32 v[212:213], v231 offset0:64 offset1:80
	ds_read2_b32 v[214:215], v231 offset0:96 offset1:112
	s_waitcnt lgkmcnt(0)
	v_mul_f32_e32 v68, v200, v208
	v_mul_f32_e64 v188, -v200, v212
	v_fma_f32 v68, -v204, v212, v68
	v_fma_f32 v188, -v204, v208, v188
	v_mul_f32_e32 v69, v201, v209
	v_mul_f32_e64 v189, -v201, v213
	v_fma_f32 v69, -v205, v213, v69
	v_fma_f32 v189, -v205, v209, v189
	v_mul_f32_e32 v70, v202, v210
	v_mul_f32_e64 v190, -v202, v214
	v_fma_f32 v70, -v206, v214, v70
	v_fma_f32 v190, -v206, v210, v190
	v_mul_f32_e32 v71, v203, v211
	v_mul_f32_e64 v191, -v203, v215
	v_fma_f32 v71, -v207, v215, v71
	v_fma_f32 v191, -v207, v211, v191
	ds_read_b128 v[200:203], v222 offset:25312
	ds_read_b128 v[204:207], v222 offset:29408
	ds_read2_b32 v[208:209], v227 offset0:128 offset1:144
	ds_read2_b32 v[210:211], v227 offset0:160 offset1:176
	ds_read2_b32 v[212:213], v231 offset0:128 offset1:144
	ds_read2_b32 v[214:215], v231 offset0:160 offset1:176
	s_waitcnt lgkmcnt(0)
	v_mul_f32_e32 v72, v200, v208
	v_mul_f32_e64 v192, -v200, v212
	v_fma_f32 v72, -v204, v212, v72
	v_fma_f32 v192, -v204, v208, v192
	v_mul_f32_e32 v73, v201, v209
	v_mul_f32_e64 v193, -v201, v213
	v_fma_f32 v73, -v205, v213, v73
	v_fma_f32 v193, -v205, v209, v193
	v_mul_f32_e32 v74, v202, v210
	v_mul_f32_e64 v194, -v202, v214
	v_fma_f32 v74, -v206, v214, v74
	v_fma_f32 v194, -v206, v210, v194
	v_mul_f32_e32 v75, v203, v211
	v_mul_f32_e64 v195, -v203, v215
	v_fma_f32 v75, -v207, v215, v75
	v_fma_f32 v195, -v207, v211, v195
	ds_read_b128 v[200:203], v222 offset:25328
	ds_read_b128 v[204:207], v222 offset:29424
	ds_read2_b32 v[208:209], v227 offset0:192 offset1:208
	ds_read2_b32 v[210:211], v227 offset0:224 offset1:240
	ds_read2_b32 v[212:213], v231 offset0:192 offset1:208
	ds_read2_b32 v[214:215], v231 offset0:224 offset1:240
	s_waitcnt lgkmcnt(0)
	v_mul_f32_e32 v76, v200, v208
	v_mul_f32_e64 v196, -v200, v212
	v_fma_f32 v76, -v204, v212, v76
	v_fma_f32 v196, -v204, v208, v196
	v_mul_f32_e32 v77, v201, v209
	v_mul_f32_e64 v197, -v201, v213
	v_fma_f32 v77, -v205, v213, v77
	v_fma_f32 v197, -v205, v209, v197
	v_mul_f32_e32 v78, v202, v210
	v_mul_f32_e64 v198, -v202, v214
	v_fma_f32 v78, -v206, v214, v78
	v_fma_f32 v198, -v206, v210, v198
	v_mul_f32_e32 v79, v203, v211
	v_mul_f32_e64 v199, -v203, v215
	v_fma_f32 v79, -v207, v215, v79
	v_fma_f32 v199, -v207, v211, v199
	s_mov_b32 s0, 16
; __device__ __forceinline__ void s5_setup(int g, LAS unsigned char* lds, const float* lam_re, const float* lam_im, const float* log_dt, const float* b_re, const float* b_im,
;                                          const float* c_re, const float* c_im, bf16* BTY, bf16* BTS, float* AP32, int tid) {
;     ...
;     for (int idx = tid; idx < 32 * 256; idx += NTHR) { const int d = idx >> 8, co = (idx >> 4) & 15, ci = idx & 15; float a = 0.f;
;         for (int p = 0; p < 64; ++p) { const float cr = ccr[co * 64 + p], cm = cci[co * 64 + p], ar = apr[d * 64 + p], ai = api[d * 64 + p];
;             const float car = cr * ar - cm * ai, cai = cr * ai + cm * ar; a += car * bbr[p * 16 + ci] - cai * bbi[p * 16 + ci]; }
;         Kd[idx] = a; }
.Lkd_loop:
	ds_read_b128 v[80:83], v220 offset:0
	ds_read_b128 v[84:87], v220 offset:16
	ds_read_b128 v[88:91], v220 offset:32
	ds_read_b128 v[92:95], v220 offset:48
	ds_read_b128 v[96:99], v220 offset:8448
	ds_read_b128 v[100:103], v220 offset:8464
	ds_read_b128 v[104:107], v220 offset:8480
	ds_read_b128 v[108:111], v220 offset:8496
	ds_read_b128 v[0:3], v220 offset:64
	ds_read_b128 v[4:7], v220 offset:80
	ds_read_b128 v[8:11], v220 offset:96
	ds_read_b128 v[12:15], v220 offset:112
	ds_read_b128 v[112:115], v220 offset:8512
	ds_read_b128 v[116:119], v220 offset:8528
	ds_read_b128 v[120:123], v220 offset:8544
	ds_read_b128 v[124:127], v220 offset:8560
	s_waitcnt lgkmcnt(8)
	v_mul_f32_e32 v216, v80, v16
	v_fmac_f32_e32 v216, v96, v136
	v_mul_f32_e32 v217, v81, v17
	v_fmac_f32_e32 v217, v97, v137
	v_mul_f32_e32 v218, v82, v18
	v_fmac_f32_e32 v218, v98, v138
	v_mul_f32_e32 v219, v83, v19
	v_fmac_f32_e32 v219, v99, v139
	v_fmac_f32_e32 v216, v84, v20
	v_fmac_f32_e32 v216, v100, v140
	v_fmac_f32_e32 v217, v85, v21
	v_fmac_f32_e32 v217, v101, v141
	v_fmac_f32_e32 v218, v86, v22
	v_fmac_f32_e32 v218, v102, v142
	v_fmac_f32_e32 v219, v87, v23
	v_fmac_f32_e32 v219, v103, v143
	v_fmac_f32_e32 v216, v88, v24
	v_fmac_f32_e32 v216, v104, v144
	v_fmac_f32_e32 v217, v89, v25
	v_fmac_f32_e32 v217, v105, v145
	v_fmac_f32_e32 v218, v90, v26
	v_fmac_f32_e32 v218, v106, v146
	v_fmac_f32_e32 v219, v91, v27
	v_fmac_f32_e32 v219, v107, v147
	v_fmac_f32_e32 v216, v92, v28
	v_fmac_f32_e32 v216, v108, v148
	v_fmac_f32_e32 v217, v93, v29
	v_fmac_f32_e32 v217, v109, v149
	v_fmac_f32_e32 v218, v94, v30
	v_fmac_f32_e32 v218, v110, v150
	v_fmac_f32_e32 v219, v95, v31
	v_fmac_f32_e32 v219, v111, v151
	ds_read_b128 v[80:83], v220 offset:128
	ds_read_b128 v[84:87], v220 offset:144
	ds_read_b128 v[88:91], v220 offset:160
	ds_read_b128 v[92:95], v220 offset:176
	ds_read_b128 v[96:99], v220 offset:8576
	ds_read_b128 v[100:103], v220 offset:8592
	ds_read_b128 v[104:107], v220 offset:8608
	ds_read_b128 v[108:111], v220 offset:8624
	s_waitcnt lgkmcnt(8)
	v_fmac_f32_e32 v216, v0, v32
	v_fmac_f32_e32 v216, v112, v152
	v_fmac_f32_e32 v217, v1, v33
	v_fmac_f32_e32 v217, v113, v153
	v_fmac_f32_e32 v218, v2, v34
	v_fmac_f32_e32 v218, v114, v154
	v_fmac_f32_e32 v219, v3, v35
	v_fmac_f32_e32 v219, v115, v155
	v_fmac_f32_e32 v216, v4, v36
	v_fmac_f32_e32 v216, v116, v156
	v_fmac_f32_e32 v217, v5, v37
	v_fmac_f32_e32 v217, v117, v157
	v_fmac_f32_e32 v218, v6, v38
	v_fmac_f32_e32 v218, v118, v158
	v_fmac_f32_e32 v219, v7, v39
	v_fmac_f32_e32 v219, v119, v159
	v_fmac_f32_e32 v216, v8, v40
	v_fmac_f32_e32 v216, v120, v160
	v_fmac_f32_e32 v217, v9, v41
	v_fmac_f32_e32 v217, v121, v161
	v_fmac_f32_e32 v218, v10, v42
	v_fmac_f32_e32 v218, v122, v162
	v_fmac_f32_e32 v219, v11, v43
	v_fmac_f32_e32 v219, v123, v163
	v_fmac_f32_e32 v216, v12, v44
	v_fmac_f32_e32 v216, v124, v164
	v_fmac_f32_e32 v217, v13, v45
	v_fmac_f32_e32 v217, v125, v165
	v_fmac_f32_e32 v218, v14, v46
	v_fmac_f32_e32 v218, v126, v166
	v_fmac_f32_e32 v219, v15, v47
	v_fmac_f32_e32 v219, v127, v167
	ds_read_b128 v[0:3], v220 offset:192
	ds_read_b128 v[4:7], v220 offset:208
	ds_read_b128 v[8:11], v220 offset:224
	ds_read_b128 v[12:15], v220 offset:240
	ds_read_b128 v[112:115], v220 offset:8640
	ds_read_b128 v[116:119], v220 offset:8656
	ds_read_b128 v[120:123], v220 offset:8672
	ds_read_b128 v[124:127], v220 offset:8688
	s_waitcnt lgkmcnt(8)
	v_fmac_f32_e32 v216, v80, v48
	v_fmac_f32_e32 v216, v96, v168
	v_fmac_f32_e32 v217, v81, v49
	v_fmac_f32_e32 v217, v97, v169
	v_fmac_f32_e32 v218, v82, v50
	v_fmac_f32_e32 v218, v98, v170
	v_fmac_f32_e32 v219, v83, v51
	v_fmac_f32_e32 v219, v99, v171
	v_fmac_f32_e32 v216, v84, v52
	v_fmac_f32_e32 v216, v100, v172
	v_fmac_f32_e32 v217, v85, v53
	v_fmac_f32_e32 v217, v101, v173
	v_fmac_f32_e32 v218, v86, v54
	v_fmac_f32_e32 v218, v102, v174
	v_fmac_f32_e32 v219, v87, v55
	v_fmac_f32_e32 v219, v103, v175
	v_fmac_f32_e32 v216, v88, v56
	v_fmac_f32_e32 v216, v104, v176
	v_fmac_f32_e32 v217, v89, v57
	v_fmac_f32_e32 v217, v105, v177
	v_fmac_f32_e32 v218, v90, v58
	v_fmac_f32_e32 v218, v106, v178
	v_fmac_f32_e32 v219, v91, v59
	v_fmac_f32_e32 v219, v107, v179
	v_fmac_f32_e32 v216, v92, v60
	v_fmac_f32_e32 v216, v108, v180
	v_fmac_f32_e32 v217, v93, v61
	v_fmac_f32_e32 v217, v109, v181
	v_fmac_f32_e32 v218, v94, v62
	v_fmac_f32_e32 v218, v110, v182
	v_fmac_f32_e32 v219, v95, v63
	v_fmac_f32_e32 v219, v111, v183
	s_waitcnt lgkmcnt(0)
	v_fmac_f32_e32 v216, v0, v64
	v_fmac_f32_e32 v216, v112, v184
	v_fmac_f32_e32 v217, v1, v65
	v_fmac_f32_e32 v217, v113, v185
	v_fmac_f32_e32 v218, v2, v66
	v_fmac_f32_e32 v218, v114, v186
	v_fmac_f32_e32 v219, v3, v67
	v_fmac_f32_e32 v219, v115, v187
	v_fmac_f32_e32 v216, v4, v68
	v_fmac_f32_e32 v216, v116, v188
	v_fmac_f32_e32 v217, v5, v69
	v_fmac_f32_e32 v217, v117, v189
	v_fmac_f32_e32 v218, v6, v70
	v_fmac_f32_e32 v218, v118, v190
	v_fmac_f32_e32 v219, v7, v71
	v_fmac_f32_e32 v219, v119, v191
	v_fmac_f32_e32 v216, v8, v72
	v_fmac_f32_e32 v216, v120, v192
	v_fmac_f32_e32 v217, v9, v73
	v_fmac_f32_e32 v217, v121, v193
	v_fmac_f32_e32 v218, v10, v74
	v_fmac_f32_e32 v218, v122, v194
	v_fmac_f32_e32 v219, v11, v75
	v_fmac_f32_e32 v219, v123, v195
	v_fmac_f32_e32 v216, v12, v76
	v_fmac_f32_e32 v216, v124, v196
	v_fmac_f32_e32 v217, v13, v77
	v_fmac_f32_e32 v217, v125, v197
	v_fmac_f32_e32 v218, v14, v78
	v_fmac_f32_e32 v218, v126, v198
	v_fmac_f32_e32 v219, v15, v79
	v_fmac_f32_e32 v219, v127, v199
	v_add_f32_e32 v216, v216, v217
	v_add_f32_e32 v218, v218, v219
	v_add_u32_e32 v220, 0x200, v220
	v_add_f32_e32 v216, v216, v218
	s_add_i32 s0, s0, -1
	ds_write_b32 v221, v216 offset:33280
	v_add_u32_e32 v221, 0x800, v221
	s_cmp_lg_u32 s0, 0
	s_cbranch_scc1 .Lkd_loop

;     __device__ __forceinline__ bool next(int i, Unit& u) const { const int L = i * G + c; if (L >= NB * nN) return false; u.z = L / nN; u.pn = L % nN; u.pm = i; return true; }
; __global__ void __launch_bounds__(NTHR, 2) fwd(Args args) {
;     ...
; #pragma unroll
;           for (int k = 0; k < MAXU / 2; ++k) tokTab[(2 * k + (tid >> 8)) * 256 + (tid & 255)] = tokv[k]; }
;         __syncthreads();
.LBB0_1511:
	s_or_b64 exec, exec, s[4:5]
	v_and_b32_e32 v7, 0x3fffff00, v2
	v_mov_b32_e32 v8, 2
	s_add_i32 s4, 0, 0x20400
	v_lshlrev_b32_e32 v7, 2, v7
	v_lshlrev_b32_sdwa v2, v8, v2 dst_sel:DWORD dst_unused:UNUSED_PAD src0_sel:DWORD src1_sel:BYTE_0
	v_add3_u32 v2, s4, v7, v2
	s_waitcnt vmcnt(0)
	ds_write2st64_b32 v2, v1, v0 offset1:8
	ds_write2st64_b32 v2, v4, v3 offset0:16 offset1:24
	ds_write_b32 v2, v6 offset:8192
	s_waitcnt lgkmcnt(0)
	s_barrier
	s_cmp_lt_i32 s92, s68
	v_mbcnt_lo_u32_b32 v0, -1, v5
	v_mbcnt_hi_u32_b32 v0, -1, v0
	v_add_u32_e32 v4, s94, v0
	s_cselect_b64 s[0:1], -1, 0
	s_cmp_ge_i32 s92, s68
	v_readfirstlane_b32 s2, v4
	s_cbranch_scc1 .LBB0_1514
	s_ashr_i32 s5, s92, 31
	s_lshr_b32 s5, s5, 28
	s_add_i32 s5, s92, s5
	s_ashr_i32 s38, s5, 4
	s_and_b32 s40, s92, 7
	s_lshl_b32 s40, s40, 1
	s_bfe_u32 s5, s92, 0x10003
	s_or_b32 s40, s40, s5
	s_andn2_b64 vcc, exec, s[0:1]
	s_cbranch_vccz .LBB0_1515

; template <class Epi, class Sched, bool ALIGN_EPI = false, bool SP2 = false>
; __device__ __forceinline__ void gemm_phase(PG8_LAS unsigned char* lds, const Geo geo, const Sched& S, const Epi& E, const int wave_) {
;     ...
;         const bool has_next = S.next(ui + 1, nxt);
;     __device__ __forceinline__ bool next(int i, Unit& u) const { const int L = i * G + c; if (L >= NB * nN) return false; u.z = L / nN; u.pn = L % nN; u.pm = i; return true; }
.LBB0_1520:
	s_add_i32 s26, s26, 1
	s_mul_i32 s0, s26, s83
	s_add_i32 s0, s0, s92
	s_cmp_lt_i32 s0, s68
	s_cselect_b64 s[42:43], -1, 0
	s_cmp_ge_i32 s0, s68
	s_cbranch_scc1 .LBB0_1522
	s_ashr_i32 s1, s0, 31
	s_lshr_b32 s1, s1, 28
	s_add_i32 s1, s0, s1
	s_ashr_i32 s27, s1, 4
	s_and_b32 s34, s0, 7
	s_lshl_b32 s34, s34, 1
	s_bfe_u32 s1, s0, 0x10003
	s_or_b32 s34, s34, s1
	s_mov_b32 s33, s26

;     __device__ __forceinline__ void operator()(const f32x4 (&acc)[2][2][4][2], const Unit& u, int wr, int wc, int fr, int fq) const {
;         asm volatile("" : "+v"(fr), "+v"(fq));
;         const int e = blkE[u.z], c0 = u.pn * 128 + wc * 32 + 8 * fq, row0 = wr * 64 + fr;
;         const float* bg = bup + (size_t)e * 2 * FF + c0; const f32x4 g0 = *(const f32x4*)bg, g1 = *(const f32x4*)(bg + 4), l0 = *(const f32x4*)(bg + FF), l1 = *(const f32x4*)(bg + FF + 4);
;         float rsb[8];
; #pragma unroll
;         for (int q = 0; q < 8; ++q) rsb[q] = ssq[tokTab[u.pm * 256 + row0 + (q >> 2) * 128 + (q & 3) * 16]] * W8_INV;
; #pragma unroll
;         for (int ai = 0; ai < 2; ++ai)
; #pragma unroll
;             for (int m = 0; m < 4; ++m) { const int r = row0 + ai * 128 + m * 16; const float rs = rsb[ai * 4 + m];
;                 float a[8];
; #pragma unroll
;                 for (int j = 0; j < 8; ++j) { const float gb = j < 4 ? g0[j & 3] : g1[j & 3], lb = j < 4 ? l0[j & 3] : l1[j & 3];
;                     const float gl = fminf(acc[ai][0][m][j >> 2][j & 3] * rs + gb, 7.0f), ln = fminf(fmaxf(acc[ai][1][m][j >> 2][j & 3] * rs + lb, -7.0f), 7.0f);
;                     a[j] = gl * __builtin_amdgcn_rcpf(1.0f + __builtin_amdgcn_exp2f(-1.702f * 1.4426950408889634f * gl)) * (ln + 1.0f); }
;                 v2u w; w.x = pk4_fp8(a[0], a[1], a[2], a[3]); w.y = pk4_fp8(a[4], a[5], a[6], a[7]);
;                 *(v2u*)(ACT + ((size_t)u.z * 256 + r) * FF + c0) = w; }
.LBB0_1534:
	s_lshl_b32 s4, s40, 7
	v_mov_b32_e32 v2, v218
	v_mov_b32_e32 v3, v219
	s_or_b32 s4, s4, s89
	v_mov_b32_e32 v0, s35
	v_lshl_add_u32 v16, v3, 3, s4
	v_readlane_b32 s0, v254, 2
	v_readlane_b32 s4, v254, 6
	s_lshl_b32 s4, s65, 10
	v_add_u32_e32 v18, s88, v2
	s_add_i32 s4, s4, 0
	v_lshl_add_u32 v2, v18, 2, s4
	v_add_u32_e32 v9, 0x20400, v2
	ds_read2_b32 v[4:5], v9 offset1:16
	ds_read_b32 v0, v0
	v_readlane_b32 s1, v254, 3
	v_ashrrev_i32_e32 v17, 31, v16
	ds_read2_b32 v[20:21], v9 offset0:160 offset1:176
	s_waitcnt lgkmcnt(0)
	v_ashrrev_i32_e32 v11, 31, v4
	v_mov_b32_e32 v10, v4
	v_lshl_add_u64 v[10:11], v[10:11], 2, s[14:15]
	global_load_dword v19, v[10:11], off
	ds_read2_b32 v[10:11], v9 offset0:32 offset1:48
	v_ashrrev_i32_e32 v13, 31, v5
	v_mov_b32_e32 v12, v5
	v_lshl_add_u64 v[4:5], v[12:13], 2, s[14:15]
	global_load_dword v24, v[4:5], off
	s_waitcnt lgkmcnt(0)
	v_ashrrev_i32_e32 v5, 31, v10
	v_mov_b32_e32 v4, v10
	v_lshl_add_u64 v[4:5], v[4:5], 2, s[14:15]
	global_load_dword v25, v[4:5], off
	ds_read2_b32 v[4:5], v9 offset0:128 offset1:144
	v_ashrrev_i32_e32 v13, 31, v11
	v_mov_b32_e32 v12, v11
	v_lshl_add_u64 v[10:11], v[12:13], 2, s[14:15]
	v_ashrrev_i32_e32 v1, 31, v0
	global_load_dword v26, v[10:11], off
	s_waitcnt lgkmcnt(0)
	v_ashrrev_i32_e32 v11, 31, v4
	v_mov_b32_e32 v10, v4
	v_lshlrev_b64 v[0:1], 14, v[0:1]
	v_lshl_add_u64 v[10:11], v[10:11], 2, s[14:15]
	v_lshl_add_u64 v[0:1], s[0:1], 0, v[0:1]
	global_load_dword v27, v[10:11], off
	v_ashrrev_i32_e32 v11, 31, v5
	v_mov_b32_e32 v10, v5
	v_lshl_add_u64 v[6:7], v[16:17], 2, v[0:1]
	v_lshl_add_u64 v[4:5], v[10:11], 2, s[14:15]
	global_load_dwordx4 v[0:3], v[6:7], off
	global_load_dword v28, v[4:5], off
	v_ashrrev_i32_e32 v5, 31, v20
	v_mov_b32_e32 v4, v20
	v_add_co_u32_e32 v8, vcc, s56, v6
	v_lshl_add_u64 v[4:5], v[4:5], 2, s[14:15]
	global_load_dword v29, v[4:5], off
	v_addc_co_u32_e32 v9, vcc, 0, v7, vcc
	global_load_dwordx4 v[8:11], v[8:9], off
	s_nop 0
	global_load_dwordx4 v[12:15], v[6:7], off offset:16
	v_readlane_b32 s5, v254, 7
	s_mov_b64 s[4:5], 0x2000
	v_ashrrev_i32_e32 v23, 31, v21
	v_lshl_add_u64 v[4:5], v[6:7], 0, s[4:5]
	global_load_dwordx4 v[4:7], v[4:5], off offset:16
	v_mov_b32_e32 v22, v21
	v_lshl_add_u64 v[20:21], v[22:23], 2, s[14:15]
	global_load_dword v20, v[20:21], off
	s_ashr_i32 s39, s38, 31
	s_lshl_b64 s[4:5], s[38:39], 19
	s_add_u32 s4, s93, s4
	s_addc_u32 s5, s87, s5
	v_readlane_b32 s0, v254, 10
	s_cmp_lg_u32 s65, s0
	v_readlane_b32 s2, v254, 4
	v_readlane_b32 s3, v254, 5
	v_readlane_b32 s6, v254, 8
	v_readlane_b32 s7, v254, 9
	s_waitcnt vmcnt(0)
	v_mul_f32_e32 v19, 0x3b800000, v19
	v_mul_f32_e32 v30, 0x3b800000, v24
	v_mul_f32_e32 v25, 0x3b800000, v25
	v_mul_f32_e32 v24, 0x3b800000, v26
	v_mul_f32_e32 v23, 0x3b800000, v27
	v_fma_f32 v26, v192, v19, v0
	v_mul_f32_e32 v22, 0x3b800000, v28
	v_fma_f32 v28, v193, v19, v1
	v_min_f32_e32 v26, 0x40e00000, v26
	v_min_f32_e32 v28, 0x40e00000, v28
	v_fma_f32 v31, v194, v19, v2
	v_mul_f32_e32 v34, 0xc01d265f, v26
	v_mul_f32_e32 v35, 0xc01d265f, v28
	v_min_f32_e32 v31, 0x40e00000, v31
	v_exp_f32_e32 v34, v34
	v_exp_f32_e32 v35, v35
	v_mul_f32_e32 v36, 0xc01d265f, v31
	v_fma_f32 v33, v195, v19, v3
	v_exp_f32_e32 v36, v36
	v_min_f32_e32 v33, 0x40e00000, v33
	v_mul_f32_e32 v37, 0xc01d265f, v33
	v_add_f32_e32 v34, 1.0, v34
	v_add_f32_e32 v35, 1.0, v35
	v_exp_f32_e32 v37, v37
	v_rcp_f32_e32 v34, v34
	v_rcp_f32_e32 v35, v35
	v_add_f32_e32 v36, 1.0, v36
	v_mul_f32_e32 v21, 0x3b800000, v29
	v_fma_f32 v27, v188, v19, v8
	v_fma_f32 v29, v189, v19, v9
	v_rcp_f32_e32 v36, v36
	v_med3_f32 v27, v27, s23, v236
	v_med3_f32 v29, v29, s23, v236
	v_fma_f32 v32, v190, v19, v10
	v_add_f32_e32 v27, 1.0, v27
	v_add_f32_e32 v29, 1.0, v29
	v_add_f32_e32 v37, 1.0, v37
	v_mul_f32_e32 v26, v26, v34
	v_mul_f32_e32 v28, v28, v35
	v_med3_f32 v32, v32, s23, v236
	v_mul_f32_e32 v26, v27, v26
	v_mul_f32_e32 v27, v29, v28
	v_rcp_f32_e32 v28, v37
	v_add_f32_e32 v32, 1.0, v32
	v_mul_f32_e32 v31, v31, v36
	v_mul_f32_e32 v29, v32, v31
	v_fma_f32 v32, v184, v19, v12
	v_min_f32_e32 v32, 0x40e00000, v32
	v_mul_f32_e32 v28, v33, v28
	v_mul_f32_e32 v33, 0xc01d265f, v32
	v_exp_f32_e32 v33, v33
	v_fma_f32 v34, v185, v19, v13
	v_min_f32_e32 v34, 0x40e00000, v34
	v_mul_f32_e32 v35, 0xc01d265f, v34
	v_add_f32_e32 v33, 1.0, v33
	v_rcp_f32_e32 v33, v33
	v_exp_f32_e32 v35, v35
	v_fma_f32 v31, v191, v19, v11
	v_fma_f32 v36, v187, v19, v15
	v_mul_f32_e32 v32, v32, v33
	v_add_f32_e32 v33, 1.0, v35
	v_rcp_f32_e32 v33, v33
	v_med3_f32 v31, v31, s23, v236
	v_min_f32_e32 v36, 0x40e00000, v36
	v_add_f32_e32 v31, 1.0, v31
	v_mul_f32_e32 v33, v34, v33
	v_fma_f32 v34, v186, v19, v14
	v_min_f32_e32 v34, 0x40e00000, v34
	v_mul_f32_e32 v35, 0xc01d265f, v34
	v_exp_f32_e32 v35, v35
	v_mul_f32_e32 v37, 0xc01d265f, v36
	v_mul_f32_e32 v28, v31, v28
	v_fma_f32 v31, v180, v19, v4
	v_add_f32_e32 v35, 1.0, v35
	v_rcp_f32_e32 v35, v35
	v_exp_f32_e32 v37, v37
	v_med3_f32 v31, v31, s23, v236
	v_add_f32_e32 v31, 1.0, v31
	v_mul_f32_e32 v31, v31, v32
	v_fma_f32 v32, v181, v19, v5
	v_med3_f32 v32, v32, s23, v236
	v_mul_f32_e32 v34, v34, v35
	v_add_f32_e32 v35, 1.0, v37
	v_add_f32_e32 v32, 1.0, v32
	v_rcp_f32_e32 v35, v35
	v_mul_f32_e32 v32, v32, v33
	v_fma_f32 v33, v182, v19, v6
	v_med3_f32 v33, v33, s23, v236
	v_fma_f32 v19, v183, v19, v7
	v_add_f32_e32 v33, 1.0, v33
	v_med3_f32 v19, v19, s23, v236
	v_mul_f32_e32 v33, v33, v34
	v_mul_f32_e32 v34, v36, v35
	v_add_f32_e32 v19, 1.0, v19
	v_mul_f32_e32 v19, v19, v34
	v_med3_f32 v34, v26, s24, v237
	v_med3_f32 v27, v27, s24, v237
	v_mov_b32_e32 v26, v65
	v_cvt_pk_fp8_f32 v26, v34, v27
	v_med3_f32 v31, v31, s24, v237
	v_med3_f32 v32, v32, s24, v237
;     __device__ __forceinline__ void operator()(const f32x4 (&acc)[2][2][4][2], const Unit& u, int wr, int wc, int fr, int fq) const {
;     ...
;         for (int ai = 0; ai < 2; ++ai)
; #pragma unroll
;             for (int m = 0; m < 4; ++m) { const int r = row0 + ai * 128 + m * 16; const float rs = rsb[ai * 4 + m];
;                 float a[8];
; #pragma unroll
;                 for (int j = 0; j < 8; ++j) { const float gb = j < 4 ? g0[j & 3] : g1[j & 3], lb = j < 4 ? l0[j & 3] : l1[j & 3];
;                     const float gl = fminf(acc[ai][0][m][j >> 2][j & 3] * rs + gb, 7.0f), ln = fminf(fmaxf(acc[ai][1][m][j >> 2][j & 3] * rs + lb, -7.0f), 7.0f);
;                     a[j] = gl * __builtin_amdgcn_rcpf(1.0f + __builtin_amdgcn_exp2f(-1.702f * 1.4426950408889634f * gl)) * (ln + 1.0f); }
;                 v2u w; w.x = pk4_fp8(a[0], a[1], a[2], a[3]); w.y = pk4_fp8(a[4], a[5], a[6], a[7]);
;                 *(v2u*)(ACT + ((size_t)u.z * 256 + r) * FF + c0) = w; }
	v_mov_b32_e32 v27, v65
	v_cvt_pk_fp8_f32 v27, v31, v32
	v_med3_f32 v29, v29, s24, v237
	v_med3_f32 v28, v28, s24, v237
	v_cvt_pk_fp8_f32 v26, v29, v28 op_sel:[0,0,1]
	v_med3_f32 v28, v33, s24, v237
	v_med3_f32 v19, v19, s24, v237
	v_cvt_pk_fp8_f32 v27, v28, v19 op_sel:[0,0,1]
	v_ashrrev_i32_e32 v19, 31, v18
	v_lshlrev_b64 v[18:19], 11, v[18:19]
	v_lshl_add_u64 v[18:19], s[4:5], 0, v[18:19]
	v_lshl_add_u64 v[16:17], v[18:19], 0, v[16:17]
	global_store_dwordx2 v[16:17], v[26:27], off
	v_fma_f32 v26, v177, v30, v1
	v_min_f32_e32 v26, 0x40e00000, v26
	v_fma_f32 v28, v176, v30, v0
	v_mul_f32_e32 v27, 0xc01d265f, v26
	v_min_f32_e32 v28, 0x40e00000, v28
	v_exp_f32_e32 v27, v27
	v_mul_f32_e32 v29, 0xc01d265f, v28
	v_exp_f32_e32 v29, v29
	v_fma_f32 v32, v169, v30, v13
	v_add_f32_e32 v27, 1.0, v27
	v_rcp_f32_e32 v27, v27
	v_add_f32_e32 v19, 1.0, v29
	v_rcp_f32_e32 v19, v19
	v_fma_f32 v29, v179, v30, v3
	v_mul_f32_e32 v26, v26, v27
	v_fma_f32 v27, v178, v30, v2
	v_min_f32_e32 v27, 0x40e00000, v27
	v_mul_f32_e32 v19, v28, v19
	v_mul_f32_e32 v28, 0xc01d265f, v27
	v_exp_f32_e32 v28, v28
	v_min_f32_e32 v29, 0x40e00000, v29
	v_mul_f32_e32 v31, 0xc01d265f, v29
	v_exp_f32_e32 v31, v31
	v_add_f32_e32 v28, 1.0, v28
	v_rcp_f32_e32 v28, v28
	v_min_f32_e32 v32, 0x40e00000, v32
	v_mul_f32_e32 v33, 0xc01d265f, v32
	v_exp_f32_e32 v33, v33
	v_mul_f32_e32 v27, v27, v28
	v_add_f32_e32 v28, 1.0, v31
	v_rcp_f32_e32 v28, v28
	v_fma_f32 v18, v172, v30, v8
	v_med3_f32 v18, v18, s23, v236
	v_add_f32_e32 v18, 1.0, v18
	v_mul_f32_e32 v28, v29, v28
	v_fma_f32 v29, v168, v30, v12
	v_min_f32_e32 v29, 0x40e00000, v29
	v_mul_f32_e32 v31, 0xc01d265f, v29
	v_exp_f32_e32 v31, v31
	v_mul_f32_e32 v18, v18, v19
	v_fma_f32 v19, v173, v30, v9
	v_med3_f32 v19, v19, s23, v236
	v_add_f32_e32 v31, 1.0, v31
	v_rcp_f32_e32 v31, v31
	v_add_f32_e32 v19, 1.0, v19
	v_mul_f32_e32 v19, v19, v26
	v_fma_f32 v26, v174, v30, v10
	v_mul_f32_e32 v29, v29, v31
	v_add_f32_e32 v31, 1.0, v33
	v_rcp_f32_e32 v31, v31
	v_med3_f32 v26, v26, s23, v236
	v_add_f32_e32 v26, 1.0, v26
	v_mul_f32_e32 v26, v26, v27
	v_mul_f32_e32 v31, v32, v31
	v_fma_f32 v32, v170, v30, v14
	v_min_f32_e32 v32, 0x40e00000, v32
	v_mul_f32_e32 v33, 0xc01d265f, v32
	v_exp_f32_e32 v33, v33
	v_fma_f32 v27, v175, v30, v11
	v_fma_f32 v34, v171, v30, v15
	v_med3_f32 v27, v27, s23, v236
	v_min_f32_e32 v34, 0x40e00000, v34
	v_add_f32_e32 v27, 1.0, v27
	v_add_f32_e32 v33, 1.0, v33
	v_mul_f32_e32 v35, 0xc01d265f, v34
	v_mul_f32_e32 v27, v27, v28
	v_fma_f32 v28, v164, v30, v4
	v_rcp_f32_e32 v33, v33
	v_exp_f32_e32 v35, v35
	v_med3_f32 v28, v28, s23, v236
	v_add_f32_e32 v28, 1.0, v28
	v_mul_f32_e32 v28, v28, v29
	v_fma_f32 v29, v165, v30, v5
	v_med3_f32 v29, v29, s23, v236
	v_mul_f32_e32 v32, v32, v33
	v_add_f32_e32 v33, 1.0, v35
	v_add_f32_e32 v29, 1.0, v29
	v_rcp_f32_e32 v33, v33
	v_mul_f32_e32 v29, v29, v31
	v_fma_f32 v31, v166, v30, v6
	v_med3_f32 v31, v31, s23, v236
	v_fma_f32 v30, v167, v30, v7
	v_add_f32_e32 v31, 1.0, v31
	v_med3_f32 v30, v30, s23, v236
	v_mul_f32_e32 v31, v31, v32
	v_mul_f32_e32 v32, v34, v33
	v_add_f32_e32 v30, 1.0, v30
	v_mul_f32_e32 v30, v30, v32
	v_med3_f32 v32, v18, s24, v237
	v_med3_f32 v19, v19, s24, v237
	v_mov_b32_e32 v18, v65
	v_cvt_pk_fp8_f32 v18, v32, v19
	v_med3_f32 v28, v28, s24, v237
	v_med3_f32 v29, v29, s24, v237
	v_mov_b32_e32 v19, v65
	v_cvt_pk_fp8_f32 v19, v28, v29
	v_med3_f32 v26, v26, s24, v237
	v_med3_f32 v27, v27, s24, v237
	v_cvt_pk_fp8_f32 v18, v26, v27 op_sel:[0,0,1]
	v_med3_f32 v26, v31, s24, v237
	v_med3_f32 v27, v30, s24, v237
	v_cvt_pk_fp8_f32 v19, v26, v27 op_sel:[0,0,1]
	v_fma_f32 v27, v160, v25, v0
	v_min_f32_e32 v28, 0x40e00000, v27
	v_add_co_u32_e32 v26, vcc, s73, v16
	v_mul_f32_e32 v27, 0xc01d265f, v28
	v_exp_f32_e32 v29, v27
	v_addc_co_u32_e32 v27, vcc, 0, v17, vcc
	global_store_dwordx2 v[26:27], v[18:19], off
	v_fma_f32 v26, v161, v25, v1
	v_min_f32_e32 v26, 0x40e00000, v26
	v_mul_f32_e32 v27, 0xc01d265f, v26
	v_exp_f32_e32 v27, v27
	v_add_f32_e32 v19, 1.0, v29
	v_rcp_f32_e32 v19, v19
	v_fma_f32 v29, v163, v25, v3
	v_add_f32_e32 v27, 1.0, v27
	v_rcp_f32_e32 v27, v27
	v_mul_f32_e32 v19, v28, v19
	v_min_f32_e32 v29, 0x40e00000, v29
	v_mul_f32_e32 v30, 0xc01d265f, v29
	v_mul_f32_e32 v26, v26, v27
	v_fma_f32 v27, v162, v25, v2
	v_min_f32_e32 v27, 0x40e00000, v27
	v_mul_f32_e32 v28, 0xc01d265f, v27
	v_exp_f32_e32 v28, v28
	v_exp_f32_e32 v30, v30
	v_fma_f32 v31, v153, v25, v13
	v_min_f32_e32 v31, 0x40e00000, v31
	v_add_f32_e32 v28, 1.0, v28
	v_rcp_f32_e32 v28, v28
	v_mul_f32_e32 v32, 0xc01d265f, v31
	v_exp_f32_e32 v32, v32
	v_fma_f32 v18, v156, v25, v8
	v_mul_f32_e32 v27, v27, v28
	v_add_f32_e32 v28, 1.0, v30
	v_rcp_f32_e32 v28, v28
	v_med3_f32 v18, v18, s23, v236
	v_add_f32_e32 v18, 1.0, v18
	v_mul_f32_e32 v18, v18, v19
	v_mul_f32_e32 v28, v29, v28
	v_fma_f32 v29, v152, v25, v12
	v_min_f32_e32 v29, 0x40e00000, v29
	v_mul_f32_e32 v30, 0xc01d265f, v29
	v_exp_f32_e32 v30, v30
	v_fma_f32 v19, v157, v25, v9
	v_med3_f32 v19, v19, s23, v236
	v_add_f32_e32 v19, 1.0, v19
	v_add_f32_e32 v30, 1.0, v30
	v_rcp_f32_e32 v30, v30
	v_mul_f32_e32 v19, v19, v26
	v_fma_f32 v26, v158, v25, v10
	v_med3_f32 v26, v26, s23, v236
	v_mul_f32_e32 v29, v29, v30
	v_add_f32_e32 v30, 1.0, v32
	v_rcp_f32_e32 v30, v30
	v_add_f32_e32 v26, 1.0, v26
	v_mul_f32_e32 v26, v26, v27
	v_fma_f32 v27, v159, v25, v11
	v_mul_f32_e32 v30, v31, v30
	v_fma_f32 v31, v154, v25, v14
	v_min_f32_e32 v31, 0x40e00000, v31
	v_mul_f32_e32 v32, 0xc01d265f, v31
	v_exp_f32_e32 v32, v32
	v_fma_f32 v33, v155, v25, v15
	v_med3_f32 v27, v27, s23, v236
	v_min_f32_e32 v33, 0x40e00000, v33
	v_add_f32_e32 v27, 1.0, v27
	v_add_f32_e32 v32, 1.0, v32
;     __device__ __forceinline__ void operator()(const f32x4 (&acc)[2][2][4][2], const Unit& u, int wr, int wc, int fr, int fq) const {
;     ...
;         for (int ai = 0; ai < 2; ++ai)
; #pragma unroll
;             for (int m = 0; m < 4; ++m) { const int r = row0 + ai * 128 + m * 16; const float rs = rsb[ai * 4 + m];
;                 float a[8];
; #pragma unroll
;                 for (int j = 0; j < 8; ++j) { const float gb = j < 4 ? g0[j & 3] : g1[j & 3], lb = j < 4 ? l0[j & 3] : l1[j & 3];
;                     const float gl = fminf(acc[ai][0][m][j >> 2][j & 3] * rs + gb, 7.0f), ln = fminf(fmaxf(acc[ai][1][m][j >> 2][j & 3] * rs + lb, -7.0f), 7.0f);
;                     a[j] = gl * __builtin_amdgcn_rcpf(1.0f + __builtin_amdgcn_exp2f(-1.702f * 1.4426950408889634f * gl)) * (ln + 1.0f); }
;                 v2u w; w.x = pk4_fp8(a[0], a[1], a[2], a[3]); w.y = pk4_fp8(a[4], a[5], a[6], a[7]);
;                 *(v2u*)(ACT + ((size_t)u.z * 256 + r) * FF + c0) = w; }
	v_mul_f32_e32 v34, 0xc01d265f, v33
	v_mul_f32_e32 v27, v27, v28
	v_fma_f32 v28, v148, v25, v4
	v_rcp_f32_e32 v32, v32
	v_exp_f32_e32 v34, v34
	v_med3_f32 v28, v28, s23, v236
	v_add_f32_e32 v28, 1.0, v28
	v_mul_f32_e32 v28, v28, v29
	v_fma_f32 v29, v149, v25, v5
	v_med3_f32 v29, v29, s23, v236
	v_mul_f32_e32 v31, v31, v32
	v_add_f32_e32 v32, 1.0, v34
	v_add_f32_e32 v29, 1.0, v29
	v_rcp_f32_e32 v32, v32
	v_mul_f32_e32 v29, v29, v30
	v_fma_f32 v30, v150, v25, v6
	v_med3_f32 v30, v30, s23, v236
	v_fma_f32 v25, v151, v25, v7
	v_add_f32_e32 v30, 1.0, v30
	v_med3_f32 v25, v25, s23, v236
	v_mul_f32_e32 v30, v30, v31
	v_mul_f32_e32 v31, v33, v32
	v_add_f32_e32 v25, 1.0, v25
	v_mul_f32_e32 v25, v25, v31
	v_med3_f32 v31, v18, s24, v237
	v_med3_f32 v19, v19, s24, v237
	v_mov_b32_e32 v18, v65
	v_cvt_pk_fp8_f32 v18, v31, v19
	v_med3_f32 v28, v28, s24, v237
	v_med3_f32 v29, v29, s24, v237
	v_mov_b32_e32 v19, v65
	v_cvt_pk_fp8_f32 v19, v28, v29
	v_med3_f32 v26, v26, s24, v237
	v_med3_f32 v27, v27, s24, v237
	v_cvt_pk_fp8_f32 v18, v26, v27 op_sel:[0,0,1]
	v_med3_f32 v26, v30, s24, v237
	v_med3_f32 v25, v25, s24, v237
	v_cvt_pk_fp8_f32 v19, v26, v25 op_sel:[0,0,1]
	v_fma_f32 v25, v144, v24, v0
	v_min_f32_e32 v25, 0x40e00000, v25
	v_mul_f32_e32 v27, 0xc01d265f, v25
	v_add_co_u32_e32 v26, vcc, s57, v16
	v_exp_f32_e32 v28, v27
	s_nop 0
	v_addc_co_u32_e32 v27, vcc, 0, v17, vcc
	global_store_dwordx2 v[26:27], v[18:19], off
	v_fma_f32 v26, v145, v24, v1
	v_min_f32_e32 v26, 0x40e00000, v26
	v_add_f32_e32 v19, 1.0, v28
	v_mul_f32_e32 v27, 0xc01d265f, v26
	v_rcp_f32_e32 v19, v19
	v_exp_f32_e32 v27, v27
	v_fma_f32 v28, v147, v24, v3
	v_min_f32_e32 v28, 0x40e00000, v28
	v_mul_f32_e32 v19, v25, v19
	v_add_f32_e32 v25, 1.0, v27
	v_rcp_f32_e32 v25, v25
	v_mul_f32_e32 v29, 0xc01d265f, v28
	v_exp_f32_e32 v29, v29
	v_fma_f32 v30, v137, v24, v13
	v_mul_f32_e32 v25, v26, v25
	v_fma_f32 v26, v146, v24, v2
	v_min_f32_e32 v26, 0x40e00000, v26
	v_mul_f32_e32 v27, 0xc01d265f, v26
	v_exp_f32_e32 v27, v27
	v_min_f32_e32 v30, 0x40e00000, v30
	v_mul_f32_e32 v31, 0xc01d265f, v30
	v_exp_f32_e32 v31, v31
	v_add_f32_e32 v27, 1.0, v27
	v_rcp_f32_e32 v27, v27
	v_fma_f32 v18, v140, v24, v8
	v_med3_f32 v18, v18, s23, v236
	v_add_f32_e32 v18, 1.0, v18
	v_mul_f32_e32 v26, v26, v27
	v_add_f32_e32 v27, 1.0, v29
	v_rcp_f32_e32 v27, v27
	v_mul_f32_e32 v18, v18, v19
	v_fma_f32 v19, v141, v24, v9
	v_med3_f32 v19, v19, s23, v236
	v_mul_f32_e32 v27, v28, v27
	v_fma_f32 v28, v136, v24, v12
	v_min_f32_e32 v28, 0x40e00000, v28
	v_mul_f32_e32 v29, 0xc01d265f, v28
	v_exp_f32_e32 v29, v29
	v_add_f32_e32 v19, 1.0, v19
	v_mul_f32_e32 v19, v19, v25
	v_fma_f32 v25, v142, v24, v10
	v_add_f32_e32 v29, 1.0, v29
	v_rcp_f32_e32 v29, v29
	v_med3_f32 v25, v25, s23, v236
	v_add_f32_e32 v25, 1.0, v25
	v_mul_f32_e32 v25, v25, v26
	v_mul_f32_e32 v28, v28, v29
	v_add_f32_e32 v29, 1.0, v31
	v_rcp_f32_e32 v29, v29
	v_fma_f32 v26, v143, v24, v11
	v_fma_f32 v32, v139, v24, v15
	v_med3_f32 v26, v26, s23, v236
	v_mul_f32_e32 v29, v30, v29
	v_fma_f32 v30, v138, v24, v14
	v_min_f32_e32 v30, 0x40e00000, v30
	v_mul_f32_e32 v31, 0xc01d265f, v30
	v_exp_f32_e32 v31, v31
	v_min_f32_e32 v32, 0x40e00000, v32
	v_add_f32_e32 v26, 1.0, v26
	v_mul_f32_e32 v33, 0xc01d265f, v32
	v_add_f32_e32 v31, 1.0, v31
	v_mul_f32_e32 v26, v26, v27
	v_fma_f32 v27, v132, v24, v4
	v_rcp_f32_e32 v31, v31
	v_exp_f32_e32 v33, v33
	v_med3_f32 v27, v27, s23, v236
	v_add_f32_e32 v27, 1.0, v27
	v_mul_f32_e32 v27, v27, v28
	v_fma_f32 v28, v133, v24, v5
	v_med3_f32 v28, v28, s23, v236
	v_mul_f32_e32 v30, v30, v31
	v_add_f32_e32 v31, 1.0, v33
	v_add_f32_e32 v28, 1.0, v28
	v_rcp_f32_e32 v31, v31
	v_mul_f32_e32 v28, v28, v29
	v_fma_f32 v29, v134, v24, v6
	v_med3_f32 v29, v29, s23, v236
	v_fma_f32 v24, v135, v24, v7
	v_add_f32_e32 v29, 1.0, v29
	v_med3_f32 v24, v24, s23, v236
	v_mul_f32_e32 v29, v29, v30
	v_mul_f32_e32 v30, v32, v31
	v_add_f32_e32 v24, 1.0, v24
	v_mul_f32_e32 v24, v24, v30
	v_med3_f32 v30, v18, s24, v237
	v_med3_f32 v19, v19, s24, v237
	v_mov_b32_e32 v18, v65
	v_cvt_pk_fp8_f32 v18, v30, v19
	v_med3_f32 v27, v27, s24, v237
	v_med3_f32 v28, v28, s24, v237
	v_mov_b32_e32 v19, v65
	v_cvt_pk_fp8_f32 v19, v27, v28
	v_med3_f32 v25, v25, s24, v237
	v_med3_f32 v26, v26, s24, v237
	v_cvt_pk_fp8_f32 v18, v25, v26 op_sel:[0,0,1]
	v_med3_f32 v25, v29, s24, v237
	v_med3_f32 v24, v24, s24, v237
	v_cvt_pk_fp8_f32 v19, v25, v24 op_sel:[0,0,1]
	v_fma_f32 v25, v128, v23, v0
	v_min_f32_e32 v26, 0x40e00000, v25
	v_add_co_u32_e32 v24, vcc, s69, v16
	v_mul_f32_e32 v25, 0xc01d265f, v26
	v_exp_f32_e32 v27, v25
	v_addc_co_u32_e32 v25, vcc, 0, v17, vcc
	global_store_dwordx2 v[24:25], v[18:19], off
	v_fma_f32 v24, v129, v23, v1
	v_min_f32_e32 v24, 0x40e00000, v24
	v_mul_f32_e32 v25, 0xc01d265f, v24
	v_exp_f32_e32 v25, v25
	v_add_f32_e32 v19, 1.0, v27
	v_rcp_f32_e32 v19, v19
	v_fma_f32 v27, v131, v23, v3
	v_add_f32_e32 v25, 1.0, v25
	v_rcp_f32_e32 v25, v25
	v_mul_f32_e32 v19, v26, v19
	v_min_f32_e32 v27, 0x40e00000, v27
	v_mul_f32_e32 v28, 0xc01d265f, v27
	v_mul_f32_e32 v24, v24, v25
	v_fma_f32 v25, v130, v23, v2
	v_min_f32_e32 v25, 0x40e00000, v25
	v_mul_f32_e32 v26, 0xc01d265f, v25
	v_exp_f32_e32 v26, v26
	v_exp_f32_e32 v28, v28
	v_fma_f32 v29, v121, v23, v13
	v_min_f32_e32 v29, 0x40e00000, v29
	v_add_f32_e32 v26, 1.0, v26
	v_rcp_f32_e32 v26, v26
	v_mul_f32_e32 v30, 0xc01d265f, v29
	v_exp_f32_e32 v30, v30
	v_fma_f32 v18, v124, v23, v8
	v_mul_f32_e32 v25, v25, v26
	v_add_f32_e32 v26, 1.0, v28
	v_rcp_f32_e32 v26, v26
	v_med3_f32 v18, v18, s23, v236
	v_add_f32_e32 v18, 1.0, v18
	v_mul_f32_e32 v18, v18, v19
	v_mul_f32_e32 v26, v27, v26
	v_fma_f32 v27, v120, v23, v12
;     __device__ __forceinline__ void operator()(const f32x4 (&acc)[2][2][4][2], const Unit& u, int wr, int wc, int fr, int fq) const {
;     ...
;         for (int ai = 0; ai < 2; ++ai)
; #pragma unroll
;             for (int m = 0; m < 4; ++m) { const int r = row0 + ai * 128 + m * 16; const float rs = rsb[ai * 4 + m];
;                 float a[8];
; #pragma unroll
;                 for (int j = 0; j < 8; ++j) { const float gb = j < 4 ? g0[j & 3] : g1[j & 3], lb = j < 4 ? l0[j & 3] : l1[j & 3];
;                     const float gl = fminf(acc[ai][0][m][j >> 2][j & 3] * rs + gb, 7.0f), ln = fminf(fmaxf(acc[ai][1][m][j >> 2][j & 3] * rs + lb, -7.0f), 7.0f);
;                     a[j] = gl * __builtin_amdgcn_rcpf(1.0f + __builtin_amdgcn_exp2f(-1.702f * 1.4426950408889634f * gl)) * (ln + 1.0f); }
;                 v2u w; w.x = pk4_fp8(a[0], a[1], a[2], a[3]); w.y = pk4_fp8(a[4], a[5], a[6], a[7]);
;                 *(v2u*)(ACT + ((size_t)u.z * 256 + r) * FF + c0) = w; }
	v_min_f32_e32 v27, 0x40e00000, v27
	v_mul_f32_e32 v28, 0xc01d265f, v27
	v_exp_f32_e32 v28, v28
	v_fma_f32 v19, v125, v23, v9
	v_med3_f32 v19, v19, s23, v236
	v_add_f32_e32 v19, 1.0, v19
	v_add_f32_e32 v28, 1.0, v28
	v_rcp_f32_e32 v28, v28
	v_mul_f32_e32 v19, v19, v24
	v_fma_f32 v24, v126, v23, v10
	v_med3_f32 v24, v24, s23, v236
	v_mul_f32_e32 v27, v27, v28
	v_add_f32_e32 v28, 1.0, v30
	v_rcp_f32_e32 v28, v28
	v_add_f32_e32 v24, 1.0, v24
	v_mul_f32_e32 v24, v24, v25
	v_fma_f32 v25, v127, v23, v11
	v_mul_f32_e32 v28, v29, v28
	v_fma_f32 v29, v122, v23, v14
	v_min_f32_e32 v29, 0x40e00000, v29
	v_mul_f32_e32 v30, 0xc01d265f, v29
	v_exp_f32_e32 v30, v30
	v_fma_f32 v31, v123, v23, v15
	v_med3_f32 v25, v25, s23, v236
	v_min_f32_e32 v31, 0x40e00000, v31
	v_add_f32_e32 v25, 1.0, v25
	v_add_f32_e32 v30, 1.0, v30
	v_mul_f32_e32 v32, 0xc01d265f, v31
	v_mul_f32_e32 v25, v25, v26
	v_fma_f32 v26, v116, v23, v4
	v_rcp_f32_e32 v30, v30
	v_exp_f32_e32 v32, v32
	v_med3_f32 v26, v26, s23, v236
	v_add_f32_e32 v26, 1.0, v26
	v_mul_f32_e32 v26, v26, v27
	v_fma_f32 v27, v117, v23, v5
	v_med3_f32 v27, v27, s23, v236
	v_mul_f32_e32 v29, v29, v30
	v_add_f32_e32 v30, 1.0, v32
	v_add_f32_e32 v27, 1.0, v27
	v_rcp_f32_e32 v30, v30
	v_mul_f32_e32 v27, v27, v28
	v_fma_f32 v28, v118, v23, v6
	v_med3_f32 v28, v28, s23, v236
	v_fma_f32 v23, v119, v23, v7
	v_add_f32_e32 v28, 1.0, v28
	v_med3_f32 v23, v23, s23, v236
	v_mul_f32_e32 v28, v28, v29
	v_mul_f32_e32 v29, v31, v30
	v_add_f32_e32 v23, 1.0, v23
	v_mul_f32_e32 v23, v23, v29
	v_med3_f32 v29, v18, s24, v237
	v_med3_f32 v19, v19, s24, v237
	v_mov_b32_e32 v18, v65
	v_cvt_pk_fp8_f32 v18, v29, v19
	v_med3_f32 v26, v26, s24, v237
	v_med3_f32 v27, v27, s24, v237
	v_mov_b32_e32 v19, v65
	v_cvt_pk_fp8_f32 v19, v26, v27
	v_med3_f32 v24, v24, s24, v237
	v_med3_f32 v25, v25, s24, v237
	v_cvt_pk_fp8_f32 v18, v24, v25 op_sel:[0,0,1]
	v_med3_f32 v24, v28, s24, v237
	v_med3_f32 v23, v23, s24, v237
	v_cvt_pk_fp8_f32 v19, v24, v23 op_sel:[0,0,1]
	v_fma_f32 v23, v112, v22, v0
	v_min_f32_e32 v23, 0x40e00000, v23
	s_mov_b32 s4, 0x40000
	v_mul_f32_e32 v25, 0xc01d265f, v23
	v_add_co_u32_e32 v24, vcc, s4, v16
	v_exp_f32_e32 v26, v25
	s_nop 0
	v_addc_co_u32_e32 v25, vcc, 0, v17, vcc
	global_store_dwordx2 v[24:25], v[18:19], off
	v_fma_f32 v24, v113, v22, v1
	v_min_f32_e32 v24, 0x40e00000, v24
	v_add_f32_e32 v19, 1.0, v26
	v_mul_f32_e32 v25, 0xc01d265f, v24
	v_rcp_f32_e32 v19, v19
	v_exp_f32_e32 v25, v25
	v_fma_f32 v26, v115, v22, v3
	v_min_f32_e32 v26, 0x40e00000, v26
	v_mul_f32_e32 v19, v23, v19
	v_add_f32_e32 v23, 1.0, v25
	v_rcp_f32_e32 v23, v23
	v_mul_f32_e32 v27, 0xc01d265f, v26
	v_exp_f32_e32 v27, v27
	v_fma_f32 v28, v105, v22, v13
	v_mul_f32_e32 v23, v24, v23
	v_fma_f32 v24, v114, v22, v2
	v_min_f32_e32 v24, 0x40e00000, v24
	v_mul_f32_e32 v25, 0xc01d265f, v24
	v_exp_f32_e32 v25, v25
	v_min_f32_e32 v28, 0x40e00000, v28
	v_mul_f32_e32 v29, 0xc01d265f, v28
	v_exp_f32_e32 v29, v29
	v_add_f32_e32 v25, 1.0, v25
	v_rcp_f32_e32 v25, v25
	v_fma_f32 v18, v108, v22, v8
	v_med3_f32 v18, v18, s23, v236
	v_add_f32_e32 v18, 1.0, v18
	v_mul_f32_e32 v24, v24, v25
	v_add_f32_e32 v25, 1.0, v27
	v_rcp_f32_e32 v25, v25
	v_mul_f32_e32 v18, v18, v19
	v_fma_f32 v19, v109, v22, v9
	v_med3_f32 v19, v19, s23, v236
	v_mul_f32_e32 v25, v26, v25
	v_fma_f32 v26, v104, v22, v12
	v_min_f32_e32 v26, 0x40e00000, v26
	v_mul_f32_e32 v27, 0xc01d265f, v26
	v_exp_f32_e32 v27, v27
	v_add_f32_e32 v19, 1.0, v19
	v_mul_f32_e32 v19, v19, v23
	v_fma_f32 v23, v110, v22, v10
	v_add_f32_e32 v27, 1.0, v27
	v_rcp_f32_e32 v27, v27
	v_med3_f32 v23, v23, s23, v236
	v_add_f32_e32 v23, 1.0, v23
	v_mul_f32_e32 v23, v23, v24
	v_mul_f32_e32 v26, v26, v27
	v_add_f32_e32 v27, 1.0, v29
	v_rcp_f32_e32 v27, v27
	v_fma_f32 v24, v111, v22, v11
	v_fma_f32 v30, v107, v22, v15
	v_med3_f32 v24, v24, s23, v236
	v_mul_f32_e32 v27, v28, v27
	v_fma_f32 v28, v106, v22, v14
	v_min_f32_e32 v28, 0x40e00000, v28
	v_mul_f32_e32 v29, 0xc01d265f, v28
	v_exp_f32_e32 v29, v29
	v_min_f32_e32 v30, 0x40e00000, v30
	v_add_f32_e32 v24, 1.0, v24
	v_mul_f32_e32 v31, 0xc01d265f, v30
	v_add_f32_e32 v29, 1.0, v29
	v_mul_f32_e32 v24, v24, v25
	v_fma_f32 v25, v100, v22, v4
	v_rcp_f32_e32 v29, v29
	v_exp_f32_e32 v31, v31
	v_med3_f32 v25, v25, s23, v236
	v_add_f32_e32 v25, 1.0, v25
	v_mul_f32_e32 v25, v25, v26
	v_fma_f32 v26, v101, v22, v5
	v_med3_f32 v26, v26, s23, v236
	v_mul_f32_e32 v28, v28, v29
	v_add_f32_e32 v29, 1.0, v31
	v_add_f32_e32 v26, 1.0, v26
	v_rcp_f32_e32 v29, v29
	v_mul_f32_e32 v26, v26, v27
	v_fma_f32 v27, v102, v22, v6
	v_med3_f32 v27, v27, s23, v236
	v_fma_f32 v22, v103, v22, v7
	v_add_f32_e32 v27, 1.0, v27
	v_med3_f32 v22, v22, s23, v236
	v_mul_f32_e32 v27, v27, v28
	v_mul_f32_e32 v28, v30, v29
	v_add_f32_e32 v22, 1.0, v22
	v_mul_f32_e32 v22, v22, v28
	v_med3_f32 v28, v18, s24, v237
	v_med3_f32 v19, v19, s24, v237
	v_mov_b32_e32 v18, v65
	v_cvt_pk_fp8_f32 v18, v28, v19
	v_med3_f32 v25, v25, s24, v237
	v_med3_f32 v26, v26, s24, v237
	v_mov_b32_e32 v19, v65
	v_cvt_pk_fp8_f32 v19, v25, v26
	v_med3_f32 v23, v23, s24, v237
	v_med3_f32 v24, v24, s24, v237
	v_cvt_pk_fp8_f32 v18, v23, v24 op_sel:[0,0,1]
	v_med3_f32 v23, v27, s24, v237
	v_med3_f32 v22, v22, s24, v237
	v_cvt_pk_fp8_f32 v19, v23, v22 op_sel:[0,0,1]
	v_fma_f32 v23, v96, v21, v0
	s_mov_b32 s4, 0x48000
	v_min_f32_e32 v24, 0x40e00000, v23
	v_add_co_u32_e32 v22, vcc, s4, v16
	v_mul_f32_e32 v23, 0xc01d265f, v24
	v_exp_f32_e32 v25, v23
	v_addc_co_u32_e32 v23, vcc, 0, v17, vcc
	global_store_dwordx2 v[22:23], v[18:19], off
	v_fma_f32 v22, v97, v21, v1
	v_min_f32_e32 v22, 0x40e00000, v22
	v_mul_f32_e32 v23, 0xc01d265f, v22
	v_exp_f32_e32 v23, v23
	v_add_f32_e32 v19, 1.0, v25
;     __device__ __forceinline__ void operator()(const f32x4 (&acc)[2][2][4][2], const Unit& u, int wr, int wc, int fr, int fq) const {
;     ...
;         for (int ai = 0; ai < 2; ++ai)
; #pragma unroll
;             for (int m = 0; m < 4; ++m) { const int r = row0 + ai * 128 + m * 16; const float rs = rsb[ai * 4 + m];
;                 float a[8];
; #pragma unroll
;                 for (int j = 0; j < 8; ++j) { const float gb = j < 4 ? g0[j & 3] : g1[j & 3], lb = j < 4 ? l0[j & 3] : l1[j & 3];
;                     const float gl = fminf(acc[ai][0][m][j >> 2][j & 3] * rs + gb, 7.0f), ln = fminf(fmaxf(acc[ai][1][m][j >> 2][j & 3] * rs + lb, -7.0f), 7.0f);
;                     a[j] = gl * __builtin_amdgcn_rcpf(1.0f + __builtin_amdgcn_exp2f(-1.702f * 1.4426950408889634f * gl)) * (ln + 1.0f); }
;                 v2u w; w.x = pk4_fp8(a[0], a[1], a[2], a[3]); w.y = pk4_fp8(a[4], a[5], a[6], a[7]);
;                 *(v2u*)(ACT + ((size_t)u.z * 256 + r) * FF + c0) = w; }
;     }
	v_rcp_f32_e32 v19, v19
	v_fma_f32 v25, v99, v21, v3
	v_add_f32_e32 v23, 1.0, v23
	v_rcp_f32_e32 v23, v23
	v_mul_f32_e32 v19, v24, v19
	v_min_f32_e32 v25, 0x40e00000, v25
	v_mul_f32_e32 v26, 0xc01d265f, v25
	v_mul_f32_e32 v22, v22, v23
	v_fma_f32 v23, v98, v21, v2
	v_min_f32_e32 v23, 0x40e00000, v23
	v_mul_f32_e32 v24, 0xc01d265f, v23
	v_exp_f32_e32 v24, v24
	v_exp_f32_e32 v26, v26
	v_fma_f32 v27, v89, v21, v13
	v_min_f32_e32 v27, 0x40e00000, v27
	v_add_f32_e32 v24, 1.0, v24
	v_rcp_f32_e32 v24, v24
	v_mul_f32_e32 v28, 0xc01d265f, v27
	v_exp_f32_e32 v28, v28
	v_fma_f32 v18, v92, v21, v8
	v_mul_f32_e32 v23, v23, v24
	v_add_f32_e32 v24, 1.0, v26
	v_rcp_f32_e32 v24, v24
	v_med3_f32 v18, v18, s23, v236
	v_add_f32_e32 v18, 1.0, v18
	v_mul_f32_e32 v18, v18, v19
	v_mul_f32_e32 v24, v25, v24
	v_fma_f32 v25, v88, v21, v12
	v_min_f32_e32 v25, 0x40e00000, v25
	v_mul_f32_e32 v26, 0xc01d265f, v25
	v_exp_f32_e32 v26, v26
	v_fma_f32 v19, v93, v21, v9
	v_med3_f32 v19, v19, s23, v236
	v_add_f32_e32 v19, 1.0, v19
	v_add_f32_e32 v26, 1.0, v26
	v_rcp_f32_e32 v26, v26
	v_mul_f32_e32 v19, v19, v22
	v_fma_f32 v22, v94, v21, v10
	v_med3_f32 v22, v22, s23, v236
	v_mul_f32_e32 v25, v25, v26
	v_add_f32_e32 v26, 1.0, v28
	v_rcp_f32_e32 v26, v26
	v_add_f32_e32 v22, 1.0, v22
	v_mul_f32_e32 v22, v22, v23
	v_fma_f32 v23, v95, v21, v11
	v_mul_f32_e32 v26, v27, v26
	v_fma_f32 v27, v90, v21, v14
	v_min_f32_e32 v27, 0x40e00000, v27
	v_mul_f32_e32 v28, 0xc01d265f, v27
	v_exp_f32_e32 v28, v28
	v_fma_f32 v29, v91, v21, v15
	v_med3_f32 v23, v23, s23, v236
	v_min_f32_e32 v29, 0x40e00000, v29
	v_add_f32_e32 v23, 1.0, v23
	v_add_f32_e32 v28, 1.0, v28
	v_mul_f32_e32 v30, 0xc01d265f, v29
	v_mul_f32_e32 v23, v23, v24
	v_fma_f32 v24, v84, v21, v4
	v_rcp_f32_e32 v28, v28
	v_exp_f32_e32 v30, v30
	v_med3_f32 v24, v24, s23, v236
	v_add_f32_e32 v24, 1.0, v24
	v_mul_f32_e32 v24, v24, v25
	v_fma_f32 v25, v85, v21, v5
	v_med3_f32 v25, v25, s23, v236
	v_mul_f32_e32 v27, v27, v28
	v_add_f32_e32 v28, 1.0, v30
	v_add_f32_e32 v25, 1.0, v25
	v_rcp_f32_e32 v28, v28
	v_mul_f32_e32 v25, v25, v26
	v_fma_f32 v26, v86, v21, v6
	v_med3_f32 v26, v26, s23, v236
	v_fma_f32 v21, v87, v21, v7
	v_add_f32_e32 v26, 1.0, v26
	v_med3_f32 v21, v21, s23, v236
	v_mul_f32_e32 v26, v26, v27
	v_mul_f32_e32 v27, v29, v28
	v_add_f32_e32 v21, 1.0, v21
	v_mul_f32_e32 v21, v21, v27
	v_med3_f32 v27, v18, s24, v237
	v_med3_f32 v19, v19, s24, v237
	v_mov_b32_e32 v18, v65
	v_cvt_pk_fp8_f32 v18, v27, v19
	v_med3_f32 v24, v24, s24, v237
	v_med3_f32 v25, v25, s24, v237
	v_mov_b32_e32 v19, v65
	v_cvt_pk_fp8_f32 v19, v24, v25
	v_mul_f32_e32 v20, 0x3b800000, v20
	v_med3_f32 v22, v22, s24, v237
	v_med3_f32 v23, v23, s24, v237
	v_fma_f32 v14, v74, v20, v14
	v_cvt_pk_fp8_f32 v18, v22, v23 op_sel:[0,0,1]
	v_med3_f32 v22, v26, s24, v237
	v_med3_f32 v21, v21, s24, v237
	v_min_f32_e32 v14, 0x40e00000, v14
	v_cvt_pk_fp8_f32 v19, v22, v21 op_sel:[0,0,1]
	v_mul_f32_e32 v21, 0xc01d265f, v14
	v_exp_f32_e32 v21, v21
	s_mov_b32 s4, 0x50000
	v_add_co_u32_e32 v22, vcc, s4, v16
	v_fma_f32 v13, v73, v20, v13
	s_nop 0
	v_addc_co_u32_e32 v23, vcc, 0, v17, vcc
	global_store_dwordx2 v[22:23], v[18:19], off
	v_add_f32_e32 v18, 1.0, v21
	v_rcp_f32_e32 v18, v18
	v_min_f32_e32 v13, 0x40e00000, v13
	v_fma_f32 v6, v70, v20, v6
	v_med3_f32 v6, v6, s23, v236
	v_mul_f32_e32 v14, v14, v18
	v_mul_f32_e32 v18, 0xc01d265f, v13
	v_exp_f32_e32 v18, v18
	v_add_f32_e32 v6, 1.0, v6
	v_fma_f32 v12, v72, v20, v12
	v_mul_f32_e32 v6, v6, v14
	v_add_f32_e32 v14, 1.0, v18
	v_min_f32_e32 v12, 0x40e00000, v12
	v_rcp_f32_e32 v14, v14
	v_mul_f32_e32 v18, 0xc01d265f, v12
	v_exp_f32_e32 v18, v18
	v_fma_f32 v5, v69, v20, v5
	v_med3_f32 v5, v5, s23, v236
	v_add_f32_e32 v5, 1.0, v5
	v_mul_f32_e32 v13, v13, v14
	v_mul_f32_e32 v5, v5, v13
	v_add_f32_e32 v13, 1.0, v18
	v_rcp_f32_e32 v13, v13
	v_fma_f32 v3, v83, v20, v3
	v_min_f32_e32 v3, 0x40e00000, v3
	v_fma_f32 v4, v68, v20, v4
	v_mul_f32_e32 v12, v12, v13
	v_mul_f32_e32 v13, 0xc01d265f, v3
	v_exp_f32_e32 v13, v13
	v_med3_f32 v4, v4, s23, v236
	v_add_f32_e32 v4, 1.0, v4
	v_fma_f32 v2, v82, v20, v2
	v_mul_f32_e32 v4, v4, v12
	v_add_f32_e32 v12, 1.0, v13
	v_min_f32_e32 v2, 0x40e00000, v2
	v_rcp_f32_e32 v12, v12
	v_mul_f32_e32 v13, 0xc01d265f, v2
	v_exp_f32_e32 v13, v13
	v_fma_f32 v11, v79, v20, v11
	v_med3_f32 v11, v11, s23, v236
	v_add_f32_e32 v11, 1.0, v11
	v_mul_f32_e32 v3, v3, v12
	v_mul_f32_e32 v3, v11, v3
	v_add_f32_e32 v11, 1.0, v13
	v_rcp_f32_e32 v11, v11
	v_fma_f32 v10, v78, v20, v10
	v_med3_f32 v10, v10, s23, v236
	v_fma_f32 v1, v81, v20, v1
	v_add_f32_e32 v10, 1.0, v10
	v_mul_f32_e32 v2, v2, v11
	v_min_f32_e32 v1, 0x40e00000, v1
	v_mul_f32_e32 v2, v10, v2
	v_mul_f32_e32 v10, 0xc01d265f, v1
	v_exp_f32_e32 v10, v10
	v_fmac_f32_e32 v0, v80, v20
	v_min_f32_e32 v0, 0x40e00000, v0
	v_mul_f32_e32 v11, 0xc01d265f, v0
	v_add_f32_e32 v10, 1.0, v10
	v_rcp_f32_e32 v10, v10
	v_exp_f32_e32 v11, v11
	v_fma_f32 v9, v77, v20, v9
	v_med3_f32 v9, v9, s23, v236
	v_fmac_f32_e32 v15, v75, v20
	v_add_f32_e32 v9, 1.0, v9
	v_mul_f32_e32 v1, v1, v10
	v_min_f32_e32 v10, 0x40e00000, v15
	v_mul_f32_e32 v1, v9, v1
	v_add_f32_e32 v9, 1.0, v11
	v_mul_f32_e32 v11, 0xc01d265f, v10
	v_rcp_f32_e32 v9, v9
	v_exp_f32_e32 v11, v11
	v_fmac_f32_e32 v8, v76, v20
	v_med3_f32 v8, v8, s23, v236
	v_mul_f32_e32 v0, v0, v9
	v_add_f32_e32 v9, 1.0, v11
	v_rcp_f32_e32 v9, v9
	v_fmac_f32_e32 v7, v71, v20
	v_add_f32_e32 v8, 1.0, v8
	v_med3_f32 v7, v7, s23, v236
	v_mul_f32_e32 v0, v8, v0
	v_mul_f32_e32 v8, v10, v9
	v_add_f32_e32 v7, 1.0, v7
	v_mul_f32_e32 v7, v7, v8
	v_med3_f32 v8, v0, s24, v237
	v_med3_f32 v1, v1, s24, v237
	v_mov_b32_e32 v0, v65
	v_cvt_pk_fp8_f32 v0, v8, v1
	v_med3_f32 v4, v4, s24, v237
	v_med3_f32 v5, v5, s24, v237
	v_mov_b32_e32 v1, v65
	v_cvt_pk_fp8_f32 v1, v4, v5
	v_med3_f32 v2, v2, s24, v237
	v_med3_f32 v3, v3, s24, v237
	v_cvt_pk_fp8_f32 v0, v2, v3 op_sel:[0,0,1]
	v_med3_f32 v2, v6, s24, v237
	v_med3_f32 v3, v7, s24, v237
	v_cvt_pk_fp8_f32 v1, v2, v3 op_sel:[0,0,1]
	v_add_co_u32_e32 v2, vcc, 0x58000, v16
	s_nop 1
	v_addc_co_u32_e32 v3, vcc, 0, v17, vcc
	global_store_dwordx2 v[2:3], v[0:1], off
	s_cbranch_scc1 .LBB0_1541
; #define GAS __attribute__((address_space(1)))
; template <bool GAIN, bool NT = false> __device__ __forceinline__ void titem8_load(const TItem& d, int lane, f32x4 (&r)[16], f32x4 (&g)[4]) {
;     const int q = lane & 7, kg = lane >> 3; const unsigned lo = (unsigned)((16 * kg) * d.N + 4 * q) * 4u;
;     const GAS char* base = (const GAS char*)d.src;
; #pragma unroll
;     for (int j = 0; j < 16; ++j) { const GAS f32x4* p = (const GAS f32x4*)(base + (size_t)j * (size_t)d.N * 4 + lo); r[j] = NT ? __builtin_nontemporal_load(p) : *p; }
;     if constexpr (GAIN) { const GAS char* gb = (const GAS char*)d.gain; const unsigned go = (unsigned)(16 * kg) * 4u;
; #pragma unroll
;         for (int j4 = 0; j4 < 4; ++j4) g[j4] = *(const GAS f32x4*)(gb + 16 * j4 + go); }
;     asm volatile("" ::: "memory"); __builtin_amdgcn_sched_barrier(0);
	v_readlane_b32 s0, v254, 26
	v_readlane_b32 s1, v254, 27
	v_mov_b32_e32 v0, v65
	s_andn2_b64 vcc, exec, s[0:1]
	s_cbranch_vccnz .LBB0_1541
	v_mbcnt_lo_u32_b32 v64, -1, 0
	v_mbcnt_hi_u32_b32 v64, -1, v64
	v_and_b32_e32 v194, 7, v64
	v_lshrrev_b32_e32 v195, 3, v64
	v_lshlrev_b32_e32 v246, 17, v195
	v_lshl_or_b32 v246, v194, 4, v246
	v_add_u32_e32 v247, 0x2000, v246
	v_add_u32_e32 v248, 0x4000, v246
	v_add_u32_e32 v249, 0x6000, v246
	v_lshlrev_b32_e32 v250, 13, v194
	v_lshl_or_b32 v250, v195, 4, v250
	v_add_u32_e32 v251, 0x1000, v250
	v_readlane_b32 s0, v254, 60
	v_readlane_b32 s4, v254, 4
	v_readlane_b32 s5, v254, 5
	s_nop 3
	s_lshl_b32 s1, s92, 3
	s_add_i32 s0, s0, s1
	s_lshr_b32 s1, s0, 10
	s_and_b32 s0, s0, 0x3ff
	s_lshr_b32 s2, s0, 6
	s_and_b32 s0, s0, 63
	s_lshl_b32 s35, s1, 24
	s_lshl_b32 s38, s2, 20
	s_add_i32 s35, s35, s38
	s_lshl_b32 s38, s0, 7
	s_add_i32 s35, s35, s38
	s_add_u32 s4, s4, s35
	s_addc_u32 s5, s5, 0
	s_add_u32 s6, s4, 0x8000
	s_addc_u32 s7, s5, 0
	s_add_u32 s8, s4, 0x10000
	s_addc_u32 s9, s5, 0
	s_add_u32 s38, s4, 0x18000
	s_addc_u32 s39, s5, 0
	s_lshl_b32 s35, s1, 22
	s_lshl_b32 s40, s0, 16
	s_add_i32 s35, s35, s40
	s_lshl_b32 s40, s2, 7
	s_add_i32 s35, s35, s40
	s_add_u32 s42, s78, 0x57dc8000
	s_addc_u32 s43, s79, 0
	s_add_u32 s42, s42, s35
	s_addc_u32 s43, s43, 0
	global_load_dwordx4 v[0:3], v246, s[4:5] nt
	global_load_dwordx4 v[4:7], v247, s[4:5] nt
	global_load_dwordx4 v[8:11], v248, s[4:5] nt
	global_load_dwordx4 v[12:15], v249, s[4:5] nt
	global_load_dwordx4 v[16:19], v246, s[6:7] nt
	global_load_dwordx4 v[20:23], v247, s[6:7] nt
	global_load_dwordx4 v[24:27], v248, s[6:7] nt
	global_load_dwordx4 v[28:31], v249, s[6:7] nt
	global_load_dwordx4 v[32:35], v246, s[8:9] nt
	global_load_dwordx4 v[36:39], v247, s[8:9] nt
	global_load_dwordx4 v[40:43], v248, s[8:9] nt
	global_load_dwordx4 v[44:47], v249, s[8:9] nt
	global_load_dwordx4 v[48:51], v246, s[38:39] nt
	global_load_dwordx4 v[52:55], v247, s[38:39] nt
	global_load_dwordx4 v[56:59], v248, s[38:39] nt
	global_load_dwordx4 v[60:63], v249, s[38:39] nt
	s_add_u32 s4, s4, 0x2000000
	s_addc_u32 s5, s5, 0
	s_add_u32 s6, s6, 0x2000000
	s_addc_u32 s7, s7, 0
	s_add_u32 s8, s8, 0x2000000
	s_addc_u32 s9, s9, 0
	s_add_u32 s38, s38, 0x2000000
	s_addc_u32 s39, s39, 0
	global_load_dwordx4 v[66:69], v246, s[4:5] nt
	global_load_dwordx4 v[70:73], v247, s[4:5] nt
	global_load_dwordx4 v[74:77], v248, s[4:5] nt
	global_load_dwordx4 v[78:81], v249, s[4:5] nt
	global_load_dwordx4 v[82:85], v246, s[6:7] nt
	global_load_dwordx4 v[86:89], v247, s[6:7] nt
	global_load_dwordx4 v[90:93], v248, s[6:7] nt
	global_load_dwordx4 v[94:97], v249, s[6:7] nt
	global_load_dwordx4 v[98:101], v246, s[8:9] nt
	global_load_dwordx4 v[102:105], v247, s[8:9] nt
	global_load_dwordx4 v[106:109], v248, s[8:9] nt
	global_load_dwordx4 v[110:113], v249, s[8:9] nt
	global_load_dwordx4 v[114:117], v246, s[38:39] nt
	global_load_dwordx4 v[118:121], v247, s[38:39] nt
	global_load_dwordx4 v[122:125], v248, s[38:39] nt
	global_load_dwordx4 v[126:129], v249, s[38:39] nt
	s_add_u32 s4, s4, 0x2000000
	s_addc_u32 s5, s5, 0
	s_add_u32 s6, s6, 0x2000000
	s_addc_u32 s7, s7, 0
	s_add_u32 s8, s8, 0x2000000
	s_addc_u32 s9, s9, 0
	s_add_u32 s38, s38, 0x2000000
	s_addc_u32 s39, s39, 0
	global_load_dwordx4 v[130:133], v246, s[4:5] nt
	global_load_dwordx4 v[134:137], v247, s[4:5] nt
	global_load_dwordx4 v[138:141], v248, s[4:5] nt
	global_load_dwordx4 v[142:145], v249, s[4:5] nt
	global_load_dwordx4 v[146:149], v246, s[6:7] nt
	global_load_dwordx4 v[150:153], v247, s[6:7] nt
	global_load_dwordx4 v[154:157], v248, s[6:7] nt
	global_load_dwordx4 v[158:161], v249, s[6:7] nt
	global_load_dwordx4 v[162:165], v246, s[8:9] nt
	global_load_dwordx4 v[166:169], v247, s[8:9] nt
	global_load_dwordx4 v[170:173], v248, s[8:9] nt
	global_load_dwordx4 v[174:177], v249, s[8:9] nt
	global_load_dwordx4 v[178:181], v246, s[38:39] nt
	global_load_dwordx4 v[182:185], v247, s[38:39] nt
	global_load_dwordx4 v[186:189], v248, s[38:39] nt
	global_load_dwordx4 v[190:193], v249, s[38:39] nt
	s_add_u32 s4, s4, 0x2000000
	s_addc_u32 s5, s5, 0
	s_add_u32 s6, s6, 0x2000000
	s_addc_u32 s7, s7, 0
	s_add_u32 s8, s8, 0x2000000
	s_addc_u32 s9, s9, 0
	s_add_u32 s38, s38, 0x2000000
	s_addc_u32 s39, s39, 0
	s_waitcnt vmcnt(32)
; #define GAS __attribute__((address_space(1)))
; template <bool GAIN, bool NT = false> __device__ __forceinline__ void titem8_store(const TItem& d, int lane, const f32x4 (&r)[16], const f32x4 (&g)[4]) {
;     const int q = lane & 7, kg = lane >> 3; const unsigned lo = (unsigned)((4 * q) * d.ldk + 16 * kg);
;     GAS char* base = (GAS char*)d.dst;
;     f32x4 s[16];
; #pragma unroll
;     for (int j = 0; j < 16; ++j) s[j] = r[j] * ((GAIN ? g[j >> 2][j & 3] : 1.0f) * W8_SCALE);
; #pragma unroll
;     for (int i = 0; i < 4; ++i) { v4u w;
;         w.x = pk4_fp8w(s[0][i], s[1][i], s[2][i], s[3][i]); w.y = pk4_fp8w(s[4][i], s[5][i], s[6][i], s[7][i]);
;         w.z = pk4_fp8w(s[8][i], s[9][i], s[10][i], s[11][i]); w.w = pk4_fp8w(s[12][i], s[13][i], s[14][i], s[15][i]);
;         GAS v4u* p = (GAS v4u*)(base + (size_t)i * (size_t)d.ldk + lo);
;         if (NT) __builtin_nontemporal_store(w, p); else *p = w; }
; }
	v_pk_mul_f32 v[0:1], v[0:1], s[30:31] op_sel_hi:[1,0]
	v_pk_mul_f32 v[2:3], v[2:3], s[30:31] op_sel_hi:[1,0]
	v_pk_mul_f32 v[4:5], v[4:5], s[30:31] op_sel_hi:[1,0]
	v_pk_mul_f32 v[6:7], v[6:7], s[30:31] op_sel_hi:[1,0]
	v_pk_mul_f32 v[8:9], v[8:9], s[30:31] op_sel_hi:[1,0]
	v_pk_mul_f32 v[10:11], v[10:11], s[30:31] op_sel_hi:[1,0]
	v_pk_mul_f32 v[12:13], v[12:13], s[30:31] op_sel_hi:[1,0]
	v_pk_mul_f32 v[14:15], v[14:15], s[30:31] op_sel_hi:[1,0]
	v_pk_mul_f32 v[16:17], v[16:17], s[30:31] op_sel_hi:[1,0]
	v_pk_mul_f32 v[18:19], v[18:19], s[30:31] op_sel_hi:[1,0]
	v_pk_mul_f32 v[20:21], v[20:21], s[30:31] op_sel_hi:[1,0]
	v_pk_mul_f32 v[22:23], v[22:23], s[30:31] op_sel_hi:[1,0]
	v_pk_mul_f32 v[24:25], v[24:25], s[30:31] op_sel_hi:[1,0]
	v_pk_mul_f32 v[26:27], v[26:27], s[30:31] op_sel_hi:[1,0]
	v_pk_mul_f32 v[28:29], v[28:29], s[30:31] op_sel_hi:[1,0]
	v_pk_mul_f32 v[30:31], v[30:31], s[30:31] op_sel_hi:[1,0]
	v_pk_mul_f32 v[32:33], v[32:33], s[30:31] op_sel_hi:[1,0]
	v_pk_mul_f32 v[34:35], v[34:35], s[30:31] op_sel_hi:[1,0]
	v_pk_mul_f32 v[36:37], v[36:37], s[30:31] op_sel_hi:[1,0]
	v_pk_mul_f32 v[38:39], v[38:39], s[30:31] op_sel_hi:[1,0]
	v_pk_mul_f32 v[40:41], v[40:41], s[30:31] op_sel_hi:[1,0]
	v_pk_mul_f32 v[42:43], v[42:43], s[30:31] op_sel_hi:[1,0]
	v_pk_mul_f32 v[44:45], v[44:45], s[30:31] op_sel_hi:[1,0]
	v_pk_mul_f32 v[46:47], v[46:47], s[30:31] op_sel_hi:[1,0]
	v_pk_mul_f32 v[48:49], v[48:49], s[30:31] op_sel_hi:[1,0]
	v_pk_mul_f32 v[50:51], v[50:51], s[30:31] op_sel_hi:[1,0]
	v_pk_mul_f32 v[52:53], v[52:53], s[30:31] op_sel_hi:[1,0]
	v_pk_mul_f32 v[54:55], v[54:55], s[30:31] op_sel_hi:[1,0]
	v_pk_mul_f32 v[56:57], v[56:57], s[30:31] op_sel_hi:[1,0]
	v_pk_mul_f32 v[58:59], v[58:59], s[30:31] op_sel_hi:[1,0]
	v_pk_mul_f32 v[60:61], v[60:61], s[30:31] op_sel_hi:[1,0]
	v_pk_mul_f32 v[62:63], v[62:63], s[30:31] op_sel_hi:[1,0]
	v_med3_f32 v0, v0, s24, v237
	v_med3_f32 v1, v1, s24, v237
	v_med3_f32 v2, v2, s24, v237
	v_med3_f32 v3, v3, s24, v237
	v_med3_f32 v4, v4, s24, v237
	v_med3_f32 v5, v5, s24, v237
	v_med3_f32 v6, v6, s24, v237
	v_med3_f32 v7, v7, s24, v237
	v_med3_f32 v8, v8, s24, v237
	v_med3_f32 v9, v9, s24, v237
	v_med3_f32 v10, v10, s24, v237
	v_med3_f32 v11, v11, s24, v237
	v_med3_f32 v12, v12, s24, v237
	v_med3_f32 v13, v13, s24, v237
	v_med3_f32 v14, v14, s24, v237
	v_med3_f32 v15, v15, s24, v237
	v_med3_f32 v16, v16, s24, v237
	v_med3_f32 v17, v17, s24, v237
	v_med3_f32 v18, v18, s24, v237
	v_med3_f32 v19, v19, s24, v237
	v_med3_f32 v20, v20, s24, v237
	v_med3_f32 v21, v21, s24, v237
	v_med3_f32 v22, v22, s24, v237
	v_med3_f32 v23, v23, s24, v237
	v_med3_f32 v24, v24, s24, v237
	v_med3_f32 v25, v25, s24, v237
	v_med3_f32 v26, v26, s24, v237
	v_med3_f32 v27, v27, s24, v237
	v_med3_f32 v28, v28, s24, v237
	v_med3_f32 v29, v29, s24, v237
	v_med3_f32 v30, v30, s24, v237
	v_med3_f32 v31, v31, s24, v237
	v_med3_f32 v32, v32, s24, v237
	v_med3_f32 v33, v33, s24, v237
	v_med3_f32 v34, v34, s24, v237
	v_med3_f32 v35, v35, s24, v237
	v_med3_f32 v36, v36, s24, v237
	v_med3_f32 v37, v37, s24, v237
	v_med3_f32 v38, v38, s24, v237
	v_med3_f32 v39, v39, s24, v237
	v_med3_f32 v40, v40, s24, v237
	v_med3_f32 v41, v41, s24, v237
	v_med3_f32 v42, v42, s24, v237
	v_med3_f32 v43, v43, s24, v237
	v_med3_f32 v44, v44, s24, v237
	v_med3_f32 v45, v45, s24, v237
	v_med3_f32 v46, v46, s24, v237
	v_med3_f32 v47, v47, s24, v237
	v_med3_f32 v48, v48, s24, v237
	v_med3_f32 v49, v49, s24, v237
	v_med3_f32 v50, v50, s24, v237
	v_med3_f32 v51, v51, s24, v237
	v_med3_f32 v52, v52, s24, v237
	v_med3_f32 v53, v53, s24, v237
	v_med3_f32 v54, v54, s24, v237
	v_med3_f32 v55, v55, s24, v237
	v_med3_f32 v56, v56, s24, v237
	v_med3_f32 v57, v57, s24, v237
	v_med3_f32 v58, v58, s24, v237
	v_med3_f32 v59, v59, s24, v237
	v_med3_f32 v60, v60, s24, v237
	v_med3_f32 v61, v61, s24, v237
	v_med3_f32 v62, v62, s24, v237
	v_med3_f32 v63, v63, s24, v237
	v_cvt_pk_fp8_f32 v0, v0, v4
	v_cvt_pk_fp8_f32 v0, v8, v12 op_sel:[0,0,1]
	v_cvt_pk_fp8_f32 v4, v1, v5
	v_cvt_pk_fp8_f32 v4, v9, v13 op_sel:[0,0,1]
	v_cvt_pk_fp8_f32 v8, v2, v6
	v_cvt_pk_fp8_f32 v8, v10, v14 op_sel:[0,0,1]
	v_cvt_pk_fp8_f32 v12, v3, v7
	v_cvt_pk_fp8_f32 v12, v11, v15 op_sel:[0,0,1]
	v_cvt_pk_fp8_f32 v1, v16, v20
	v_cvt_pk_fp8_f32 v1, v24, v28 op_sel:[0,0,1]
	v_cvt_pk_fp8_f32 v5, v17, v21
	v_cvt_pk_fp8_f32 v5, v25, v29 op_sel:[0,0,1]
	v_cvt_pk_fp8_f32 v9, v18, v22
	v_cvt_pk_fp8_f32 v9, v26, v30 op_sel:[0,0,1]
	v_cvt_pk_fp8_f32 v13, v19, v23
	v_cvt_pk_fp8_f32 v13, v27, v31 op_sel:[0,0,1]
	v_cvt_pk_fp8_f32 v2, v32, v36
	v_cvt_pk_fp8_f32 v2, v40, v44 op_sel:[0,0,1]
	v_cvt_pk_fp8_f32 v6, v33, v37
	v_cvt_pk_fp8_f32 v6, v41, v45 op_sel:[0,0,1]
	v_cvt_pk_fp8_f32 v10, v34, v38
	v_cvt_pk_fp8_f32 v10, v42, v46 op_sel:[0,0,1]
	v_cvt_pk_fp8_f32 v14, v35, v39
	v_cvt_pk_fp8_f32 v14, v43, v47 op_sel:[0,0,1]
	v_cvt_pk_fp8_f32 v3, v48, v52
	v_cvt_pk_fp8_f32 v3, v56, v60 op_sel:[0,0,1]
	v_cvt_pk_fp8_f32 v7, v49, v53
	v_cvt_pk_fp8_f32 v7, v57, v61 op_sel:[0,0,1]
	v_cvt_pk_fp8_f32 v11, v50, v54
	v_cvt_pk_fp8_f32 v11, v58, v62 op_sel:[0,0,1]
	v_cvt_pk_fp8_f32 v15, v51, v55
	v_cvt_pk_fp8_f32 v15, v59, v63 op_sel:[0,0,1]
	global_store_dwordx4 v250, v[0:3], s[42:43] nt
	global_store_dwordx4 v250, v[4:7], s[42:43] offset:2048 nt
	global_store_dwordx4 v251, v[8:11], s[42:43] nt
	global_store_dwordx4 v251, v[12:15], s[42:43] offset:2048 nt
	s_add_u32 s42, s42, 0x800000
	s_addc_u32 s43, s43, 0
	global_load_dwordx4 v[0:3], v246, s[4:5] nt
	global_load_dwordx4 v[4:7], v247, s[4:5] nt
	global_load_dwordx4 v[8:11], v248, s[4:5] nt
	global_load_dwordx4 v[12:15], v249, s[4:5] nt
	global_load_dwordx4 v[16:19], v246, s[6:7] nt
	global_load_dwordx4 v[20:23], v247, s[6:7] nt
	global_load_dwordx4 v[24:27], v248, s[6:7] nt
	global_load_dwordx4 v[28:31], v249, s[6:7] nt
	global_load_dwordx4 v[32:35], v246, s[8:9] nt
	global_load_dwordx4 v[36:39], v247, s[8:9] nt
	global_load_dwordx4 v[40:43], v248, s[8:9] nt
	global_load_dwordx4 v[44:47], v249, s[8:9] nt
	global_load_dwordx4 v[48:51], v246, s[38:39] nt
	global_load_dwordx4 v[52:55], v247, s[38:39] nt
	global_load_dwordx4 v[56:59], v248, s[38:39] nt
	global_load_dwordx4 v[60:63], v249, s[38:39] nt
	s_add_u32 s4, s4, 0x2000000
	s_addc_u32 s5, s5, 0
	s_add_u32 s6, s6, 0x2000000
	s_addc_u32 s7, s7, 0
	s_add_u32 s8, s8, 0x2000000
	s_addc_u32 s9, s9, 0
	s_add_u32 s38, s38, 0x2000000
	s_addc_u32 s39, s39, 0
	s_waitcnt vmcnt(36)
; #define GAS __attribute__((address_space(1)))
; template <bool GAIN, bool NT = false> __device__ __forceinline__ void titem8_load(const TItem& d, int lane, f32x4 (&r)[16], f32x4 (&g)[4]) {
;     const int q = lane & 7, kg = lane >> 3; const unsigned lo = (unsigned)((16 * kg) * d.N + 4 * q) * 4u;
;     const GAS char* base = (const GAS char*)d.src;
; #pragma unroll
;     for (int j = 0; j < 16; ++j) { const GAS f32x4* p = (const GAS f32x4*)(base + (size_t)j * (size_t)d.N * 4 + lo); r[j] = NT ? __builtin_nontemporal_load(p) : *p; }
; template <bool GAIN, bool NT = false> __device__ __forceinline__ void titem8_store(const TItem& d, int lane, const f32x4 (&r)[16], const f32x4 (&g)[4]) {
;     const int q = lane & 7, kg = lane >> 3; const unsigned lo = (unsigned)((4 * q) * d.ldk + 16 * kg);
;     GAS char* base = (GAS char*)d.dst;
;     f32x4 s[16];
; #pragma unroll
;     for (int j = 0; j < 16; ++j) s[j] = r[j] * ((GAIN ? g[j >> 2][j & 3] : 1.0f) * W8_SCALE);
; #pragma unroll
;     for (int i = 0; i < 4; ++i) { v4u w;
;         w.x = pk4_fp8w(s[0][i], s[1][i], s[2][i], s[3][i]); w.y = pk4_fp8w(s[4][i], s[5][i], s[6][i], s[7][i]);
;         w.z = pk4_fp8w(s[8][i], s[9][i], s[10][i], s[11][i]); w.w = pk4_fp8w(s[12][i], s[13][i], s[14][i], s[15][i]);
;         GAS v4u* p = (GAS v4u*)(base + (size_t)i * (size_t)d.ldk + lo);
;         if (NT) __builtin_nontemporal_store(w, p); else *p = w; }
	v_pk_mul_f32 v[66:67], v[66:67], s[30:31] op_sel_hi:[1,0]
	v_pk_mul_f32 v[68:69], v[68:69], s[30:31] op_sel_hi:[1,0]
	v_pk_mul_f32 v[70:71], v[70:71], s[30:31] op_sel_hi:[1,0]
	v_pk_mul_f32 v[72:73], v[72:73], s[30:31] op_sel_hi:[1,0]
	v_pk_mul_f32 v[74:75], v[74:75], s[30:31] op_sel_hi:[1,0]
	v_pk_mul_f32 v[76:77], v[76:77], s[30:31] op_sel_hi:[1,0]
	v_pk_mul_f32 v[78:79], v[78:79], s[30:31] op_sel_hi:[1,0]
	v_pk_mul_f32 v[80:81], v[80:81], s[30:31] op_sel_hi:[1,0]
	v_pk_mul_f32 v[82:83], v[82:83], s[30:31] op_sel_hi:[1,0]
	v_pk_mul_f32 v[84:85], v[84:85], s[30:31] op_sel_hi:[1,0]
	v_pk_mul_f32 v[86:87], v[86:87], s[30:31] op_sel_hi:[1,0]
	v_pk_mul_f32 v[88:89], v[88:89], s[30:31] op_sel_hi:[1,0]
	v_pk_mul_f32 v[90:91], v[90:91], s[30:31] op_sel_hi:[1,0]
	v_pk_mul_f32 v[92:93], v[92:93], s[30:31] op_sel_hi:[1,0]
	v_pk_mul_f32 v[94:95], v[94:95], s[30:31] op_sel_hi:[1,0]
	v_pk_mul_f32 v[96:97], v[96:97], s[30:31] op_sel_hi:[1,0]
	v_pk_mul_f32 v[98:99], v[98:99], s[30:31] op_sel_hi:[1,0]
	v_pk_mul_f32 v[100:101], v[100:101], s[30:31] op_sel_hi:[1,0]
	v_pk_mul_f32 v[102:103], v[102:103], s[30:31] op_sel_hi:[1,0]
	v_pk_mul_f32 v[104:105], v[104:105], s[30:31] op_sel_hi:[1,0]
	v_pk_mul_f32 v[106:107], v[106:107], s[30:31] op_sel_hi:[1,0]
	v_pk_mul_f32 v[108:109], v[108:109], s[30:31] op_sel_hi:[1,0]
	v_pk_mul_f32 v[110:111], v[110:111], s[30:31] op_sel_hi:[1,0]
	v_pk_mul_f32 v[112:113], v[112:113], s[30:31] op_sel_hi:[1,0]
	v_pk_mul_f32 v[114:115], v[114:115], s[30:31] op_sel_hi:[1,0]
	v_pk_mul_f32 v[116:117], v[116:117], s[30:31] op_sel_hi:[1,0]
	v_pk_mul_f32 v[118:119], v[118:119], s[30:31] op_sel_hi:[1,0]
	v_pk_mul_f32 v[120:121], v[120:121], s[30:31] op_sel_hi:[1,0]
	v_pk_mul_f32 v[122:123], v[122:123], s[30:31] op_sel_hi:[1,0]
	v_pk_mul_f32 v[124:125], v[124:125], s[30:31] op_sel_hi:[1,0]
	v_pk_mul_f32 v[126:127], v[126:127], s[30:31] op_sel_hi:[1,0]
	v_pk_mul_f32 v[128:129], v[128:129], s[30:31] op_sel_hi:[1,0]
	v_med3_f32 v66, v66, s24, v237
	v_med3_f32 v67, v67, s24, v237
	v_med3_f32 v68, v68, s24, v237
	v_med3_f32 v69, v69, s24, v237
	v_med3_f32 v70, v70, s24, v237
	v_med3_f32 v71, v71, s24, v237
	v_med3_f32 v72, v72, s24, v237
	v_med3_f32 v73, v73, s24, v237
	v_med3_f32 v74, v74, s24, v237
	v_med3_f32 v75, v75, s24, v237
	v_med3_f32 v76, v76, s24, v237
	v_med3_f32 v77, v77, s24, v237
	v_med3_f32 v78, v78, s24, v237
	v_med3_f32 v79, v79, s24, v237
	v_med3_f32 v80, v80, s24, v237
	v_med3_f32 v81, v81, s24, v237
	v_med3_f32 v82, v82, s24, v237
	v_med3_f32 v83, v83, s24, v237
	v_med3_f32 v84, v84, s24, v237
	v_med3_f32 v85, v85, s24, v237
	v_med3_f32 v86, v86, s24, v237
	v_med3_f32 v87, v87, s24, v237
	v_med3_f32 v88, v88, s24, v237
	v_med3_f32 v89, v89, s24, v237
	v_med3_f32 v90, v90, s24, v237
	v_med3_f32 v91, v91, s24, v237
	v_med3_f32 v92, v92, s24, v237
	v_med3_f32 v93, v93, s24, v237
	v_med3_f32 v94, v94, s24, v237
	v_med3_f32 v95, v95, s24, v237
	v_med3_f32 v96, v96, s24, v237
	v_med3_f32 v97, v97, s24, v237
	v_med3_f32 v98, v98, s24, v237
	v_med3_f32 v99, v99, s24, v237
	v_med3_f32 v100, v100, s24, v237
	v_med3_f32 v101, v101, s24, v237
	v_med3_f32 v102, v102, s24, v237
	v_med3_f32 v103, v103, s24, v237
	v_med3_f32 v104, v104, s24, v237
	v_med3_f32 v105, v105, s24, v237
	v_med3_f32 v106, v106, s24, v237
	v_med3_f32 v107, v107, s24, v237
	v_med3_f32 v108, v108, s24, v237
	v_med3_f32 v109, v109, s24, v237
	v_med3_f32 v110, v110, s24, v237
	v_med3_f32 v111, v111, s24, v237
	v_med3_f32 v112, v112, s24, v237
	v_med3_f32 v113, v113, s24, v237
	v_med3_f32 v114, v114, s24, v237
	v_med3_f32 v115, v115, s24, v237
	v_med3_f32 v116, v116, s24, v237
	v_med3_f32 v117, v117, s24, v237
	v_med3_f32 v118, v118, s24, v237
	v_med3_f32 v119, v119, s24, v237
	v_med3_f32 v120, v120, s24, v237
	v_med3_f32 v121, v121, s24, v237
	v_med3_f32 v122, v122, s24, v237
	v_med3_f32 v123, v123, s24, v237
	v_med3_f32 v124, v124, s24, v237
	v_med3_f32 v125, v125, s24, v237
	v_med3_f32 v126, v126, s24, v237
	v_med3_f32 v127, v127, s24, v237
	v_med3_f32 v128, v128, s24, v237
	v_med3_f32 v129, v129, s24, v237
	v_cvt_pk_fp8_f32 v66, v66, v70
	v_cvt_pk_fp8_f32 v66, v74, v78 op_sel:[0,0,1]
	v_cvt_pk_fp8_f32 v70, v67, v71
	v_cvt_pk_fp8_f32 v70, v75, v79 op_sel:[0,0,1]
	v_cvt_pk_fp8_f32 v74, v68, v72
	v_cvt_pk_fp8_f32 v74, v76, v80 op_sel:[0,0,1]
	v_cvt_pk_fp8_f32 v78, v69, v73
	v_cvt_pk_fp8_f32 v78, v77, v81 op_sel:[0,0,1]
	v_cvt_pk_fp8_f32 v67, v82, v86
	v_cvt_pk_fp8_f32 v67, v90, v94 op_sel:[0,0,1]
	v_cvt_pk_fp8_f32 v71, v83, v87
	v_cvt_pk_fp8_f32 v71, v91, v95 op_sel:[0,0,1]
	v_cvt_pk_fp8_f32 v75, v84, v88
	v_cvt_pk_fp8_f32 v75, v92, v96 op_sel:[0,0,1]
	v_cvt_pk_fp8_f32 v79, v85, v89
	v_cvt_pk_fp8_f32 v79, v93, v97 op_sel:[0,0,1]
	v_cvt_pk_fp8_f32 v68, v98, v102
	v_cvt_pk_fp8_f32 v68, v106, v110 op_sel:[0,0,1]
	v_cvt_pk_fp8_f32 v72, v99, v103
	v_cvt_pk_fp8_f32 v72, v107, v111 op_sel:[0,0,1]
	v_cvt_pk_fp8_f32 v76, v100, v104
	v_cvt_pk_fp8_f32 v76, v108, v112 op_sel:[0,0,1]
	v_cvt_pk_fp8_f32 v80, v101, v105
	v_cvt_pk_fp8_f32 v80, v109, v113 op_sel:[0,0,1]
	v_cvt_pk_fp8_f32 v69, v114, v118
	v_cvt_pk_fp8_f32 v69, v122, v126 op_sel:[0,0,1]
	v_cvt_pk_fp8_f32 v73, v115, v119
	v_cvt_pk_fp8_f32 v73, v123, v127 op_sel:[0,0,1]
	v_cvt_pk_fp8_f32 v77, v116, v120
	v_cvt_pk_fp8_f32 v77, v124, v128 op_sel:[0,0,1]
	v_cvt_pk_fp8_f32 v81, v117, v121
	v_cvt_pk_fp8_f32 v81, v125, v129 op_sel:[0,0,1]
	global_store_dwordx4 v250, v[66:69], s[42:43] nt
	global_store_dwordx4 v250, v[70:73], s[42:43] offset:2048 nt
	global_store_dwordx4 v251, v[74:77], s[42:43] nt
	global_store_dwordx4 v251, v[78:81], s[42:43] offset:2048 nt
	s_add_u32 s42, s42, 0x800000
	s_addc_u32 s43, s43, 0
	global_load_dwordx4 v[66:69], v246, s[4:5] nt
	global_load_dwordx4 v[70:73], v247, s[4:5] nt
	global_load_dwordx4 v[74:77], v248, s[4:5] nt
	global_load_dwordx4 v[78:81], v249, s[4:5] nt
	global_load_dwordx4 v[82:85], v246, s[6:7] nt
	global_load_dwordx4 v[86:89], v247, s[6:7] nt
	global_load_dwordx4 v[90:93], v248, s[6:7] nt
	global_load_dwordx4 v[94:97], v249, s[6:7] nt
	global_load_dwordx4 v[98:101], v246, s[8:9] nt
	global_load_dwordx4 v[102:105], v247, s[8:9] nt
	global_load_dwordx4 v[106:109], v248, s[8:9] nt
	global_load_dwordx4 v[110:113], v249, s[8:9] nt
	global_load_dwordx4 v[114:117], v246, s[38:39] nt
	global_load_dwordx4 v[118:121], v247, s[38:39] nt
	global_load_dwordx4 v[122:125], v248, s[38:39] nt
	global_load_dwordx4 v[126:129], v249, s[38:39] nt
	s_add_u32 s4, s4, 0x2000000
	s_addc_u32 s5, s5, 0
	s_add_u32 s6, s6, 0x2000000
	s_addc_u32 s7, s7, 0
	s_add_u32 s8, s8, 0x2000000
	s_addc_u32 s9, s9, 0
	s_add_u32 s38, s38, 0x2000000
	s_addc_u32 s39, s39, 0
	s_waitcnt vmcnt(40)
; #define GAS __attribute__((address_space(1)))
; template <bool GAIN, bool NT = false> __device__ __forceinline__ void titem8_load(const TItem& d, int lane, f32x4 (&r)[16], f32x4 (&g)[4]) {
;     const int q = lane & 7, kg = lane >> 3; const unsigned lo = (unsigned)((16 * kg) * d.N + 4 * q) * 4u;
;     const GAS char* base = (const GAS char*)d.src;
; #pragma unroll
;     for (int j = 0; j < 16; ++j) { const GAS f32x4* p = (const GAS f32x4*)(base + (size_t)j * (size_t)d.N * 4 + lo); r[j] = NT ? __builtin_nontemporal_load(p) : *p; }
; template <bool GAIN, bool NT = false> __device__ __forceinline__ void titem8_store(const TItem& d, int lane, const f32x4 (&r)[16], const f32x4 (&g)[4]) {
;     const int q = lane & 7, kg = lane >> 3; const unsigned lo = (unsigned)((4 * q) * d.ldk + 16 * kg);
;     GAS char* base = (GAS char*)d.dst;
;     f32x4 s[16];
; #pragma unroll
;     for (int j = 0; j < 16; ++j) s[j] = r[j] * ((GAIN ? g[j >> 2][j & 3] : 1.0f) * W8_SCALE);
; #pragma unroll
;     for (int i = 0; i < 4; ++i) { v4u w;
;         w.x = pk4_fp8w(s[0][i], s[1][i], s[2][i], s[3][i]); w.y = pk4_fp8w(s[4][i], s[5][i], s[6][i], s[7][i]);
;         w.z = pk4_fp8w(s[8][i], s[9][i], s[10][i], s[11][i]); w.w = pk4_fp8w(s[12][i], s[13][i], s[14][i], s[15][i]);
;         GAS v4u* p = (GAS v4u*)(base + (size_t)i * (size_t)d.ldk + lo);
;         if (NT) __builtin_nontemporal_store(w, p); else *p = w; }
	v_pk_mul_f32 v[130:131], v[130:131], s[30:31] op_sel_hi:[1,0]
	v_pk_mul_f32 v[132:133], v[132:133], s[30:31] op_sel_hi:[1,0]
	v_pk_mul_f32 v[134:135], v[134:135], s[30:31] op_sel_hi:[1,0]
	v_pk_mul_f32 v[136:137], v[136:137], s[30:31] op_sel_hi:[1,0]
	v_pk_mul_f32 v[138:139], v[138:139], s[30:31] op_sel_hi:[1,0]
	v_pk_mul_f32 v[140:141], v[140:141], s[30:31] op_sel_hi:[1,0]
	v_pk_mul_f32 v[142:143], v[142:143], s[30:31] op_sel_hi:[1,0]
	v_pk_mul_f32 v[144:145], v[144:145], s[30:31] op_sel_hi:[1,0]
	v_pk_mul_f32 v[146:147], v[146:147], s[30:31] op_sel_hi:[1,0]
	v_pk_mul_f32 v[148:149], v[148:149], s[30:31] op_sel_hi:[1,0]
	v_pk_mul_f32 v[150:151], v[150:151], s[30:31] op_sel_hi:[1,0]
	v_pk_mul_f32 v[152:153], v[152:153], s[30:31] op_sel_hi:[1,0]
	v_pk_mul_f32 v[154:155], v[154:155], s[30:31] op_sel_hi:[1,0]
	v_pk_mul_f32 v[156:157], v[156:157], s[30:31] op_sel_hi:[1,0]
	v_pk_mul_f32 v[158:159], v[158:159], s[30:31] op_sel_hi:[1,0]
	v_pk_mul_f32 v[160:161], v[160:161], s[30:31] op_sel_hi:[1,0]
	v_pk_mul_f32 v[162:163], v[162:163], s[30:31] op_sel_hi:[1,0]
	v_pk_mul_f32 v[164:165], v[164:165], s[30:31] op_sel_hi:[1,0]
	v_pk_mul_f32 v[166:167], v[166:167], s[30:31] op_sel_hi:[1,0]
	v_pk_mul_f32 v[168:169], v[168:169], s[30:31] op_sel_hi:[1,0]
	v_pk_mul_f32 v[170:171], v[170:171], s[30:31] op_sel_hi:[1,0]
	v_pk_mul_f32 v[172:173], v[172:173], s[30:31] op_sel_hi:[1,0]
	v_pk_mul_f32 v[174:175], v[174:175], s[30:31] op_sel_hi:[1,0]
	v_pk_mul_f32 v[176:177], v[176:177], s[30:31] op_sel_hi:[1,0]
	v_pk_mul_f32 v[178:179], v[178:179], s[30:31] op_sel_hi:[1,0]
	v_pk_mul_f32 v[180:181], v[180:181], s[30:31] op_sel_hi:[1,0]
	v_pk_mul_f32 v[182:183], v[182:183], s[30:31] op_sel_hi:[1,0]
	v_pk_mul_f32 v[184:185], v[184:185], s[30:31] op_sel_hi:[1,0]
	v_pk_mul_f32 v[186:187], v[186:187], s[30:31] op_sel_hi:[1,0]
	v_pk_mul_f32 v[188:189], v[188:189], s[30:31] op_sel_hi:[1,0]
	v_pk_mul_f32 v[190:191], v[190:191], s[30:31] op_sel_hi:[1,0]
	v_pk_mul_f32 v[192:193], v[192:193], s[30:31] op_sel_hi:[1,0]
	v_med3_f32 v130, v130, s24, v237
	v_med3_f32 v131, v131, s24, v237
	v_med3_f32 v132, v132, s24, v237
	v_med3_f32 v133, v133, s24, v237
	v_med3_f32 v134, v134, s24, v237
	v_med3_f32 v135, v135, s24, v237
	v_med3_f32 v136, v136, s24, v237
	v_med3_f32 v137, v137, s24, v237
	v_med3_f32 v138, v138, s24, v237
	v_med3_f32 v139, v139, s24, v237
	v_med3_f32 v140, v140, s24, v237
	v_med3_f32 v141, v141, s24, v237
	v_med3_f32 v142, v142, s24, v237
	v_med3_f32 v143, v143, s24, v237
	v_med3_f32 v144, v144, s24, v237
	v_med3_f32 v145, v145, s24, v237
	v_med3_f32 v146, v146, s24, v237
	v_med3_f32 v147, v147, s24, v237
	v_med3_f32 v148, v148, s24, v237
	v_med3_f32 v149, v149, s24, v237
	v_med3_f32 v150, v150, s24, v237
	v_med3_f32 v151, v151, s24, v237
	v_med3_f32 v152, v152, s24, v237
	v_med3_f32 v153, v153, s24, v237
	v_med3_f32 v154, v154, s24, v237
	v_med3_f32 v155, v155, s24, v237
	v_med3_f32 v156, v156, s24, v237
	v_med3_f32 v157, v157, s24, v237
	v_med3_f32 v158, v158, s24, v237
	v_med3_f32 v159, v159, s24, v237
	v_med3_f32 v160, v160, s24, v237
	v_med3_f32 v161, v161, s24, v237
	v_med3_f32 v162, v162, s24, v237
	v_med3_f32 v163, v163, s24, v237
	v_med3_f32 v164, v164, s24, v237
	v_med3_f32 v165, v165, s24, v237
	v_med3_f32 v166, v166, s24, v237
	v_med3_f32 v167, v167, s24, v237
	v_med3_f32 v168, v168, s24, v237
	v_med3_f32 v169, v169, s24, v237
	v_med3_f32 v170, v170, s24, v237
	v_med3_f32 v171, v171, s24, v237
	v_med3_f32 v172, v172, s24, v237
	v_med3_f32 v173, v173, s24, v237
	v_med3_f32 v174, v174, s24, v237
	v_med3_f32 v175, v175, s24, v237
	v_med3_f32 v176, v176, s24, v237
	v_med3_f32 v177, v177, s24, v237
	v_med3_f32 v178, v178, s24, v237
	v_med3_f32 v179, v179, s24, v237
	v_med3_f32 v180, v180, s24, v237
	v_med3_f32 v181, v181, s24, v237
	v_med3_f32 v182, v182, s24, v237
	v_med3_f32 v183, v183, s24, v237
	v_med3_f32 v184, v184, s24, v237
	v_med3_f32 v185, v185, s24, v237
	v_med3_f32 v186, v186, s24, v237
	v_med3_f32 v187, v187, s24, v237
	v_med3_f32 v188, v188, s24, v237
	v_med3_f32 v189, v189, s24, v237
	v_med3_f32 v190, v190, s24, v237
	v_med3_f32 v191, v191, s24, v237
	v_med3_f32 v192, v192, s24, v237
	v_med3_f32 v193, v193, s24, v237
	v_cvt_pk_fp8_f32 v130, v130, v134
	v_cvt_pk_fp8_f32 v130, v138, v142 op_sel:[0,0,1]
	v_cvt_pk_fp8_f32 v134, v131, v135
	v_cvt_pk_fp8_f32 v134, v139, v143 op_sel:[0,0,1]
	v_cvt_pk_fp8_f32 v138, v132, v136
	v_cvt_pk_fp8_f32 v138, v140, v144 op_sel:[0,0,1]
	v_cvt_pk_fp8_f32 v142, v133, v137
	v_cvt_pk_fp8_f32 v142, v141, v145 op_sel:[0,0,1]
	v_cvt_pk_fp8_f32 v131, v146, v150
	v_cvt_pk_fp8_f32 v131, v154, v158 op_sel:[0,0,1]
	v_cvt_pk_fp8_f32 v135, v147, v151
	v_cvt_pk_fp8_f32 v135, v155, v159 op_sel:[0,0,1]
	v_cvt_pk_fp8_f32 v139, v148, v152
	v_cvt_pk_fp8_f32 v139, v156, v160 op_sel:[0,0,1]
	v_cvt_pk_fp8_f32 v143, v149, v153
	v_cvt_pk_fp8_f32 v143, v157, v161 op_sel:[0,0,1]
	v_cvt_pk_fp8_f32 v132, v162, v166
	v_cvt_pk_fp8_f32 v132, v170, v174 op_sel:[0,0,1]
	v_cvt_pk_fp8_f32 v136, v163, v167
	v_cvt_pk_fp8_f32 v136, v171, v175 op_sel:[0,0,1]
	v_cvt_pk_fp8_f32 v140, v164, v168
	v_cvt_pk_fp8_f32 v140, v172, v176 op_sel:[0,0,1]
	v_cvt_pk_fp8_f32 v144, v165, v169
	v_cvt_pk_fp8_f32 v144, v173, v177 op_sel:[0,0,1]
	v_cvt_pk_fp8_f32 v133, v178, v182
	v_cvt_pk_fp8_f32 v133, v186, v190 op_sel:[0,0,1]
	v_cvt_pk_fp8_f32 v137, v179, v183
	v_cvt_pk_fp8_f32 v137, v187, v191 op_sel:[0,0,1]
	v_cvt_pk_fp8_f32 v141, v180, v184
	v_cvt_pk_fp8_f32 v141, v188, v192 op_sel:[0,0,1]
	v_cvt_pk_fp8_f32 v145, v181, v185
	v_cvt_pk_fp8_f32 v145, v189, v193 op_sel:[0,0,1]
	global_store_dwordx4 v250, v[130:133], s[42:43] nt
	global_store_dwordx4 v250, v[134:137], s[42:43] offset:2048 nt
	global_store_dwordx4 v251, v[138:141], s[42:43] nt
	global_store_dwordx4 v251, v[142:145], s[42:43] offset:2048 nt
	s_add_u32 s42, s42, 0x800000
	s_addc_u32 s43, s43, 0
	global_load_dwordx4 v[130:133], v246, s[4:5] nt
	global_load_dwordx4 v[134:137], v247, s[4:5] nt
	global_load_dwordx4 v[138:141], v248, s[4:5] nt
	global_load_dwordx4 v[142:145], v249, s[4:5] nt
	global_load_dwordx4 v[146:149], v246, s[6:7] nt
	global_load_dwordx4 v[150:153], v247, s[6:7] nt
	global_load_dwordx4 v[154:157], v248, s[6:7] nt
	global_load_dwordx4 v[158:161], v249, s[6:7] nt
	global_load_dwordx4 v[162:165], v246, s[8:9] nt
	global_load_dwordx4 v[166:169], v247, s[8:9] nt
	global_load_dwordx4 v[170:173], v248, s[8:9] nt
	global_load_dwordx4 v[174:177], v249, s[8:9] nt
	global_load_dwordx4 v[178:181], v246, s[38:39] nt
	global_load_dwordx4 v[182:185], v247, s[38:39] nt
	global_load_dwordx4 v[186:189], v248, s[38:39] nt
	global_load_dwordx4 v[190:193], v249, s[38:39] nt
	s_add_u32 s4, s4, 0x2000000
	s_addc_u32 s5, s5, 0
	s_add_u32 s6, s6, 0x2000000
	s_addc_u32 s7, s7, 0
	s_add_u32 s8, s8, 0x2000000
	s_addc_u32 s9, s9, 0
	s_add_u32 s38, s38, 0x2000000
	s_addc_u32 s39, s39, 0
	s_waitcnt vmcnt(40)
; #define GAS __attribute__((address_space(1)))
; template <bool GAIN, bool NT = false> __device__ __forceinline__ void titem8_load(const TItem& d, int lane, f32x4 (&r)[16], f32x4 (&g)[4]) {
;     const int q = lane & 7, kg = lane >> 3; const unsigned lo = (unsigned)((16 * kg) * d.N + 4 * q) * 4u;
;     const GAS char* base = (const GAS char*)d.src;
; #pragma unroll
;     for (int j = 0; j < 16; ++j) { const GAS f32x4* p = (const GAS f32x4*)(base + (size_t)j * (size_t)d.N * 4 + lo); r[j] = NT ? __builtin_nontemporal_load(p) : *p; }
; template <bool GAIN, bool NT = false> __device__ __forceinline__ void titem8_store(const TItem& d, int lane, const f32x4 (&r)[16], const f32x4 (&g)[4]) {
;     const int q = lane & 7, kg = lane >> 3; const unsigned lo = (unsigned)((4 * q) * d.ldk + 16 * kg);
;     GAS char* base = (GAS char*)d.dst;
;     f32x4 s[16];
; #pragma unroll
;     for (int j = 0; j < 16; ++j) s[j] = r[j] * ((GAIN ? g[j >> 2][j & 3] : 1.0f) * W8_SCALE);
; #pragma unroll
;     for (int i = 0; i < 4; ++i) { v4u w;
;         w.x = pk4_fp8w(s[0][i], s[1][i], s[2][i], s[3][i]); w.y = pk4_fp8w(s[4][i], s[5][i], s[6][i], s[7][i]);
;         w.z = pk4_fp8w(s[8][i], s[9][i], s[10][i], s[11][i]); w.w = pk4_fp8w(s[12][i], s[13][i], s[14][i], s[15][i]);
;         GAS v4u* p = (GAS v4u*)(base + (size_t)i * (size_t)d.ldk + lo);
;         if (NT) __builtin_nontemporal_store(w, p); else *p = w; }
	v_pk_mul_f32 v[0:1], v[0:1], s[30:31] op_sel_hi:[1,0]
	v_pk_mul_f32 v[2:3], v[2:3], s[30:31] op_sel_hi:[1,0]
	v_pk_mul_f32 v[4:5], v[4:5], s[30:31] op_sel_hi:[1,0]
	v_pk_mul_f32 v[6:7], v[6:7], s[30:31] op_sel_hi:[1,0]
	v_pk_mul_f32 v[8:9], v[8:9], s[30:31] op_sel_hi:[1,0]
	v_pk_mul_f32 v[10:11], v[10:11], s[30:31] op_sel_hi:[1,0]
	v_pk_mul_f32 v[12:13], v[12:13], s[30:31] op_sel_hi:[1,0]
	v_pk_mul_f32 v[14:15], v[14:15], s[30:31] op_sel_hi:[1,0]
	v_pk_mul_f32 v[16:17], v[16:17], s[30:31] op_sel_hi:[1,0]
	v_pk_mul_f32 v[18:19], v[18:19], s[30:31] op_sel_hi:[1,0]
	v_pk_mul_f32 v[20:21], v[20:21], s[30:31] op_sel_hi:[1,0]
	v_pk_mul_f32 v[22:23], v[22:23], s[30:31] op_sel_hi:[1,0]
	v_pk_mul_f32 v[24:25], v[24:25], s[30:31] op_sel_hi:[1,0]
	v_pk_mul_f32 v[26:27], v[26:27], s[30:31] op_sel_hi:[1,0]
	v_pk_mul_f32 v[28:29], v[28:29], s[30:31] op_sel_hi:[1,0]
	v_pk_mul_f32 v[30:31], v[30:31], s[30:31] op_sel_hi:[1,0]
	v_pk_mul_f32 v[32:33], v[32:33], s[30:31] op_sel_hi:[1,0]
	v_pk_mul_f32 v[34:35], v[34:35], s[30:31] op_sel_hi:[1,0]
	v_pk_mul_f32 v[36:37], v[36:37], s[30:31] op_sel_hi:[1,0]
	v_pk_mul_f32 v[38:39], v[38:39], s[30:31] op_sel_hi:[1,0]
	v_pk_mul_f32 v[40:41], v[40:41], s[30:31] op_sel_hi:[1,0]
	v_pk_mul_f32 v[42:43], v[42:43], s[30:31] op_sel_hi:[1,0]
	v_pk_mul_f32 v[44:45], v[44:45], s[30:31] op_sel_hi:[1,0]
	v_pk_mul_f32 v[46:47], v[46:47], s[30:31] op_sel_hi:[1,0]
	v_pk_mul_f32 v[48:49], v[48:49], s[30:31] op_sel_hi:[1,0]
	v_pk_mul_f32 v[50:51], v[50:51], s[30:31] op_sel_hi:[1,0]
	v_pk_mul_f32 v[52:53], v[52:53], s[30:31] op_sel_hi:[1,0]
	v_pk_mul_f32 v[54:55], v[54:55], s[30:31] op_sel_hi:[1,0]
	v_pk_mul_f32 v[56:57], v[56:57], s[30:31] op_sel_hi:[1,0]
	v_pk_mul_f32 v[58:59], v[58:59], s[30:31] op_sel_hi:[1,0]
	v_pk_mul_f32 v[60:61], v[60:61], s[30:31] op_sel_hi:[1,0]
	v_pk_mul_f32 v[62:63], v[62:63], s[30:31] op_sel_hi:[1,0]
	v_med3_f32 v0, v0, s24, v237
	v_med3_f32 v1, v1, s24, v237
	v_med3_f32 v2, v2, s24, v237
	v_med3_f32 v3, v3, s24, v237
	v_med3_f32 v4, v4, s24, v237
	v_med3_f32 v5, v5, s24, v237
	v_med3_f32 v6, v6, s24, v237
	v_med3_f32 v7, v7, s24, v237
	v_med3_f32 v8, v8, s24, v237
	v_med3_f32 v9, v9, s24, v237
	v_med3_f32 v10, v10, s24, v237
	v_med3_f32 v11, v11, s24, v237
	v_med3_f32 v12, v12, s24, v237
	v_med3_f32 v13, v13, s24, v237
	v_med3_f32 v14, v14, s24, v237
	v_med3_f32 v15, v15, s24, v237
	v_med3_f32 v16, v16, s24, v237
	v_med3_f32 v17, v17, s24, v237
	v_med3_f32 v18, v18, s24, v237
	v_med3_f32 v19, v19, s24, v237
	v_med3_f32 v20, v20, s24, v237
	v_med3_f32 v21, v21, s24, v237
	v_med3_f32 v22, v22, s24, v237
	v_med3_f32 v23, v23, s24, v237
	v_med3_f32 v24, v24, s24, v237
	v_med3_f32 v25, v25, s24, v237
	v_med3_f32 v26, v26, s24, v237
	v_med3_f32 v27, v27, s24, v237
	v_med3_f32 v28, v28, s24, v237
	v_med3_f32 v29, v29, s24, v237
	v_med3_f32 v30, v30, s24, v237
	v_med3_f32 v31, v31, s24, v237
	v_med3_f32 v32, v32, s24, v237
	v_med3_f32 v33, v33, s24, v237
	v_med3_f32 v34, v34, s24, v237
	v_med3_f32 v35, v35, s24, v237
	v_med3_f32 v36, v36, s24, v237
	v_med3_f32 v37, v37, s24, v237
	v_med3_f32 v38, v38, s24, v237
	v_med3_f32 v39, v39, s24, v237
	v_med3_f32 v40, v40, s24, v237
	v_med3_f32 v41, v41, s24, v237
	v_med3_f32 v42, v42, s24, v237
	v_med3_f32 v43, v43, s24, v237
	v_med3_f32 v44, v44, s24, v237
	v_med3_f32 v45, v45, s24, v237
	v_med3_f32 v46, v46, s24, v237
	v_med3_f32 v47, v47, s24, v237
	v_med3_f32 v48, v48, s24, v237
	v_med3_f32 v49, v49, s24, v237
	v_med3_f32 v50, v50, s24, v237
	v_med3_f32 v51, v51, s24, v237
	v_med3_f32 v52, v52, s24, v237
	v_med3_f32 v53, v53, s24, v237
	v_med3_f32 v54, v54, s24, v237
	v_med3_f32 v55, v55, s24, v237
	v_med3_f32 v56, v56, s24, v237
	v_med3_f32 v57, v57, s24, v237
	v_med3_f32 v58, v58, s24, v237
	v_med3_f32 v59, v59, s24, v237
	v_med3_f32 v60, v60, s24, v237
	v_med3_f32 v61, v61, s24, v237
	v_med3_f32 v62, v62, s24, v237
	v_med3_f32 v63, v63, s24, v237
	v_cvt_pk_fp8_f32 v0, v0, v4
	v_cvt_pk_fp8_f32 v0, v8, v12 op_sel:[0,0,1]
	v_cvt_pk_fp8_f32 v4, v1, v5
	v_cvt_pk_fp8_f32 v4, v9, v13 op_sel:[0,0,1]
	v_cvt_pk_fp8_f32 v8, v2, v6
	v_cvt_pk_fp8_f32 v8, v10, v14 op_sel:[0,0,1]
	v_cvt_pk_fp8_f32 v12, v3, v7
	v_cvt_pk_fp8_f32 v12, v11, v15 op_sel:[0,0,1]
	v_cvt_pk_fp8_f32 v1, v16, v20
	v_cvt_pk_fp8_f32 v1, v24, v28 op_sel:[0,0,1]
	v_cvt_pk_fp8_f32 v5, v17, v21
	v_cvt_pk_fp8_f32 v5, v25, v29 op_sel:[0,0,1]
	v_cvt_pk_fp8_f32 v9, v18, v22
	v_cvt_pk_fp8_f32 v9, v26, v30 op_sel:[0,0,1]
	v_cvt_pk_fp8_f32 v13, v19, v23
	v_cvt_pk_fp8_f32 v13, v27, v31 op_sel:[0,0,1]
	v_cvt_pk_fp8_f32 v2, v32, v36
	v_cvt_pk_fp8_f32 v2, v40, v44 op_sel:[0,0,1]
	v_cvt_pk_fp8_f32 v6, v33, v37
	v_cvt_pk_fp8_f32 v6, v41, v45 op_sel:[0,0,1]
	v_cvt_pk_fp8_f32 v10, v34, v38
	v_cvt_pk_fp8_f32 v10, v42, v46 op_sel:[0,0,1]
	v_cvt_pk_fp8_f32 v14, v35, v39
	v_cvt_pk_fp8_f32 v14, v43, v47 op_sel:[0,0,1]
	v_cvt_pk_fp8_f32 v3, v48, v52
	v_cvt_pk_fp8_f32 v3, v56, v60 op_sel:[0,0,1]
	v_cvt_pk_fp8_f32 v7, v49, v53
	v_cvt_pk_fp8_f32 v7, v57, v61 op_sel:[0,0,1]
	v_cvt_pk_fp8_f32 v11, v50, v54
	v_cvt_pk_fp8_f32 v11, v58, v62 op_sel:[0,0,1]
	v_cvt_pk_fp8_f32 v15, v51, v55
	v_cvt_pk_fp8_f32 v15, v59, v63 op_sel:[0,0,1]
	global_store_dwordx4 v250, v[0:3], s[42:43] nt
	global_store_dwordx4 v250, v[4:7], s[42:43] offset:2048 nt
	global_store_dwordx4 v251, v[8:11], s[42:43] nt
	global_store_dwordx4 v251, v[12:15], s[42:43] offset:2048 nt
	s_add_u32 s42, s42, 0x800000
	s_addc_u32 s43, s43, 0
	global_load_dwordx4 v[0:3], v246, s[4:5] nt
	global_load_dwordx4 v[4:7], v247, s[4:5] nt
	global_load_dwordx4 v[8:11], v248, s[4:5] nt
	global_load_dwordx4 v[12:15], v249, s[4:5] nt
	global_load_dwordx4 v[16:19], v246, s[6:7] nt
	global_load_dwordx4 v[20:23], v247, s[6:7] nt
	global_load_dwordx4 v[24:27], v248, s[6:7] nt
	global_load_dwordx4 v[28:31], v249, s[6:7] nt
	global_load_dwordx4 v[32:35], v246, s[8:9] nt
	global_load_dwordx4 v[36:39], v247, s[8:9] nt
	global_load_dwordx4 v[40:43], v248, s[8:9] nt
	global_load_dwordx4 v[44:47], v249, s[8:9] nt
	global_load_dwordx4 v[48:51], v246, s[38:39] nt
	global_load_dwordx4 v[52:55], v247, s[38:39] nt
	global_load_dwordx4 v[56:59], v248, s[38:39] nt
	global_load_dwordx4 v[60:63], v249, s[38:39] nt
	s_add_u32 s4, s4, 0x2000000
	s_addc_u32 s5, s5, 0
	s_add_u32 s6, s6, 0x2000000
	s_addc_u32 s7, s7, 0
	s_add_u32 s8, s8, 0x2000000
	s_addc_u32 s9, s9, 0
	s_add_u32 s38, s38, 0x2000000
	s_addc_u32 s39, s39, 0
	s_waitcnt vmcnt(40)
; #define GAS __attribute__((address_space(1)))
; template <bool GAIN, bool NT = false> __device__ __forceinline__ void titem8_load(const TItem& d, int lane, f32x4 (&r)[16], f32x4 (&g)[4]) {
;     const int q = lane & 7, kg = lane >> 3; const unsigned lo = (unsigned)((16 * kg) * d.N + 4 * q) * 4u;
;     const GAS char* base = (const GAS char*)d.src;
; #pragma unroll
;     for (int j = 0; j < 16; ++j) { const GAS f32x4* p = (const GAS f32x4*)(base + (size_t)j * (size_t)d.N * 4 + lo); r[j] = NT ? __builtin_nontemporal_load(p) : *p; }
; template <bool GAIN, bool NT = false> __device__ __forceinline__ void titem8_store(const TItem& d, int lane, const f32x4 (&r)[16], const f32x4 (&g)[4]) {
;     const int q = lane & 7, kg = lane >> 3; const unsigned lo = (unsigned)((4 * q) * d.ldk + 16 * kg);
;     GAS char* base = (GAS char*)d.dst;
;     f32x4 s[16];
; #pragma unroll
;     for (int j = 0; j < 16; ++j) s[j] = r[j] * ((GAIN ? g[j >> 2][j & 3] : 1.0f) * W8_SCALE);
; #pragma unroll
;     for (int i = 0; i < 4; ++i) { v4u w;
;         w.x = pk4_fp8w(s[0][i], s[1][i], s[2][i], s[3][i]); w.y = pk4_fp8w(s[4][i], s[5][i], s[6][i], s[7][i]);
;         w.z = pk4_fp8w(s[8][i], s[9][i], s[10][i], s[11][i]); w.w = pk4_fp8w(s[12][i], s[13][i], s[14][i], s[15][i]);
;         GAS v4u* p = (GAS v4u*)(base + (size_t)i * (size_t)d.ldk + lo);
;         if (NT) __builtin_nontemporal_store(w, p); else *p = w; }
	v_pk_mul_f32 v[66:67], v[66:67], s[30:31] op_sel_hi:[1,0]
	v_pk_mul_f32 v[68:69], v[68:69], s[30:31] op_sel_hi:[1,0]
	v_pk_mul_f32 v[70:71], v[70:71], s[30:31] op_sel_hi:[1,0]
	v_pk_mul_f32 v[72:73], v[72:73], s[30:31] op_sel_hi:[1,0]
	v_pk_mul_f32 v[74:75], v[74:75], s[30:31] op_sel_hi:[1,0]
	v_pk_mul_f32 v[76:77], v[76:77], s[30:31] op_sel_hi:[1,0]
	v_pk_mul_f32 v[78:79], v[78:79], s[30:31] op_sel_hi:[1,0]
	v_pk_mul_f32 v[80:81], v[80:81], s[30:31] op_sel_hi:[1,0]
	v_pk_mul_f32 v[82:83], v[82:83], s[30:31] op_sel_hi:[1,0]
	v_pk_mul_f32 v[84:85], v[84:85], s[30:31] op_sel_hi:[1,0]
	v_pk_mul_f32 v[86:87], v[86:87], s[30:31] op_sel_hi:[1,0]
	v_pk_mul_f32 v[88:89], v[88:89], s[30:31] op_sel_hi:[1,0]
	v_pk_mul_f32 v[90:91], v[90:91], s[30:31] op_sel_hi:[1,0]
	v_pk_mul_f32 v[92:93], v[92:93], s[30:31] op_sel_hi:[1,0]
	v_pk_mul_f32 v[94:95], v[94:95], s[30:31] op_sel_hi:[1,0]
	v_pk_mul_f32 v[96:97], v[96:97], s[30:31] op_sel_hi:[1,0]
	v_pk_mul_f32 v[98:99], v[98:99], s[30:31] op_sel_hi:[1,0]
	v_pk_mul_f32 v[100:101], v[100:101], s[30:31] op_sel_hi:[1,0]
	v_pk_mul_f32 v[102:103], v[102:103], s[30:31] op_sel_hi:[1,0]
	v_pk_mul_f32 v[104:105], v[104:105], s[30:31] op_sel_hi:[1,0]
	v_pk_mul_f32 v[106:107], v[106:107], s[30:31] op_sel_hi:[1,0]
	v_pk_mul_f32 v[108:109], v[108:109], s[30:31] op_sel_hi:[1,0]
	v_pk_mul_f32 v[110:111], v[110:111], s[30:31] op_sel_hi:[1,0]
	v_pk_mul_f32 v[112:113], v[112:113], s[30:31] op_sel_hi:[1,0]
	v_pk_mul_f32 v[114:115], v[114:115], s[30:31] op_sel_hi:[1,0]
	v_pk_mul_f32 v[116:117], v[116:117], s[30:31] op_sel_hi:[1,0]
	v_pk_mul_f32 v[118:119], v[118:119], s[30:31] op_sel_hi:[1,0]
	v_pk_mul_f32 v[120:121], v[120:121], s[30:31] op_sel_hi:[1,0]
	v_pk_mul_f32 v[122:123], v[122:123], s[30:31] op_sel_hi:[1,0]
	v_pk_mul_f32 v[124:125], v[124:125], s[30:31] op_sel_hi:[1,0]
	v_pk_mul_f32 v[126:127], v[126:127], s[30:31] op_sel_hi:[1,0]
	v_pk_mul_f32 v[128:129], v[128:129], s[30:31] op_sel_hi:[1,0]
	v_med3_f32 v66, v66, s24, v237
	v_med3_f32 v67, v67, s24, v237
	v_med3_f32 v68, v68, s24, v237
	v_med3_f32 v69, v69, s24, v237
	v_med3_f32 v70, v70, s24, v237
	v_med3_f32 v71, v71, s24, v237
	v_med3_f32 v72, v72, s24, v237
	v_med3_f32 v73, v73, s24, v237
	v_med3_f32 v74, v74, s24, v237
	v_med3_f32 v75, v75, s24, v237
	v_med3_f32 v76, v76, s24, v237
	v_med3_f32 v77, v77, s24, v237
	v_med3_f32 v78, v78, s24, v237
	v_med3_f32 v79, v79, s24, v237
	v_med3_f32 v80, v80, s24, v237
	v_med3_f32 v81, v81, s24, v237
	v_med3_f32 v82, v82, s24, v237
	v_med3_f32 v83, v83, s24, v237
	v_med3_f32 v84, v84, s24, v237
	v_med3_f32 v85, v85, s24, v237
	v_med3_f32 v86, v86, s24, v237
	v_med3_f32 v87, v87, s24, v237
	v_med3_f32 v88, v88, s24, v237
	v_med3_f32 v89, v89, s24, v237
	v_med3_f32 v90, v90, s24, v237
	v_med3_f32 v91, v91, s24, v237
	v_med3_f32 v92, v92, s24, v237
	v_med3_f32 v93, v93, s24, v237
	v_med3_f32 v94, v94, s24, v237
	v_med3_f32 v95, v95, s24, v237
	v_med3_f32 v96, v96, s24, v237
	v_med3_f32 v97, v97, s24, v237
	v_med3_f32 v98, v98, s24, v237
	v_med3_f32 v99, v99, s24, v237
	v_med3_f32 v100, v100, s24, v237
	v_med3_f32 v101, v101, s24, v237
	v_med3_f32 v102, v102, s24, v237
	v_med3_f32 v103, v103, s24, v237
	v_med3_f32 v104, v104, s24, v237
	v_med3_f32 v105, v105, s24, v237
	v_med3_f32 v106, v106, s24, v237
	v_med3_f32 v107, v107, s24, v237
	v_med3_f32 v108, v108, s24, v237
	v_med3_f32 v109, v109, s24, v237
	v_med3_f32 v110, v110, s24, v237
	v_med3_f32 v111, v111, s24, v237
	v_med3_f32 v112, v112, s24, v237
	v_med3_f32 v113, v113, s24, v237
	v_med3_f32 v114, v114, s24, v237
	v_med3_f32 v115, v115, s24, v237
	v_med3_f32 v116, v116, s24, v237
	v_med3_f32 v117, v117, s24, v237
	v_med3_f32 v118, v118, s24, v237
	v_med3_f32 v119, v119, s24, v237
	v_med3_f32 v120, v120, s24, v237
	v_med3_f32 v121, v121, s24, v237
	v_med3_f32 v122, v122, s24, v237
	v_med3_f32 v123, v123, s24, v237
	v_med3_f32 v124, v124, s24, v237
	v_med3_f32 v125, v125, s24, v237
	v_med3_f32 v126, v126, s24, v237
	v_med3_f32 v127, v127, s24, v237
	v_med3_f32 v128, v128, s24, v237
	v_med3_f32 v129, v129, s24, v237
	v_cvt_pk_fp8_f32 v66, v66, v70
	v_cvt_pk_fp8_f32 v66, v74, v78 op_sel:[0,0,1]
	v_cvt_pk_fp8_f32 v70, v67, v71
	v_cvt_pk_fp8_f32 v70, v75, v79 op_sel:[0,0,1]
	v_cvt_pk_fp8_f32 v74, v68, v72
	v_cvt_pk_fp8_f32 v74, v76, v80 op_sel:[0,0,1]
	v_cvt_pk_fp8_f32 v78, v69, v73
	v_cvt_pk_fp8_f32 v78, v77, v81 op_sel:[0,0,1]
	v_cvt_pk_fp8_f32 v67, v82, v86
	v_cvt_pk_fp8_f32 v67, v90, v94 op_sel:[0,0,1]
	v_cvt_pk_fp8_f32 v71, v83, v87
	v_cvt_pk_fp8_f32 v71, v91, v95 op_sel:[0,0,1]
	v_cvt_pk_fp8_f32 v75, v84, v88
	v_cvt_pk_fp8_f32 v75, v92, v96 op_sel:[0,0,1]
	v_cvt_pk_fp8_f32 v79, v85, v89
	v_cvt_pk_fp8_f32 v79, v93, v97 op_sel:[0,0,1]
	v_cvt_pk_fp8_f32 v68, v98, v102
	v_cvt_pk_fp8_f32 v68, v106, v110 op_sel:[0,0,1]
	v_cvt_pk_fp8_f32 v72, v99, v103
	v_cvt_pk_fp8_f32 v72, v107, v111 op_sel:[0,0,1]
	v_cvt_pk_fp8_f32 v76, v100, v104
	v_cvt_pk_fp8_f32 v76, v108, v112 op_sel:[0,0,1]
	v_cvt_pk_fp8_f32 v80, v101, v105
	v_cvt_pk_fp8_f32 v80, v109, v113 op_sel:[0,0,1]
	v_cvt_pk_fp8_f32 v69, v114, v118
	v_cvt_pk_fp8_f32 v69, v122, v126 op_sel:[0,0,1]
	v_cvt_pk_fp8_f32 v73, v115, v119
	v_cvt_pk_fp8_f32 v73, v123, v127 op_sel:[0,0,1]
	v_cvt_pk_fp8_f32 v77, v116, v120
	v_cvt_pk_fp8_f32 v77, v124, v128 op_sel:[0,0,1]
	v_cvt_pk_fp8_f32 v81, v117, v121
	v_cvt_pk_fp8_f32 v81, v125, v129 op_sel:[0,0,1]
	global_store_dwordx4 v250, v[66:69], s[42:43] nt
	global_store_dwordx4 v250, v[70:73], s[42:43] offset:2048 nt
	global_store_dwordx4 v251, v[74:77], s[42:43] nt
	global_store_dwordx4 v251, v[78:81], s[42:43] offset:2048 nt
	s_add_u32 s42, s42, 0x800000
	s_addc_u32 s43, s43, 0
	global_load_dwordx4 v[66:69], v246, s[4:5] nt
	global_load_dwordx4 v[70:73], v247, s[4:5] nt
	global_load_dwordx4 v[74:77], v248, s[4:5] nt
	global_load_dwordx4 v[78:81], v249, s[4:5] nt
	global_load_dwordx4 v[82:85], v246, s[6:7] nt
	global_load_dwordx4 v[86:89], v247, s[6:7] nt
	global_load_dwordx4 v[90:93], v248, s[6:7] nt
	global_load_dwordx4 v[94:97], v249, s[6:7] nt
	global_load_dwordx4 v[98:101], v246, s[8:9] nt
	global_load_dwordx4 v[102:105], v247, s[8:9] nt
	global_load_dwordx4 v[106:109], v248, s[8:9] nt
	global_load_dwordx4 v[110:113], v249, s[8:9] nt
	global_load_dwordx4 v[114:117], v246, s[38:39] nt
	global_load_dwordx4 v[118:121], v247, s[38:39] nt
	global_load_dwordx4 v[122:125], v248, s[38:39] nt
	global_load_dwordx4 v[126:129], v249, s[38:39] nt
	s_add_u32 s4, s4, 0x2000000
	s_addc_u32 s5, s5, 0
	s_add_u32 s6, s6, 0x2000000
	s_addc_u32 s7, s7, 0
	s_add_u32 s8, s8, 0x2000000
	s_addc_u32 s9, s9, 0
	s_add_u32 s38, s38, 0x2000000
	s_addc_u32 s39, s39, 0
	s_waitcnt vmcnt(40)
; #define GAS __attribute__((address_space(1)))
; template <bool GAIN, bool NT = false> __device__ __forceinline__ void titem8_load(const TItem& d, int lane, f32x4 (&r)[16], f32x4 (&g)[4]) {
;     const int q = lane & 7, kg = lane >> 3; const unsigned lo = (unsigned)((16 * kg) * d.N + 4 * q) * 4u;
;     const GAS char* base = (const GAS char*)d.src;
; #pragma unroll
;     for (int j = 0; j < 16; ++j) { const GAS f32x4* p = (const GAS f32x4*)(base + (size_t)j * (size_t)d.N * 4 + lo); r[j] = NT ? __builtin_nontemporal_load(p) : *p; }
; template <bool GAIN, bool NT = false> __device__ __forceinline__ void titem8_store(const TItem& d, int lane, const f32x4 (&r)[16], const f32x4 (&g)[4]) {
;     const int q = lane & 7, kg = lane >> 3; const unsigned lo = (unsigned)((4 * q) * d.ldk + 16 * kg);
;     GAS char* base = (GAS char*)d.dst;
;     f32x4 s[16];
; #pragma unroll
;     for (int j = 0; j < 16; ++j) s[j] = r[j] * ((GAIN ? g[j >> 2][j & 3] : 1.0f) * W8_SCALE);
; #pragma unroll
;     for (int i = 0; i < 4; ++i) { v4u w;
;         w.x = pk4_fp8w(s[0][i], s[1][i], s[2][i], s[3][i]); w.y = pk4_fp8w(s[4][i], s[5][i], s[6][i], s[7][i]);
;         w.z = pk4_fp8w(s[8][i], s[9][i], s[10][i], s[11][i]); w.w = pk4_fp8w(s[12][i], s[13][i], s[14][i], s[15][i]);
;         GAS v4u* p = (GAS v4u*)(base + (size_t)i * (size_t)d.ldk + lo);
;         if (NT) __builtin_nontemporal_store(w, p); else *p = w; }
	v_pk_mul_f32 v[130:131], v[130:131], s[30:31] op_sel_hi:[1,0]
	v_pk_mul_f32 v[132:133], v[132:133], s[30:31] op_sel_hi:[1,0]
	v_pk_mul_f32 v[134:135], v[134:135], s[30:31] op_sel_hi:[1,0]
	v_pk_mul_f32 v[136:137], v[136:137], s[30:31] op_sel_hi:[1,0]
	v_pk_mul_f32 v[138:139], v[138:139], s[30:31] op_sel_hi:[1,0]
	v_pk_mul_f32 v[140:141], v[140:141], s[30:31] op_sel_hi:[1,0]
	v_pk_mul_f32 v[142:143], v[142:143], s[30:31] op_sel_hi:[1,0]
	v_pk_mul_f32 v[144:145], v[144:145], s[30:31] op_sel_hi:[1,0]
	v_pk_mul_f32 v[146:147], v[146:147], s[30:31] op_sel_hi:[1,0]
	v_pk_mul_f32 v[148:149], v[148:149], s[30:31] op_sel_hi:[1,0]
	v_pk_mul_f32 v[150:151], v[150:151], s[30:31] op_sel_hi:[1,0]
	v_pk_mul_f32 v[152:153], v[152:153], s[30:31] op_sel_hi:[1,0]
	v_pk_mul_f32 v[154:155], v[154:155], s[30:31] op_sel_hi:[1,0]
	v_pk_mul_f32 v[156:157], v[156:157], s[30:31] op_sel_hi:[1,0]
	v_pk_mul_f32 v[158:159], v[158:159], s[30:31] op_sel_hi:[1,0]
	v_pk_mul_f32 v[160:161], v[160:161], s[30:31] op_sel_hi:[1,0]
	v_pk_mul_f32 v[162:163], v[162:163], s[30:31] op_sel_hi:[1,0]
	v_pk_mul_f32 v[164:165], v[164:165], s[30:31] op_sel_hi:[1,0]
	v_pk_mul_f32 v[166:167], v[166:167], s[30:31] op_sel_hi:[1,0]
	v_pk_mul_f32 v[168:169], v[168:169], s[30:31] op_sel_hi:[1,0]
	v_pk_mul_f32 v[170:171], v[170:171], s[30:31] op_sel_hi:[1,0]
	v_pk_mul_f32 v[172:173], v[172:173], s[30:31] op_sel_hi:[1,0]
	v_pk_mul_f32 v[174:175], v[174:175], s[30:31] op_sel_hi:[1,0]
	v_pk_mul_f32 v[176:177], v[176:177], s[30:31] op_sel_hi:[1,0]
	v_pk_mul_f32 v[178:179], v[178:179], s[30:31] op_sel_hi:[1,0]
	v_pk_mul_f32 v[180:181], v[180:181], s[30:31] op_sel_hi:[1,0]
	v_pk_mul_f32 v[182:183], v[182:183], s[30:31] op_sel_hi:[1,0]
	v_pk_mul_f32 v[184:185], v[184:185], s[30:31] op_sel_hi:[1,0]
	v_pk_mul_f32 v[186:187], v[186:187], s[30:31] op_sel_hi:[1,0]
	v_pk_mul_f32 v[188:189], v[188:189], s[30:31] op_sel_hi:[1,0]
	v_pk_mul_f32 v[190:191], v[190:191], s[30:31] op_sel_hi:[1,0]
	v_pk_mul_f32 v[192:193], v[192:193], s[30:31] op_sel_hi:[1,0]
	v_med3_f32 v130, v130, s24, v237
	v_med3_f32 v131, v131, s24, v237
	v_med3_f32 v132, v132, s24, v237
	v_med3_f32 v133, v133, s24, v237
	v_med3_f32 v134, v134, s24, v237
	v_med3_f32 v135, v135, s24, v237
	v_med3_f32 v136, v136, s24, v237
	v_med3_f32 v137, v137, s24, v237
	v_med3_f32 v138, v138, s24, v237
	v_med3_f32 v139, v139, s24, v237
	v_med3_f32 v140, v140, s24, v237
	v_med3_f32 v141, v141, s24, v237
	v_med3_f32 v142, v142, s24, v237
	v_med3_f32 v143, v143, s24, v237
	v_med3_f32 v144, v144, s24, v237
	v_med3_f32 v145, v145, s24, v237
	v_med3_f32 v146, v146, s24, v237
	v_med3_f32 v147, v147, s24, v237
	v_med3_f32 v148, v148, s24, v237
	v_med3_f32 v149, v149, s24, v237
	v_med3_f32 v150, v150, s24, v237
	v_med3_f32 v151, v151, s24, v237
	v_med3_f32 v152, v152, s24, v237
	v_med3_f32 v153, v153, s24, v237
	v_med3_f32 v154, v154, s24, v237
	v_med3_f32 v155, v155, s24, v237
	v_med3_f32 v156, v156, s24, v237
	v_med3_f32 v157, v157, s24, v237
	v_med3_f32 v158, v158, s24, v237
	v_med3_f32 v159, v159, s24, v237
	v_med3_f32 v160, v160, s24, v237
	v_med3_f32 v161, v161, s24, v237
	v_med3_f32 v162, v162, s24, v237
	v_med3_f32 v163, v163, s24, v237
	v_med3_f32 v164, v164, s24, v237
	v_med3_f32 v165, v165, s24, v237
	v_med3_f32 v166, v166, s24, v237
	v_med3_f32 v167, v167, s24, v237
	v_med3_f32 v168, v168, s24, v237
	v_med3_f32 v169, v169, s24, v237
	v_med3_f32 v170, v170, s24, v237
	v_med3_f32 v171, v171, s24, v237
	v_med3_f32 v172, v172, s24, v237
	v_med3_f32 v173, v173, s24, v237
	v_med3_f32 v174, v174, s24, v237
	v_med3_f32 v175, v175, s24, v237
	v_med3_f32 v176, v176, s24, v237
	v_med3_f32 v177, v177, s24, v237
	v_med3_f32 v178, v178, s24, v237
	v_med3_f32 v179, v179, s24, v237
	v_med3_f32 v180, v180, s24, v237
	v_med3_f32 v181, v181, s24, v237
	v_med3_f32 v182, v182, s24, v237
	v_med3_f32 v183, v183, s24, v237
	v_med3_f32 v184, v184, s24, v237
	v_med3_f32 v185, v185, s24, v237
	v_med3_f32 v186, v186, s24, v237
	v_med3_f32 v187, v187, s24, v237
	v_med3_f32 v188, v188, s24, v237
	v_med3_f32 v189, v189, s24, v237
	v_med3_f32 v190, v190, s24, v237
	v_med3_f32 v191, v191, s24, v237
	v_med3_f32 v192, v192, s24, v237
	v_med3_f32 v193, v193, s24, v237
	v_cvt_pk_fp8_f32 v130, v130, v134
	v_cvt_pk_fp8_f32 v130, v138, v142 op_sel:[0,0,1]
	v_cvt_pk_fp8_f32 v134, v131, v135
	v_cvt_pk_fp8_f32 v134, v139, v143 op_sel:[0,0,1]
	v_cvt_pk_fp8_f32 v138, v132, v136
	v_cvt_pk_fp8_f32 v138, v140, v144 op_sel:[0,0,1]
	v_cvt_pk_fp8_f32 v142, v133, v137
	v_cvt_pk_fp8_f32 v142, v141, v145 op_sel:[0,0,1]
	v_cvt_pk_fp8_f32 v131, v146, v150
	v_cvt_pk_fp8_f32 v131, v154, v158 op_sel:[0,0,1]
	v_cvt_pk_fp8_f32 v135, v147, v151
	v_cvt_pk_fp8_f32 v135, v155, v159 op_sel:[0,0,1]
	v_cvt_pk_fp8_f32 v139, v148, v152
	v_cvt_pk_fp8_f32 v139, v156, v160 op_sel:[0,0,1]
	v_cvt_pk_fp8_f32 v143, v149, v153
	v_cvt_pk_fp8_f32 v143, v157, v161 op_sel:[0,0,1]
	v_cvt_pk_fp8_f32 v132, v162, v166
	v_cvt_pk_fp8_f32 v132, v170, v174 op_sel:[0,0,1]
	v_cvt_pk_fp8_f32 v136, v163, v167
	v_cvt_pk_fp8_f32 v136, v171, v175 op_sel:[0,0,1]
	v_cvt_pk_fp8_f32 v140, v164, v168
	v_cvt_pk_fp8_f32 v140, v172, v176 op_sel:[0,0,1]
	v_cvt_pk_fp8_f32 v144, v165, v169
	v_cvt_pk_fp8_f32 v144, v173, v177 op_sel:[0,0,1]
	v_cvt_pk_fp8_f32 v133, v178, v182
	v_cvt_pk_fp8_f32 v133, v186, v190 op_sel:[0,0,1]
	v_cvt_pk_fp8_f32 v137, v179, v183
	v_cvt_pk_fp8_f32 v137, v187, v191 op_sel:[0,0,1]
	v_cvt_pk_fp8_f32 v141, v180, v184
	v_cvt_pk_fp8_f32 v141, v188, v192 op_sel:[0,0,1]
	v_cvt_pk_fp8_f32 v145, v181, v185
	v_cvt_pk_fp8_f32 v145, v189, v193 op_sel:[0,0,1]
	global_store_dwordx4 v250, v[130:133], s[42:43] nt
	global_store_dwordx4 v250, v[134:137], s[42:43] offset:2048 nt
	global_store_dwordx4 v251, v[138:141], s[42:43] nt
	global_store_dwordx4 v251, v[142:145], s[42:43] offset:2048 nt
	s_add_u32 s42, s42, 0x800000
	s_addc_u32 s43, s43, 0
	global_load_dwordx4 v[130:133], v246, s[4:5] nt
	global_load_dwordx4 v[134:137], v247, s[4:5] nt
	global_load_dwordx4 v[138:141], v248, s[4:5] nt
	global_load_dwordx4 v[142:145], v249, s[4:5] nt
	global_load_dwordx4 v[146:149], v246, s[6:7] nt
	global_load_dwordx4 v[150:153], v247, s[6:7] nt
	global_load_dwordx4 v[154:157], v248, s[6:7] nt
	global_load_dwordx4 v[158:161], v249, s[6:7] nt
	global_load_dwordx4 v[162:165], v246, s[8:9] nt
	global_load_dwordx4 v[166:169], v247, s[8:9] nt
	global_load_dwordx4 v[170:173], v248, s[8:9] nt
	global_load_dwordx4 v[174:177], v249, s[8:9] nt
	global_load_dwordx4 v[178:181], v246, s[38:39] nt
	global_load_dwordx4 v[182:185], v247, s[38:39] nt
	global_load_dwordx4 v[186:189], v248, s[38:39] nt
	global_load_dwordx4 v[190:193], v249, s[38:39] nt
	s_add_u32 s4, s4, 0x2000000
	s_addc_u32 s5, s5, 0
	s_add_u32 s6, s6, 0x2000000
	s_addc_u32 s7, s7, 0
	s_add_u32 s8, s8, 0x2000000
	s_addc_u32 s9, s9, 0
	s_add_u32 s38, s38, 0x2000000
	s_addc_u32 s39, s39, 0
	s_waitcnt vmcnt(40)
; #define GAS __attribute__((address_space(1)))
; template <bool GAIN, bool NT = false> __device__ __forceinline__ void titem8_load(const TItem& d, int lane, f32x4 (&r)[16], f32x4 (&g)[4]) {
;     const int q = lane & 7, kg = lane >> 3; const unsigned lo = (unsigned)((16 * kg) * d.N + 4 * q) * 4u;
;     const GAS char* base = (const GAS char*)d.src;
; #pragma unroll
;     for (int j = 0; j < 16; ++j) { const GAS f32x4* p = (const GAS f32x4*)(base + (size_t)j * (size_t)d.N * 4 + lo); r[j] = NT ? __builtin_nontemporal_load(p) : *p; }
; template <bool GAIN, bool NT = false> __device__ __forceinline__ void titem8_store(const TItem& d, int lane, const f32x4 (&r)[16], const f32x4 (&g)[4]) {
;     const int q = lane & 7, kg = lane >> 3; const unsigned lo = (unsigned)((4 * q) * d.ldk + 16 * kg);
;     GAS char* base = (GAS char*)d.dst;
;     f32x4 s[16];
; #pragma unroll
;     for (int j = 0; j < 16; ++j) s[j] = r[j] * ((GAIN ? g[j >> 2][j & 3] : 1.0f) * W8_SCALE);
; #pragma unroll
;     for (int i = 0; i < 4; ++i) { v4u w;
;         w.x = pk4_fp8w(s[0][i], s[1][i], s[2][i], s[3][i]); w.y = pk4_fp8w(s[4][i], s[5][i], s[6][i], s[7][i]);
;         w.z = pk4_fp8w(s[8][i], s[9][i], s[10][i], s[11][i]); w.w = pk4_fp8w(s[12][i], s[13][i], s[14][i], s[15][i]);
;         GAS v4u* p = (GAS v4u*)(base + (size_t)i * (size_t)d.ldk + lo);
;         if (NT) __builtin_nontemporal_store(w, p); else *p = w; }
	v_pk_mul_f32 v[0:1], v[0:1], s[30:31] op_sel_hi:[1,0]
	v_pk_mul_f32 v[2:3], v[2:3], s[30:31] op_sel_hi:[1,0]
	v_pk_mul_f32 v[4:5], v[4:5], s[30:31] op_sel_hi:[1,0]
	v_pk_mul_f32 v[6:7], v[6:7], s[30:31] op_sel_hi:[1,0]
	v_pk_mul_f32 v[8:9], v[8:9], s[30:31] op_sel_hi:[1,0]
	v_pk_mul_f32 v[10:11], v[10:11], s[30:31] op_sel_hi:[1,0]
	v_pk_mul_f32 v[12:13], v[12:13], s[30:31] op_sel_hi:[1,0]
	v_pk_mul_f32 v[14:15], v[14:15], s[30:31] op_sel_hi:[1,0]
	v_pk_mul_f32 v[16:17], v[16:17], s[30:31] op_sel_hi:[1,0]
	v_pk_mul_f32 v[18:19], v[18:19], s[30:31] op_sel_hi:[1,0]
	v_pk_mul_f32 v[20:21], v[20:21], s[30:31] op_sel_hi:[1,0]
	v_pk_mul_f32 v[22:23], v[22:23], s[30:31] op_sel_hi:[1,0]
	v_pk_mul_f32 v[24:25], v[24:25], s[30:31] op_sel_hi:[1,0]
	v_pk_mul_f32 v[26:27], v[26:27], s[30:31] op_sel_hi:[1,0]
	v_pk_mul_f32 v[28:29], v[28:29], s[30:31] op_sel_hi:[1,0]
	v_pk_mul_f32 v[30:31], v[30:31], s[30:31] op_sel_hi:[1,0]
	v_pk_mul_f32 v[32:33], v[32:33], s[30:31] op_sel_hi:[1,0]
	v_pk_mul_f32 v[34:35], v[34:35], s[30:31] op_sel_hi:[1,0]
	v_pk_mul_f32 v[36:37], v[36:37], s[30:31] op_sel_hi:[1,0]
	v_pk_mul_f32 v[38:39], v[38:39], s[30:31] op_sel_hi:[1,0]
	v_pk_mul_f32 v[40:41], v[40:41], s[30:31] op_sel_hi:[1,0]
	v_pk_mul_f32 v[42:43], v[42:43], s[30:31] op_sel_hi:[1,0]
	v_pk_mul_f32 v[44:45], v[44:45], s[30:31] op_sel_hi:[1,0]
	v_pk_mul_f32 v[46:47], v[46:47], s[30:31] op_sel_hi:[1,0]
	v_pk_mul_f32 v[48:49], v[48:49], s[30:31] op_sel_hi:[1,0]
	v_pk_mul_f32 v[50:51], v[50:51], s[30:31] op_sel_hi:[1,0]
	v_pk_mul_f32 v[52:53], v[52:53], s[30:31] op_sel_hi:[1,0]
	v_pk_mul_f32 v[54:55], v[54:55], s[30:31] op_sel_hi:[1,0]
	v_pk_mul_f32 v[56:57], v[56:57], s[30:31] op_sel_hi:[1,0]
	v_pk_mul_f32 v[58:59], v[58:59], s[30:31] op_sel_hi:[1,0]
	v_pk_mul_f32 v[60:61], v[60:61], s[30:31] op_sel_hi:[1,0]
	v_pk_mul_f32 v[62:63], v[62:63], s[30:31] op_sel_hi:[1,0]
	v_med3_f32 v0, v0, s24, v237
	v_med3_f32 v1, v1, s24, v237
	v_med3_f32 v2, v2, s24, v237
	v_med3_f32 v3, v3, s24, v237
	v_med3_f32 v4, v4, s24, v237
	v_med3_f32 v5, v5, s24, v237
	v_med3_f32 v6, v6, s24, v237
	v_med3_f32 v7, v7, s24, v237
	v_med3_f32 v8, v8, s24, v237
	v_med3_f32 v9, v9, s24, v237
	v_med3_f32 v10, v10, s24, v237
	v_med3_f32 v11, v11, s24, v237
	v_med3_f32 v12, v12, s24, v237
	v_med3_f32 v13, v13, s24, v237
	v_med3_f32 v14, v14, s24, v237
	v_med3_f32 v15, v15, s24, v237
	v_med3_f32 v16, v16, s24, v237
	v_med3_f32 v17, v17, s24, v237
	v_med3_f32 v18, v18, s24, v237
	v_med3_f32 v19, v19, s24, v237
	v_med3_f32 v20, v20, s24, v237
	v_med3_f32 v21, v21, s24, v237
	v_med3_f32 v22, v22, s24, v237
	v_med3_f32 v23, v23, s24, v237
	v_med3_f32 v24, v24, s24, v237
	v_med3_f32 v25, v25, s24, v237
	v_med3_f32 v26, v26, s24, v237
	v_med3_f32 v27, v27, s24, v237
	v_med3_f32 v28, v28, s24, v237
	v_med3_f32 v29, v29, s24, v237
	v_med3_f32 v30, v30, s24, v237
	v_med3_f32 v31, v31, s24, v237
	v_med3_f32 v32, v32, s24, v237
	v_med3_f32 v33, v33, s24, v237
	v_med3_f32 v34, v34, s24, v237
	v_med3_f32 v35, v35, s24, v237
	v_med3_f32 v36, v36, s24, v237
	v_med3_f32 v37, v37, s24, v237
	v_med3_f32 v38, v38, s24, v237
	v_med3_f32 v39, v39, s24, v237
	v_med3_f32 v40, v40, s24, v237
	v_med3_f32 v41, v41, s24, v237
	v_med3_f32 v42, v42, s24, v237
	v_med3_f32 v43, v43, s24, v237
	v_med3_f32 v44, v44, s24, v237
	v_med3_f32 v45, v45, s24, v237
	v_med3_f32 v46, v46, s24, v237
	v_med3_f32 v47, v47, s24, v237
	v_med3_f32 v48, v48, s24, v237
	v_med3_f32 v49, v49, s24, v237
	v_med3_f32 v50, v50, s24, v237
	v_med3_f32 v51, v51, s24, v237
	v_med3_f32 v52, v52, s24, v237
	v_med3_f32 v53, v53, s24, v237
	v_med3_f32 v54, v54, s24, v237
	v_med3_f32 v55, v55, s24, v237
	v_med3_f32 v56, v56, s24, v237
	v_med3_f32 v57, v57, s24, v237
	v_med3_f32 v58, v58, s24, v237
	v_med3_f32 v59, v59, s24, v237
	v_med3_f32 v60, v60, s24, v237
	v_med3_f32 v61, v61, s24, v237
	v_med3_f32 v62, v62, s24, v237
	v_med3_f32 v63, v63, s24, v237
	v_cvt_pk_fp8_f32 v0, v0, v4
	v_cvt_pk_fp8_f32 v0, v8, v12 op_sel:[0,0,1]
	v_cvt_pk_fp8_f32 v4, v1, v5
	v_cvt_pk_fp8_f32 v4, v9, v13 op_sel:[0,0,1]
	v_cvt_pk_fp8_f32 v8, v2, v6
	v_cvt_pk_fp8_f32 v8, v10, v14 op_sel:[0,0,1]
	v_cvt_pk_fp8_f32 v12, v3, v7
	v_cvt_pk_fp8_f32 v12, v11, v15 op_sel:[0,0,1]
	v_cvt_pk_fp8_f32 v1, v16, v20
	v_cvt_pk_fp8_f32 v1, v24, v28 op_sel:[0,0,1]
	v_cvt_pk_fp8_f32 v5, v17, v21
	v_cvt_pk_fp8_f32 v5, v25, v29 op_sel:[0,0,1]
	v_cvt_pk_fp8_f32 v9, v18, v22
	v_cvt_pk_fp8_f32 v9, v26, v30 op_sel:[0,0,1]
	v_cvt_pk_fp8_f32 v13, v19, v23
	v_cvt_pk_fp8_f32 v13, v27, v31 op_sel:[0,0,1]
	v_cvt_pk_fp8_f32 v2, v32, v36
	v_cvt_pk_fp8_f32 v2, v40, v44 op_sel:[0,0,1]
	v_cvt_pk_fp8_f32 v6, v33, v37
	v_cvt_pk_fp8_f32 v6, v41, v45 op_sel:[0,0,1]
	v_cvt_pk_fp8_f32 v10, v34, v38
	v_cvt_pk_fp8_f32 v10, v42, v46 op_sel:[0,0,1]
	v_cvt_pk_fp8_f32 v14, v35, v39
	v_cvt_pk_fp8_f32 v14, v43, v47 op_sel:[0,0,1]
	v_cvt_pk_fp8_f32 v3, v48, v52
	v_cvt_pk_fp8_f32 v3, v56, v60 op_sel:[0,0,1]
	v_cvt_pk_fp8_f32 v7, v49, v53
	v_cvt_pk_fp8_f32 v7, v57, v61 op_sel:[0,0,1]
	v_cvt_pk_fp8_f32 v11, v50, v54
	v_cvt_pk_fp8_f32 v11, v58, v62 op_sel:[0,0,1]
	v_cvt_pk_fp8_f32 v15, v51, v55
	v_cvt_pk_fp8_f32 v15, v59, v63 op_sel:[0,0,1]
	global_store_dwordx4 v250, v[0:3], s[42:43] nt
	global_store_dwordx4 v250, v[4:7], s[42:43] offset:2048 nt
	global_store_dwordx4 v251, v[8:11], s[42:43] nt
	global_store_dwordx4 v251, v[12:15], s[42:43] offset:2048 nt
	s_add_u32 s42, s42, 0x800000
	s_addc_u32 s43, s43, 0
	global_load_dwordx4 v[0:3], v246, s[4:5] nt
	global_load_dwordx4 v[4:7], v247, s[4:5] nt
	global_load_dwordx4 v[8:11], v248, s[4:5] nt
	global_load_dwordx4 v[12:15], v249, s[4:5] nt
	global_load_dwordx4 v[16:19], v246, s[6:7] nt
	global_load_dwordx4 v[20:23], v247, s[6:7] nt
	global_load_dwordx4 v[24:27], v248, s[6:7] nt
	global_load_dwordx4 v[28:31], v249, s[6:7] nt
	global_load_dwordx4 v[32:35], v246, s[8:9] nt
	global_load_dwordx4 v[36:39], v247, s[8:9] nt
	global_load_dwordx4 v[40:43], v248, s[8:9] nt
	global_load_dwordx4 v[44:47], v249, s[8:9] nt
	global_load_dwordx4 v[48:51], v246, s[38:39] nt
	global_load_dwordx4 v[52:55], v247, s[38:39] nt
	global_load_dwordx4 v[56:59], v248, s[38:39] nt
	global_load_dwordx4 v[60:63], v249, s[38:39] nt
	s_add_u32 s4, s4, 0x2000000
	s_addc_u32 s5, s5, 0
	s_add_u32 s6, s6, 0x2000000
	s_addc_u32 s7, s7, 0
	s_add_u32 s8, s8, 0x2000000
	s_addc_u32 s9, s9, 0
	s_add_u32 s38, s38, 0x2000000
	s_addc_u32 s39, s39, 0
	s_waitcnt vmcnt(40)
; #define GAS __attribute__((address_space(1)))
; template <bool GAIN, bool NT = false> __device__ __forceinline__ void titem8_load(const TItem& d, int lane, f32x4 (&r)[16], f32x4 (&g)[4]) {
;     const int q = lane & 7, kg = lane >> 3; const unsigned lo = (unsigned)((16 * kg) * d.N + 4 * q) * 4u;
;     const GAS char* base = (const GAS char*)d.src;
; #pragma unroll
;     for (int j = 0; j < 16; ++j) { const GAS f32x4* p = (const GAS f32x4*)(base + (size_t)j * (size_t)d.N * 4 + lo); r[j] = NT ? __builtin_nontemporal_load(p) : *p; }
; template <bool GAIN, bool NT = false> __device__ __forceinline__ void titem8_store(const TItem& d, int lane, const f32x4 (&r)[16], const f32x4 (&g)[4]) {
;     const int q = lane & 7, kg = lane >> 3; const unsigned lo = (unsigned)((4 * q) * d.ldk + 16 * kg);
;     GAS char* base = (GAS char*)d.dst;
;     f32x4 s[16];
; #pragma unroll
;     for (int j = 0; j < 16; ++j) s[j] = r[j] * ((GAIN ? g[j >> 2][j & 3] : 1.0f) * W8_SCALE);
; #pragma unroll
;     for (int i = 0; i < 4; ++i) { v4u w;
;         w.x = pk4_fp8w(s[0][i], s[1][i], s[2][i], s[3][i]); w.y = pk4_fp8w(s[4][i], s[5][i], s[6][i], s[7][i]);
;         w.z = pk4_fp8w(s[8][i], s[9][i], s[10][i], s[11][i]); w.w = pk4_fp8w(s[12][i], s[13][i], s[14][i], s[15][i]);
;         GAS v4u* p = (GAS v4u*)(base + (size_t)i * (size_t)d.ldk + lo);
;         if (NT) __builtin_nontemporal_store(w, p); else *p = w; }
	v_pk_mul_f32 v[66:67], v[66:67], s[30:31] op_sel_hi:[1,0]
	v_pk_mul_f32 v[68:69], v[68:69], s[30:31] op_sel_hi:[1,0]
	v_pk_mul_f32 v[70:71], v[70:71], s[30:31] op_sel_hi:[1,0]
	v_pk_mul_f32 v[72:73], v[72:73], s[30:31] op_sel_hi:[1,0]
	v_pk_mul_f32 v[74:75], v[74:75], s[30:31] op_sel_hi:[1,0]
	v_pk_mul_f32 v[76:77], v[76:77], s[30:31] op_sel_hi:[1,0]
	v_pk_mul_f32 v[78:79], v[78:79], s[30:31] op_sel_hi:[1,0]
	v_pk_mul_f32 v[80:81], v[80:81], s[30:31] op_sel_hi:[1,0]
	v_pk_mul_f32 v[82:83], v[82:83], s[30:31] op_sel_hi:[1,0]
	v_pk_mul_f32 v[84:85], v[84:85], s[30:31] op_sel_hi:[1,0]
	v_pk_mul_f32 v[86:87], v[86:87], s[30:31] op_sel_hi:[1,0]
	v_pk_mul_f32 v[88:89], v[88:89], s[30:31] op_sel_hi:[1,0]
	v_pk_mul_f32 v[90:91], v[90:91], s[30:31] op_sel_hi:[1,0]
	v_pk_mul_f32 v[92:93], v[92:93], s[30:31] op_sel_hi:[1,0]
	v_pk_mul_f32 v[94:95], v[94:95], s[30:31] op_sel_hi:[1,0]
	v_pk_mul_f32 v[96:97], v[96:97], s[30:31] op_sel_hi:[1,0]
	v_pk_mul_f32 v[98:99], v[98:99], s[30:31] op_sel_hi:[1,0]
	v_pk_mul_f32 v[100:101], v[100:101], s[30:31] op_sel_hi:[1,0]
	v_pk_mul_f32 v[102:103], v[102:103], s[30:31] op_sel_hi:[1,0]
	v_pk_mul_f32 v[104:105], v[104:105], s[30:31] op_sel_hi:[1,0]
	v_pk_mul_f32 v[106:107], v[106:107], s[30:31] op_sel_hi:[1,0]
	v_pk_mul_f32 v[108:109], v[108:109], s[30:31] op_sel_hi:[1,0]
	v_pk_mul_f32 v[110:111], v[110:111], s[30:31] op_sel_hi:[1,0]
	v_pk_mul_f32 v[112:113], v[112:113], s[30:31] op_sel_hi:[1,0]
	v_pk_mul_f32 v[114:115], v[114:115], s[30:31] op_sel_hi:[1,0]
	v_pk_mul_f32 v[116:117], v[116:117], s[30:31] op_sel_hi:[1,0]
	v_pk_mul_f32 v[118:119], v[118:119], s[30:31] op_sel_hi:[1,0]
	v_pk_mul_f32 v[120:121], v[120:121], s[30:31] op_sel_hi:[1,0]
	v_pk_mul_f32 v[122:123], v[122:123], s[30:31] op_sel_hi:[1,0]
	v_pk_mul_f32 v[124:125], v[124:125], s[30:31] op_sel_hi:[1,0]
	v_pk_mul_f32 v[126:127], v[126:127], s[30:31] op_sel_hi:[1,0]
	v_pk_mul_f32 v[128:129], v[128:129], s[30:31] op_sel_hi:[1,0]
	v_med3_f32 v66, v66, s24, v237
	v_med3_f32 v67, v67, s24, v237
	v_med3_f32 v68, v68, s24, v237
	v_med3_f32 v69, v69, s24, v237
	v_med3_f32 v70, v70, s24, v237
	v_med3_f32 v71, v71, s24, v237
	v_med3_f32 v72, v72, s24, v237
	v_med3_f32 v73, v73, s24, v237
	v_med3_f32 v74, v74, s24, v237
	v_med3_f32 v75, v75, s24, v237
	v_med3_f32 v76, v76, s24, v237
	v_med3_f32 v77, v77, s24, v237
	v_med3_f32 v78, v78, s24, v237
	v_med3_f32 v79, v79, s24, v237
	v_med3_f32 v80, v80, s24, v237
	v_med3_f32 v81, v81, s24, v237
	v_med3_f32 v82, v82, s24, v237
	v_med3_f32 v83, v83, s24, v237
	v_med3_f32 v84, v84, s24, v237
	v_med3_f32 v85, v85, s24, v237
	v_med3_f32 v86, v86, s24, v237
	v_med3_f32 v87, v87, s24, v237
	v_med3_f32 v88, v88, s24, v237
	v_med3_f32 v89, v89, s24, v237
	v_med3_f32 v90, v90, s24, v237
	v_med3_f32 v91, v91, s24, v237
	v_med3_f32 v92, v92, s24, v237
	v_med3_f32 v93, v93, s24, v237
	v_med3_f32 v94, v94, s24, v237
	v_med3_f32 v95, v95, s24, v237
	v_med3_f32 v96, v96, s24, v237
	v_med3_f32 v97, v97, s24, v237
	v_med3_f32 v98, v98, s24, v237
	v_med3_f32 v99, v99, s24, v237
	v_med3_f32 v100, v100, s24, v237
	v_med3_f32 v101, v101, s24, v237
	v_med3_f32 v102, v102, s24, v237
	v_med3_f32 v103, v103, s24, v237
	v_med3_f32 v104, v104, s24, v237
	v_med3_f32 v105, v105, s24, v237
	v_med3_f32 v106, v106, s24, v237
	v_med3_f32 v107, v107, s24, v237
	v_med3_f32 v108, v108, s24, v237
	v_med3_f32 v109, v109, s24, v237
	v_med3_f32 v110, v110, s24, v237
	v_med3_f32 v111, v111, s24, v237
	v_med3_f32 v112, v112, s24, v237
	v_med3_f32 v113, v113, s24, v237
	v_med3_f32 v114, v114, s24, v237
	v_med3_f32 v115, v115, s24, v237
	v_med3_f32 v116, v116, s24, v237
	v_med3_f32 v117, v117, s24, v237
	v_med3_f32 v118, v118, s24, v237
	v_med3_f32 v119, v119, s24, v237
	v_med3_f32 v120, v120, s24, v237
	v_med3_f32 v121, v121, s24, v237
	v_med3_f32 v122, v122, s24, v237
	v_med3_f32 v123, v123, s24, v237
	v_med3_f32 v124, v124, s24, v237
	v_med3_f32 v125, v125, s24, v237
	v_med3_f32 v126, v126, s24, v237
	v_med3_f32 v127, v127, s24, v237
	v_med3_f32 v128, v128, s24, v237
	v_med3_f32 v129, v129, s24, v237
	v_cvt_pk_fp8_f32 v66, v66, v70
	v_cvt_pk_fp8_f32 v66, v74, v78 op_sel:[0,0,1]
	v_cvt_pk_fp8_f32 v70, v67, v71
	v_cvt_pk_fp8_f32 v70, v75, v79 op_sel:[0,0,1]
	v_cvt_pk_fp8_f32 v74, v68, v72
	v_cvt_pk_fp8_f32 v74, v76, v80 op_sel:[0,0,1]
	v_cvt_pk_fp8_f32 v78, v69, v73
	v_cvt_pk_fp8_f32 v78, v77, v81 op_sel:[0,0,1]
	v_cvt_pk_fp8_f32 v67, v82, v86
	v_cvt_pk_fp8_f32 v67, v90, v94 op_sel:[0,0,1]
	v_cvt_pk_fp8_f32 v71, v83, v87
	v_cvt_pk_fp8_f32 v71, v91, v95 op_sel:[0,0,1]
	v_cvt_pk_fp8_f32 v75, v84, v88
	v_cvt_pk_fp8_f32 v75, v92, v96 op_sel:[0,0,1]
	v_cvt_pk_fp8_f32 v79, v85, v89
	v_cvt_pk_fp8_f32 v79, v93, v97 op_sel:[0,0,1]
	v_cvt_pk_fp8_f32 v68, v98, v102
	v_cvt_pk_fp8_f32 v68, v106, v110 op_sel:[0,0,1]
	v_cvt_pk_fp8_f32 v72, v99, v103
	v_cvt_pk_fp8_f32 v72, v107, v111 op_sel:[0,0,1]
	v_cvt_pk_fp8_f32 v76, v100, v104
	v_cvt_pk_fp8_f32 v76, v108, v112 op_sel:[0,0,1]
	v_cvt_pk_fp8_f32 v80, v101, v105
	v_cvt_pk_fp8_f32 v80, v109, v113 op_sel:[0,0,1]
	v_cvt_pk_fp8_f32 v69, v114, v118
	v_cvt_pk_fp8_f32 v69, v122, v126 op_sel:[0,0,1]
	v_cvt_pk_fp8_f32 v73, v115, v119
	v_cvt_pk_fp8_f32 v73, v123, v127 op_sel:[0,0,1]
	v_cvt_pk_fp8_f32 v77, v116, v120
	v_cvt_pk_fp8_f32 v77, v124, v128 op_sel:[0,0,1]
	v_cvt_pk_fp8_f32 v81, v117, v121
	v_cvt_pk_fp8_f32 v81, v125, v129 op_sel:[0,0,1]
	global_store_dwordx4 v250, v[66:69], s[42:43] nt
	global_store_dwordx4 v250, v[70:73], s[42:43] offset:2048 nt
	global_store_dwordx4 v251, v[74:77], s[42:43] nt
	global_store_dwordx4 v251, v[78:81], s[42:43] offset:2048 nt
	s_add_u32 s42, s42, 0x800000
	s_addc_u32 s43, s43, 0
	global_load_dwordx4 v[66:69], v246, s[4:5] nt
	global_load_dwordx4 v[70:73], v247, s[4:5] nt
	global_load_dwordx4 v[74:77], v248, s[4:5] nt
	global_load_dwordx4 v[78:81], v249, s[4:5] nt
	global_load_dwordx4 v[82:85], v246, s[6:7] nt
	global_load_dwordx4 v[86:89], v247, s[6:7] nt
	global_load_dwordx4 v[90:93], v248, s[6:7] nt
	global_load_dwordx4 v[94:97], v249, s[6:7] nt
	global_load_dwordx4 v[98:101], v246, s[8:9] nt
	global_load_dwordx4 v[102:105], v247, s[8:9] nt
	global_load_dwordx4 v[106:109], v248, s[8:9] nt
	global_load_dwordx4 v[110:113], v249, s[8:9] nt
	global_load_dwordx4 v[114:117], v246, s[38:39] nt
	global_load_dwordx4 v[118:121], v247, s[38:39] nt
	global_load_dwordx4 v[122:125], v248, s[38:39] nt
	global_load_dwordx4 v[126:129], v249, s[38:39] nt
	s_add_u32 s4, s4, 0x2000000
	s_addc_u32 s5, s5, 0
	s_add_u32 s6, s6, 0x2000000
	s_addc_u32 s7, s7, 0
	s_add_u32 s8, s8, 0x2000000
	s_addc_u32 s9, s9, 0
	s_add_u32 s38, s38, 0x2000000
	s_addc_u32 s39, s39, 0
	s_waitcnt vmcnt(40)
; #define GAS __attribute__((address_space(1)))
; template <bool GAIN, bool NT = false> __device__ __forceinline__ void titem8_load(const TItem& d, int lane, f32x4 (&r)[16], f32x4 (&g)[4]) {
;     const int q = lane & 7, kg = lane >> 3; const unsigned lo = (unsigned)((16 * kg) * d.N + 4 * q) * 4u;
;     const GAS char* base = (const GAS char*)d.src;
; #pragma unroll
;     for (int j = 0; j < 16; ++j) { const GAS f32x4* p = (const GAS f32x4*)(base + (size_t)j * (size_t)d.N * 4 + lo); r[j] = NT ? __builtin_nontemporal_load(p) : *p; }
; template <bool GAIN, bool NT = false> __device__ __forceinline__ void titem8_store(const TItem& d, int lane, const f32x4 (&r)[16], const f32x4 (&g)[4]) {
;     const int q = lane & 7, kg = lane >> 3; const unsigned lo = (unsigned)((4 * q) * d.ldk + 16 * kg);
;     GAS char* base = (GAS char*)d.dst;
;     f32x4 s[16];
; #pragma unroll
;     for (int j = 0; j < 16; ++j) s[j] = r[j] * ((GAIN ? g[j >> 2][j & 3] : 1.0f) * W8_SCALE);
; #pragma unroll
;     for (int i = 0; i < 4; ++i) { v4u w;
;         w.x = pk4_fp8w(s[0][i], s[1][i], s[2][i], s[3][i]); w.y = pk4_fp8w(s[4][i], s[5][i], s[6][i], s[7][i]);
;         w.z = pk4_fp8w(s[8][i], s[9][i], s[10][i], s[11][i]); w.w = pk4_fp8w(s[12][i], s[13][i], s[14][i], s[15][i]);
;         GAS v4u* p = (GAS v4u*)(base + (size_t)i * (size_t)d.ldk + lo);
;         if (NT) __builtin_nontemporal_store(w, p); else *p = w; }
	v_pk_mul_f32 v[130:131], v[130:131], s[30:31] op_sel_hi:[1,0]
	v_pk_mul_f32 v[132:133], v[132:133], s[30:31] op_sel_hi:[1,0]
	v_pk_mul_f32 v[134:135], v[134:135], s[30:31] op_sel_hi:[1,0]
	v_pk_mul_f32 v[136:137], v[136:137], s[30:31] op_sel_hi:[1,0]
	v_pk_mul_f32 v[138:139], v[138:139], s[30:31] op_sel_hi:[1,0]
	v_pk_mul_f32 v[140:141], v[140:141], s[30:31] op_sel_hi:[1,0]
	v_pk_mul_f32 v[142:143], v[142:143], s[30:31] op_sel_hi:[1,0]
	v_pk_mul_f32 v[144:145], v[144:145], s[30:31] op_sel_hi:[1,0]
	v_pk_mul_f32 v[146:147], v[146:147], s[30:31] op_sel_hi:[1,0]
	v_pk_mul_f32 v[148:149], v[148:149], s[30:31] op_sel_hi:[1,0]
	v_pk_mul_f32 v[150:151], v[150:151], s[30:31] op_sel_hi:[1,0]
	v_pk_mul_f32 v[152:153], v[152:153], s[30:31] op_sel_hi:[1,0]
	v_pk_mul_f32 v[154:155], v[154:155], s[30:31] op_sel_hi:[1,0]
	v_pk_mul_f32 v[156:157], v[156:157], s[30:31] op_sel_hi:[1,0]
	v_pk_mul_f32 v[158:159], v[158:159], s[30:31] op_sel_hi:[1,0]
	v_pk_mul_f32 v[160:161], v[160:161], s[30:31] op_sel_hi:[1,0]
	v_pk_mul_f32 v[162:163], v[162:163], s[30:31] op_sel_hi:[1,0]
	v_pk_mul_f32 v[164:165], v[164:165], s[30:31] op_sel_hi:[1,0]
	v_pk_mul_f32 v[166:167], v[166:167], s[30:31] op_sel_hi:[1,0]
	v_pk_mul_f32 v[168:169], v[168:169], s[30:31] op_sel_hi:[1,0]
	v_pk_mul_f32 v[170:171], v[170:171], s[30:31] op_sel_hi:[1,0]
	v_pk_mul_f32 v[172:173], v[172:173], s[30:31] op_sel_hi:[1,0]
	v_pk_mul_f32 v[174:175], v[174:175], s[30:31] op_sel_hi:[1,0]
	v_pk_mul_f32 v[176:177], v[176:177], s[30:31] op_sel_hi:[1,0]
	v_pk_mul_f32 v[178:179], v[178:179], s[30:31] op_sel_hi:[1,0]
	v_pk_mul_f32 v[180:181], v[180:181], s[30:31] op_sel_hi:[1,0]
	v_pk_mul_f32 v[182:183], v[182:183], s[30:31] op_sel_hi:[1,0]
	v_pk_mul_f32 v[184:185], v[184:185], s[30:31] op_sel_hi:[1,0]
	v_pk_mul_f32 v[186:187], v[186:187], s[30:31] op_sel_hi:[1,0]
	v_pk_mul_f32 v[188:189], v[188:189], s[30:31] op_sel_hi:[1,0]
	v_pk_mul_f32 v[190:191], v[190:191], s[30:31] op_sel_hi:[1,0]
	v_pk_mul_f32 v[192:193], v[192:193], s[30:31] op_sel_hi:[1,0]
	v_med3_f32 v130, v130, s24, v237
	v_med3_f32 v131, v131, s24, v237
	v_med3_f32 v132, v132, s24, v237
	v_med3_f32 v133, v133, s24, v237
	v_med3_f32 v134, v134, s24, v237
	v_med3_f32 v135, v135, s24, v237
	v_med3_f32 v136, v136, s24, v237
	v_med3_f32 v137, v137, s24, v237
	v_med3_f32 v138, v138, s24, v237
	v_med3_f32 v139, v139, s24, v237
	v_med3_f32 v140, v140, s24, v237
	v_med3_f32 v141, v141, s24, v237
	v_med3_f32 v142, v142, s24, v237
	v_med3_f32 v143, v143, s24, v237
	v_med3_f32 v144, v144, s24, v237
	v_med3_f32 v145, v145, s24, v237
	v_med3_f32 v146, v146, s24, v237
	v_med3_f32 v147, v147, s24, v237
	v_med3_f32 v148, v148, s24, v237
	v_med3_f32 v149, v149, s24, v237
	v_med3_f32 v150, v150, s24, v237
	v_med3_f32 v151, v151, s24, v237
	v_med3_f32 v152, v152, s24, v237
	v_med3_f32 v153, v153, s24, v237
	v_med3_f32 v154, v154, s24, v237
	v_med3_f32 v155, v155, s24, v237
	v_med3_f32 v156, v156, s24, v237
	v_med3_f32 v157, v157, s24, v237
	v_med3_f32 v158, v158, s24, v237
	v_med3_f32 v159, v159, s24, v237
	v_med3_f32 v160, v160, s24, v237
	v_med3_f32 v161, v161, s24, v237
	v_med3_f32 v162, v162, s24, v237
	v_med3_f32 v163, v163, s24, v237
	v_med3_f32 v164, v164, s24, v237
	v_med3_f32 v165, v165, s24, v237
	v_med3_f32 v166, v166, s24, v237
	v_med3_f32 v167, v167, s24, v237
	v_med3_f32 v168, v168, s24, v237
	v_med3_f32 v169, v169, s24, v237
	v_med3_f32 v170, v170, s24, v237
	v_med3_f32 v171, v171, s24, v237
	v_med3_f32 v172, v172, s24, v237
	v_med3_f32 v173, v173, s24, v237
	v_med3_f32 v174, v174, s24, v237
	v_med3_f32 v175, v175, s24, v237
	v_med3_f32 v176, v176, s24, v237
	v_med3_f32 v177, v177, s24, v237
	v_med3_f32 v178, v178, s24, v237
	v_med3_f32 v179, v179, s24, v237
	v_med3_f32 v180, v180, s24, v237
	v_med3_f32 v181, v181, s24, v237
	v_med3_f32 v182, v182, s24, v237
	v_med3_f32 v183, v183, s24, v237
	v_med3_f32 v184, v184, s24, v237
	v_med3_f32 v185, v185, s24, v237
	v_med3_f32 v186, v186, s24, v237
	v_med3_f32 v187, v187, s24, v237
	v_med3_f32 v188, v188, s24, v237
	v_med3_f32 v189, v189, s24, v237
	v_med3_f32 v190, v190, s24, v237
	v_med3_f32 v191, v191, s24, v237
	v_med3_f32 v192, v192, s24, v237
	v_med3_f32 v193, v193, s24, v237
	v_cvt_pk_fp8_f32 v130, v130, v134
	v_cvt_pk_fp8_f32 v130, v138, v142 op_sel:[0,0,1]
	v_cvt_pk_fp8_f32 v134, v131, v135
	v_cvt_pk_fp8_f32 v134, v139, v143 op_sel:[0,0,1]
	v_cvt_pk_fp8_f32 v138, v132, v136
	v_cvt_pk_fp8_f32 v138, v140, v144 op_sel:[0,0,1]
	v_cvt_pk_fp8_f32 v142, v133, v137
	v_cvt_pk_fp8_f32 v142, v141, v145 op_sel:[0,0,1]
	v_cvt_pk_fp8_f32 v131, v146, v150
	v_cvt_pk_fp8_f32 v131, v154, v158 op_sel:[0,0,1]
	v_cvt_pk_fp8_f32 v135, v147, v151
	v_cvt_pk_fp8_f32 v135, v155, v159 op_sel:[0,0,1]
	v_cvt_pk_fp8_f32 v139, v148, v152
	v_cvt_pk_fp8_f32 v139, v156, v160 op_sel:[0,0,1]
	v_cvt_pk_fp8_f32 v143, v149, v153
	v_cvt_pk_fp8_f32 v143, v157, v161 op_sel:[0,0,1]
	v_cvt_pk_fp8_f32 v132, v162, v166
	v_cvt_pk_fp8_f32 v132, v170, v174 op_sel:[0,0,1]
	v_cvt_pk_fp8_f32 v136, v163, v167
	v_cvt_pk_fp8_f32 v136, v171, v175 op_sel:[0,0,1]
	v_cvt_pk_fp8_f32 v140, v164, v168
	v_cvt_pk_fp8_f32 v140, v172, v176 op_sel:[0,0,1]
	v_cvt_pk_fp8_f32 v144, v165, v169
	v_cvt_pk_fp8_f32 v144, v173, v177 op_sel:[0,0,1]
	v_cvt_pk_fp8_f32 v133, v178, v182
	v_cvt_pk_fp8_f32 v133, v186, v190 op_sel:[0,0,1]
	v_cvt_pk_fp8_f32 v137, v179, v183
	v_cvt_pk_fp8_f32 v137, v187, v191 op_sel:[0,0,1]
	v_cvt_pk_fp8_f32 v141, v180, v184
	v_cvt_pk_fp8_f32 v141, v188, v192 op_sel:[0,0,1]
	v_cvt_pk_fp8_f32 v145, v181, v185
	v_cvt_pk_fp8_f32 v145, v189, v193 op_sel:[0,0,1]
	global_store_dwordx4 v250, v[130:133], s[42:43] nt
	global_store_dwordx4 v250, v[134:137], s[42:43] offset:2048 nt
	global_store_dwordx4 v251, v[138:141], s[42:43] nt
	global_store_dwordx4 v251, v[142:145], s[42:43] offset:2048 nt
	s_add_u32 s42, s42, 0x800000
	s_addc_u32 s43, s43, 0
	global_load_dwordx4 v[130:133], v246, s[4:5] nt
	global_load_dwordx4 v[134:137], v247, s[4:5] nt
	global_load_dwordx4 v[138:141], v248, s[4:5] nt
	global_load_dwordx4 v[142:145], v249, s[4:5] nt
	global_load_dwordx4 v[146:149], v246, s[6:7] nt
	global_load_dwordx4 v[150:153], v247, s[6:7] nt
	global_load_dwordx4 v[154:157], v248, s[6:7] nt
	global_load_dwordx4 v[158:161], v249, s[6:7] nt
	global_load_dwordx4 v[162:165], v246, s[8:9] nt
	global_load_dwordx4 v[166:169], v247, s[8:9] nt
	global_load_dwordx4 v[170:173], v248, s[8:9] nt
	global_load_dwordx4 v[174:177], v249, s[8:9] nt
	global_load_dwordx4 v[178:181], v246, s[38:39] nt
	global_load_dwordx4 v[182:185], v247, s[38:39] nt
	global_load_dwordx4 v[186:189], v248, s[38:39] nt
	global_load_dwordx4 v[190:193], v249, s[38:39] nt
	s_add_u32 s4, s4, 0x2000000
	s_addc_u32 s5, s5, 0
	s_add_u32 s6, s6, 0x2000000
	s_addc_u32 s7, s7, 0
	s_add_u32 s8, s8, 0x2000000
	s_addc_u32 s9, s9, 0
	s_add_u32 s38, s38, 0x2000000
	s_addc_u32 s39, s39, 0
	s_waitcnt vmcnt(40)
; #define GAS __attribute__((address_space(1)))
; template <bool GAIN, bool NT = false> __device__ __forceinline__ void titem8_load(const TItem& d, int lane, f32x4 (&r)[16], f32x4 (&g)[4]) {
;     const int q = lane & 7, kg = lane >> 3; const unsigned lo = (unsigned)((16 * kg) * d.N + 4 * q) * 4u;
;     const GAS char* base = (const GAS char*)d.src;
; #pragma unroll
;     for (int j = 0; j < 16; ++j) { const GAS f32x4* p = (const GAS f32x4*)(base + (size_t)j * (size_t)d.N * 4 + lo); r[j] = NT ? __builtin_nontemporal_load(p) : *p; }
; template <bool GAIN, bool NT = false> __device__ __forceinline__ void titem8_store(const TItem& d, int lane, const f32x4 (&r)[16], const f32x4 (&g)[4]) {
;     const int q = lane & 7, kg = lane >> 3; const unsigned lo = (unsigned)((4 * q) * d.ldk + 16 * kg);
;     GAS char* base = (GAS char*)d.dst;
;     f32x4 s[16];
; #pragma unroll
;     for (int j = 0; j < 16; ++j) s[j] = r[j] * ((GAIN ? g[j >> 2][j & 3] : 1.0f) * W8_SCALE);
; #pragma unroll
;     for (int i = 0; i < 4; ++i) { v4u w;
;         w.x = pk4_fp8w(s[0][i], s[1][i], s[2][i], s[3][i]); w.y = pk4_fp8w(s[4][i], s[5][i], s[6][i], s[7][i]);
;         w.z = pk4_fp8w(s[8][i], s[9][i], s[10][i], s[11][i]); w.w = pk4_fp8w(s[12][i], s[13][i], s[14][i], s[15][i]);
;         GAS v4u* p = (GAS v4u*)(base + (size_t)i * (size_t)d.ldk + lo);
;         if (NT) __builtin_nontemporal_store(w, p); else *p = w; }
	v_pk_mul_f32 v[0:1], v[0:1], s[30:31] op_sel_hi:[1,0]
	v_pk_mul_f32 v[2:3], v[2:3], s[30:31] op_sel_hi:[1,0]
	v_pk_mul_f32 v[4:5], v[4:5], s[30:31] op_sel_hi:[1,0]
	v_pk_mul_f32 v[6:7], v[6:7], s[30:31] op_sel_hi:[1,0]
	v_pk_mul_f32 v[8:9], v[8:9], s[30:31] op_sel_hi:[1,0]
	v_pk_mul_f32 v[10:11], v[10:11], s[30:31] op_sel_hi:[1,0]
	v_pk_mul_f32 v[12:13], v[12:13], s[30:31] op_sel_hi:[1,0]
	v_pk_mul_f32 v[14:15], v[14:15], s[30:31] op_sel_hi:[1,0]
	v_pk_mul_f32 v[16:17], v[16:17], s[30:31] op_sel_hi:[1,0]
	v_pk_mul_f32 v[18:19], v[18:19], s[30:31] op_sel_hi:[1,0]
	v_pk_mul_f32 v[20:21], v[20:21], s[30:31] op_sel_hi:[1,0]
	v_pk_mul_f32 v[22:23], v[22:23], s[30:31] op_sel_hi:[1,0]
	v_pk_mul_f32 v[24:25], v[24:25], s[30:31] op_sel_hi:[1,0]
	v_pk_mul_f32 v[26:27], v[26:27], s[30:31] op_sel_hi:[1,0]
	v_pk_mul_f32 v[28:29], v[28:29], s[30:31] op_sel_hi:[1,0]
	v_pk_mul_f32 v[30:31], v[30:31], s[30:31] op_sel_hi:[1,0]
	v_pk_mul_f32 v[32:33], v[32:33], s[30:31] op_sel_hi:[1,0]
	v_pk_mul_f32 v[34:35], v[34:35], s[30:31] op_sel_hi:[1,0]
	v_pk_mul_f32 v[36:37], v[36:37], s[30:31] op_sel_hi:[1,0]
	v_pk_mul_f32 v[38:39], v[38:39], s[30:31] op_sel_hi:[1,0]
	v_pk_mul_f32 v[40:41], v[40:41], s[30:31] op_sel_hi:[1,0]
	v_pk_mul_f32 v[42:43], v[42:43], s[30:31] op_sel_hi:[1,0]
	v_pk_mul_f32 v[44:45], v[44:45], s[30:31] op_sel_hi:[1,0]
	v_pk_mul_f32 v[46:47], v[46:47], s[30:31] op_sel_hi:[1,0]
	v_pk_mul_f32 v[48:49], v[48:49], s[30:31] op_sel_hi:[1,0]
	v_pk_mul_f32 v[50:51], v[50:51], s[30:31] op_sel_hi:[1,0]
	v_pk_mul_f32 v[52:53], v[52:53], s[30:31] op_sel_hi:[1,0]
	v_pk_mul_f32 v[54:55], v[54:55], s[30:31] op_sel_hi:[1,0]
	v_pk_mul_f32 v[56:57], v[56:57], s[30:31] op_sel_hi:[1,0]
	v_pk_mul_f32 v[58:59], v[58:59], s[30:31] op_sel_hi:[1,0]
	v_pk_mul_f32 v[60:61], v[60:61], s[30:31] op_sel_hi:[1,0]
	v_pk_mul_f32 v[62:63], v[62:63], s[30:31] op_sel_hi:[1,0]
	v_med3_f32 v0, v0, s24, v237
	v_med3_f32 v1, v1, s24, v237
	v_med3_f32 v2, v2, s24, v237
	v_med3_f32 v3, v3, s24, v237
	v_med3_f32 v4, v4, s24, v237
	v_med3_f32 v5, v5, s24, v237
	v_med3_f32 v6, v6, s24, v237
	v_med3_f32 v7, v7, s24, v237
	v_med3_f32 v8, v8, s24, v237
	v_med3_f32 v9, v9, s24, v237
	v_med3_f32 v10, v10, s24, v237
	v_med3_f32 v11, v11, s24, v237
	v_med3_f32 v12, v12, s24, v237
	v_med3_f32 v13, v13, s24, v237
	v_med3_f32 v14, v14, s24, v237
	v_med3_f32 v15, v15, s24, v237
	v_med3_f32 v16, v16, s24, v237
	v_med3_f32 v17, v17, s24, v237
	v_med3_f32 v18, v18, s24, v237
	v_med3_f32 v19, v19, s24, v237
	v_med3_f32 v20, v20, s24, v237
	v_med3_f32 v21, v21, s24, v237
	v_med3_f32 v22, v22, s24, v237
	v_med3_f32 v23, v23, s24, v237
	v_med3_f32 v24, v24, s24, v237
	v_med3_f32 v25, v25, s24, v237
	v_med3_f32 v26, v26, s24, v237
	v_med3_f32 v27, v27, s24, v237
	v_med3_f32 v28, v28, s24, v237
	v_med3_f32 v29, v29, s24, v237
	v_med3_f32 v30, v30, s24, v237
	v_med3_f32 v31, v31, s24, v237
	v_med3_f32 v32, v32, s24, v237
	v_med3_f32 v33, v33, s24, v237
	v_med3_f32 v34, v34, s24, v237
	v_med3_f32 v35, v35, s24, v237
	v_med3_f32 v36, v36, s24, v237
	v_med3_f32 v37, v37, s24, v237
	v_med3_f32 v38, v38, s24, v237
	v_med3_f32 v39, v39, s24, v237
	v_med3_f32 v40, v40, s24, v237
	v_med3_f32 v41, v41, s24, v237
	v_med3_f32 v42, v42, s24, v237
	v_med3_f32 v43, v43, s24, v237
	v_med3_f32 v44, v44, s24, v237
	v_med3_f32 v45, v45, s24, v237
	v_med3_f32 v46, v46, s24, v237
	v_med3_f32 v47, v47, s24, v237
	v_med3_f32 v48, v48, s24, v237
	v_med3_f32 v49, v49, s24, v237
	v_med3_f32 v50, v50, s24, v237
	v_med3_f32 v51, v51, s24, v237
	v_med3_f32 v52, v52, s24, v237
	v_med3_f32 v53, v53, s24, v237
	v_med3_f32 v54, v54, s24, v237
	v_med3_f32 v55, v55, s24, v237
	v_med3_f32 v56, v56, s24, v237
	v_med3_f32 v57, v57, s24, v237
	v_med3_f32 v58, v58, s24, v237
	v_med3_f32 v59, v59, s24, v237
	v_med3_f32 v60, v60, s24, v237
	v_med3_f32 v61, v61, s24, v237
	v_med3_f32 v62, v62, s24, v237
	v_med3_f32 v63, v63, s24, v237
	v_cvt_pk_fp8_f32 v0, v0, v4
	v_cvt_pk_fp8_f32 v0, v8, v12 op_sel:[0,0,1]
	v_cvt_pk_fp8_f32 v4, v1, v5
	v_cvt_pk_fp8_f32 v4, v9, v13 op_sel:[0,0,1]
	v_cvt_pk_fp8_f32 v8, v2, v6
	v_cvt_pk_fp8_f32 v8, v10, v14 op_sel:[0,0,1]
	v_cvt_pk_fp8_f32 v12, v3, v7
	v_cvt_pk_fp8_f32 v12, v11, v15 op_sel:[0,0,1]
	v_cvt_pk_fp8_f32 v1, v16, v20
	v_cvt_pk_fp8_f32 v1, v24, v28 op_sel:[0,0,1]
	v_cvt_pk_fp8_f32 v5, v17, v21
	v_cvt_pk_fp8_f32 v5, v25, v29 op_sel:[0,0,1]
	v_cvt_pk_fp8_f32 v9, v18, v22
	v_cvt_pk_fp8_f32 v9, v26, v30 op_sel:[0,0,1]
	v_cvt_pk_fp8_f32 v13, v19, v23
	v_cvt_pk_fp8_f32 v13, v27, v31 op_sel:[0,0,1]
	v_cvt_pk_fp8_f32 v2, v32, v36
	v_cvt_pk_fp8_f32 v2, v40, v44 op_sel:[0,0,1]
	v_cvt_pk_fp8_f32 v6, v33, v37
	v_cvt_pk_fp8_f32 v6, v41, v45 op_sel:[0,0,1]
	v_cvt_pk_fp8_f32 v10, v34, v38
	v_cvt_pk_fp8_f32 v10, v42, v46 op_sel:[0,0,1]
	v_cvt_pk_fp8_f32 v14, v35, v39
	v_cvt_pk_fp8_f32 v14, v43, v47 op_sel:[0,0,1]
	v_cvt_pk_fp8_f32 v3, v48, v52
	v_cvt_pk_fp8_f32 v3, v56, v60 op_sel:[0,0,1]
	v_cvt_pk_fp8_f32 v7, v49, v53
	v_cvt_pk_fp8_f32 v7, v57, v61 op_sel:[0,0,1]
	v_cvt_pk_fp8_f32 v11, v50, v54
	v_cvt_pk_fp8_f32 v11, v58, v62 op_sel:[0,0,1]
	v_cvt_pk_fp8_f32 v15, v51, v55
	v_cvt_pk_fp8_f32 v15, v59, v63 op_sel:[0,0,1]
	global_store_dwordx4 v250, v[0:3], s[42:43] nt
	global_store_dwordx4 v250, v[4:7], s[42:43] offset:2048 nt
	global_store_dwordx4 v251, v[8:11], s[42:43] nt
	global_store_dwordx4 v251, v[12:15], s[42:43] offset:2048 nt
	s_add_u32 s42, s42, 0x800000
	s_addc_u32 s43, s43, 0
	global_load_dwordx4 v[0:3], v246, s[4:5] nt
	global_load_dwordx4 v[4:7], v247, s[4:5] nt
	global_load_dwordx4 v[8:11], v248, s[4:5] nt
	global_load_dwordx4 v[12:15], v249, s[4:5] nt
	global_load_dwordx4 v[16:19], v246, s[6:7] nt
	global_load_dwordx4 v[20:23], v247, s[6:7] nt
	global_load_dwordx4 v[24:27], v248, s[6:7] nt
	global_load_dwordx4 v[28:31], v249, s[6:7] nt
	global_load_dwordx4 v[32:35], v246, s[8:9] nt
	global_load_dwordx4 v[36:39], v247, s[8:9] nt
	global_load_dwordx4 v[40:43], v248, s[8:9] nt
	global_load_dwordx4 v[44:47], v249, s[8:9] nt
	global_load_dwordx4 v[48:51], v246, s[38:39] nt
	global_load_dwordx4 v[52:55], v247, s[38:39] nt
	global_load_dwordx4 v[56:59], v248, s[38:39] nt
	global_load_dwordx4 v[60:63], v249, s[38:39] nt
	s_add_u32 s4, s4, 0x2000000
	s_addc_u32 s5, s5, 0
	s_add_u32 s6, s6, 0x2000000
	s_addc_u32 s7, s7, 0
	s_add_u32 s8, s8, 0x2000000
	s_addc_u32 s9, s9, 0
	s_add_u32 s38, s38, 0x2000000
	s_addc_u32 s39, s39, 0
	s_waitcnt vmcnt(40)
; #define GAS __attribute__((address_space(1)))
; template <bool GAIN, bool NT = false> __device__ __forceinline__ void titem8_load(const TItem& d, int lane, f32x4 (&r)[16], f32x4 (&g)[4]) {
;     const int q = lane & 7, kg = lane >> 3; const unsigned lo = (unsigned)((16 * kg) * d.N + 4 * q) * 4u;
;     const GAS char* base = (const GAS char*)d.src;
; #pragma unroll
;     for (int j = 0; j < 16; ++j) { const GAS f32x4* p = (const GAS f32x4*)(base + (size_t)j * (size_t)d.N * 4 + lo); r[j] = NT ? __builtin_nontemporal_load(p) : *p; }
; template <bool GAIN, bool NT = false> __device__ __forceinline__ void titem8_store(const TItem& d, int lane, const f32x4 (&r)[16], const f32x4 (&g)[4]) {
;     const int q = lane & 7, kg = lane >> 3; const unsigned lo = (unsigned)((4 * q) * d.ldk + 16 * kg);
;     GAS char* base = (GAS char*)d.dst;
;     f32x4 s[16];
; #pragma unroll
;     for (int j = 0; j < 16; ++j) s[j] = r[j] * ((GAIN ? g[j >> 2][j & 3] : 1.0f) * W8_SCALE);
; #pragma unroll
;     for (int i = 0; i < 4; ++i) { v4u w;
;         w.x = pk4_fp8w(s[0][i], s[1][i], s[2][i], s[3][i]); w.y = pk4_fp8w(s[4][i], s[5][i], s[6][i], s[7][i]);
;         w.z = pk4_fp8w(s[8][i], s[9][i], s[10][i], s[11][i]); w.w = pk4_fp8w(s[12][i], s[13][i], s[14][i], s[15][i]);
;         GAS v4u* p = (GAS v4u*)(base + (size_t)i * (size_t)d.ldk + lo);
;         if (NT) __builtin_nontemporal_store(w, p); else *p = w; }
	v_pk_mul_f32 v[66:67], v[66:67], s[30:31] op_sel_hi:[1,0]
	v_pk_mul_f32 v[68:69], v[68:69], s[30:31] op_sel_hi:[1,0]
	v_pk_mul_f32 v[70:71], v[70:71], s[30:31] op_sel_hi:[1,0]
	v_pk_mul_f32 v[72:73], v[72:73], s[30:31] op_sel_hi:[1,0]
	v_pk_mul_f32 v[74:75], v[74:75], s[30:31] op_sel_hi:[1,0]
	v_pk_mul_f32 v[76:77], v[76:77], s[30:31] op_sel_hi:[1,0]
	v_pk_mul_f32 v[78:79], v[78:79], s[30:31] op_sel_hi:[1,0]
	v_pk_mul_f32 v[80:81], v[80:81], s[30:31] op_sel_hi:[1,0]
	v_pk_mul_f32 v[82:83], v[82:83], s[30:31] op_sel_hi:[1,0]
	v_pk_mul_f32 v[84:85], v[84:85], s[30:31] op_sel_hi:[1,0]
	v_pk_mul_f32 v[86:87], v[86:87], s[30:31] op_sel_hi:[1,0]
	v_pk_mul_f32 v[88:89], v[88:89], s[30:31] op_sel_hi:[1,0]
	v_pk_mul_f32 v[90:91], v[90:91], s[30:31] op_sel_hi:[1,0]
	v_pk_mul_f32 v[92:93], v[92:93], s[30:31] op_sel_hi:[1,0]
	v_pk_mul_f32 v[94:95], v[94:95], s[30:31] op_sel_hi:[1,0]
	v_pk_mul_f32 v[96:97], v[96:97], s[30:31] op_sel_hi:[1,0]
	v_pk_mul_f32 v[98:99], v[98:99], s[30:31] op_sel_hi:[1,0]
	v_pk_mul_f32 v[100:101], v[100:101], s[30:31] op_sel_hi:[1,0]
	v_pk_mul_f32 v[102:103], v[102:103], s[30:31] op_sel_hi:[1,0]
	v_pk_mul_f32 v[104:105], v[104:105], s[30:31] op_sel_hi:[1,0]
	v_pk_mul_f32 v[106:107], v[106:107], s[30:31] op_sel_hi:[1,0]
	v_pk_mul_f32 v[108:109], v[108:109], s[30:31] op_sel_hi:[1,0]
	v_pk_mul_f32 v[110:111], v[110:111], s[30:31] op_sel_hi:[1,0]
	v_pk_mul_f32 v[112:113], v[112:113], s[30:31] op_sel_hi:[1,0]
	v_pk_mul_f32 v[114:115], v[114:115], s[30:31] op_sel_hi:[1,0]
	v_pk_mul_f32 v[116:117], v[116:117], s[30:31] op_sel_hi:[1,0]
	v_pk_mul_f32 v[118:119], v[118:119], s[30:31] op_sel_hi:[1,0]
	v_pk_mul_f32 v[120:121], v[120:121], s[30:31] op_sel_hi:[1,0]
	v_pk_mul_f32 v[122:123], v[122:123], s[30:31] op_sel_hi:[1,0]
	v_pk_mul_f32 v[124:125], v[124:125], s[30:31] op_sel_hi:[1,0]
	v_pk_mul_f32 v[126:127], v[126:127], s[30:31] op_sel_hi:[1,0]
	v_pk_mul_f32 v[128:129], v[128:129], s[30:31] op_sel_hi:[1,0]
	v_med3_f32 v66, v66, s24, v237
	v_med3_f32 v67, v67, s24, v237
	v_med3_f32 v68, v68, s24, v237
	v_med3_f32 v69, v69, s24, v237
	v_med3_f32 v70, v70, s24, v237
	v_med3_f32 v71, v71, s24, v237
	v_med3_f32 v72, v72, s24, v237
	v_med3_f32 v73, v73, s24, v237
	v_med3_f32 v74, v74, s24, v237
	v_med3_f32 v75, v75, s24, v237
	v_med3_f32 v76, v76, s24, v237
	v_med3_f32 v77, v77, s24, v237
	v_med3_f32 v78, v78, s24, v237
	v_med3_f32 v79, v79, s24, v237
	v_med3_f32 v80, v80, s24, v237
	v_med3_f32 v81, v81, s24, v237
	v_med3_f32 v82, v82, s24, v237
	v_med3_f32 v83, v83, s24, v237
	v_med3_f32 v84, v84, s24, v237
	v_med3_f32 v85, v85, s24, v237
	v_med3_f32 v86, v86, s24, v237
	v_med3_f32 v87, v87, s24, v237
	v_med3_f32 v88, v88, s24, v237
	v_med3_f32 v89, v89, s24, v237
	v_med3_f32 v90, v90, s24, v237
	v_med3_f32 v91, v91, s24, v237
	v_med3_f32 v92, v92, s24, v237
	v_med3_f32 v93, v93, s24, v237
	v_med3_f32 v94, v94, s24, v237
	v_med3_f32 v95, v95, s24, v237
	v_med3_f32 v96, v96, s24, v237
	v_med3_f32 v97, v97, s24, v237
	v_med3_f32 v98, v98, s24, v237
	v_med3_f32 v99, v99, s24, v237
	v_med3_f32 v100, v100, s24, v237
	v_med3_f32 v101, v101, s24, v237
	v_med3_f32 v102, v102, s24, v237
	v_med3_f32 v103, v103, s24, v237
	v_med3_f32 v104, v104, s24, v237
	v_med3_f32 v105, v105, s24, v237
	v_med3_f32 v106, v106, s24, v237
	v_med3_f32 v107, v107, s24, v237
	v_med3_f32 v108, v108, s24, v237
	v_med3_f32 v109, v109, s24, v237
	v_med3_f32 v110, v110, s24, v237
	v_med3_f32 v111, v111, s24, v237
	v_med3_f32 v112, v112, s24, v237
	v_med3_f32 v113, v113, s24, v237
	v_med3_f32 v114, v114, s24, v237
	v_med3_f32 v115, v115, s24, v237
	v_med3_f32 v116, v116, s24, v237
	v_med3_f32 v117, v117, s24, v237
	v_med3_f32 v118, v118, s24, v237
	v_med3_f32 v119, v119, s24, v237
	v_med3_f32 v120, v120, s24, v237
	v_med3_f32 v121, v121, s24, v237
	v_med3_f32 v122, v122, s24, v237
	v_med3_f32 v123, v123, s24, v237
	v_med3_f32 v124, v124, s24, v237
	v_med3_f32 v125, v125, s24, v237
	v_med3_f32 v126, v126, s24, v237
	v_med3_f32 v127, v127, s24, v237
	v_med3_f32 v128, v128, s24, v237
	v_med3_f32 v129, v129, s24, v237
	v_cvt_pk_fp8_f32 v66, v66, v70
	v_cvt_pk_fp8_f32 v66, v74, v78 op_sel:[0,0,1]
	v_cvt_pk_fp8_f32 v70, v67, v71
	v_cvt_pk_fp8_f32 v70, v75, v79 op_sel:[0,0,1]
	v_cvt_pk_fp8_f32 v74, v68, v72
	v_cvt_pk_fp8_f32 v74, v76, v80 op_sel:[0,0,1]
	v_cvt_pk_fp8_f32 v78, v69, v73
	v_cvt_pk_fp8_f32 v78, v77, v81 op_sel:[0,0,1]
	v_cvt_pk_fp8_f32 v67, v82, v86
	v_cvt_pk_fp8_f32 v67, v90, v94 op_sel:[0,0,1]
	v_cvt_pk_fp8_f32 v71, v83, v87
	v_cvt_pk_fp8_f32 v71, v91, v95 op_sel:[0,0,1]
	v_cvt_pk_fp8_f32 v75, v84, v88
	v_cvt_pk_fp8_f32 v75, v92, v96 op_sel:[0,0,1]
	v_cvt_pk_fp8_f32 v79, v85, v89
	v_cvt_pk_fp8_f32 v79, v93, v97 op_sel:[0,0,1]
	v_cvt_pk_fp8_f32 v68, v98, v102
	v_cvt_pk_fp8_f32 v68, v106, v110 op_sel:[0,0,1]
	v_cvt_pk_fp8_f32 v72, v99, v103
	v_cvt_pk_fp8_f32 v72, v107, v111 op_sel:[0,0,1]
	v_cvt_pk_fp8_f32 v76, v100, v104
	v_cvt_pk_fp8_f32 v76, v108, v112 op_sel:[0,0,1]
	v_cvt_pk_fp8_f32 v80, v101, v105
	v_cvt_pk_fp8_f32 v80, v109, v113 op_sel:[0,0,1]
	v_cvt_pk_fp8_f32 v69, v114, v118
	v_cvt_pk_fp8_f32 v69, v122, v126 op_sel:[0,0,1]
	v_cvt_pk_fp8_f32 v73, v115, v119
	v_cvt_pk_fp8_f32 v73, v123, v127 op_sel:[0,0,1]
	v_cvt_pk_fp8_f32 v77, v116, v120
	v_cvt_pk_fp8_f32 v77, v124, v128 op_sel:[0,0,1]
	v_cvt_pk_fp8_f32 v81, v117, v121
	v_cvt_pk_fp8_f32 v81, v125, v129 op_sel:[0,0,1]
	global_store_dwordx4 v250, v[66:69], s[42:43] nt
	global_store_dwordx4 v250, v[70:73], s[42:43] offset:2048 nt
	global_store_dwordx4 v251, v[74:77], s[42:43] nt
	global_store_dwordx4 v251, v[78:81], s[42:43] offset:2048 nt
	s_add_u32 s42, s42, 0x800000
	s_addc_u32 s43, s43, 0
	global_load_dwordx4 v[66:69], v246, s[4:5] nt
	global_load_dwordx4 v[70:73], v247, s[4:5] nt
	global_load_dwordx4 v[74:77], v248, s[4:5] nt
	global_load_dwordx4 v[78:81], v249, s[4:5] nt
	global_load_dwordx4 v[82:85], v246, s[6:7] nt
	global_load_dwordx4 v[86:89], v247, s[6:7] nt
	global_load_dwordx4 v[90:93], v248, s[6:7] nt
	global_load_dwordx4 v[94:97], v249, s[6:7] nt
	global_load_dwordx4 v[98:101], v246, s[8:9] nt
	global_load_dwordx4 v[102:105], v247, s[8:9] nt
	global_load_dwordx4 v[106:109], v248, s[8:9] nt
	global_load_dwordx4 v[110:113], v249, s[8:9] nt
	global_load_dwordx4 v[114:117], v246, s[38:39] nt
	global_load_dwordx4 v[118:121], v247, s[38:39] nt
	global_load_dwordx4 v[122:125], v248, s[38:39] nt
	global_load_dwordx4 v[126:129], v249, s[38:39] nt
	s_add_u32 s4, s4, 0x2000000
	s_addc_u32 s5, s5, 0
	s_add_u32 s6, s6, 0x2000000
	s_addc_u32 s7, s7, 0
	s_add_u32 s8, s8, 0x2000000
	s_addc_u32 s9, s9, 0
	s_add_u32 s38, s38, 0x2000000
	s_addc_u32 s39, s39, 0
	s_waitcnt vmcnt(40)
; #define GAS __attribute__((address_space(1)))
; template <bool GAIN, bool NT = false> __device__ __forceinline__ void titem8_load(const TItem& d, int lane, f32x4 (&r)[16], f32x4 (&g)[4]) {
;     const int q = lane & 7, kg = lane >> 3; const unsigned lo = (unsigned)((16 * kg) * d.N + 4 * q) * 4u;
;     const GAS char* base = (const GAS char*)d.src;
; #pragma unroll
;     for (int j = 0; j < 16; ++j) { const GAS f32x4* p = (const GAS f32x4*)(base + (size_t)j * (size_t)d.N * 4 + lo); r[j] = NT ? __builtin_nontemporal_load(p) : *p; }
; template <bool GAIN, bool NT = false> __device__ __forceinline__ void titem8_store(const TItem& d, int lane, const f32x4 (&r)[16], const f32x4 (&g)[4]) {
;     const int q = lane & 7, kg = lane >> 3; const unsigned lo = (unsigned)((4 * q) * d.ldk + 16 * kg);
;     GAS char* base = (GAS char*)d.dst;
;     f32x4 s[16];
; #pragma unroll
;     for (int j = 0; j < 16; ++j) s[j] = r[j] * ((GAIN ? g[j >> 2][j & 3] : 1.0f) * W8_SCALE);
; #pragma unroll
;     for (int i = 0; i < 4; ++i) { v4u w;
;         w.x = pk4_fp8w(s[0][i], s[1][i], s[2][i], s[3][i]); w.y = pk4_fp8w(s[4][i], s[5][i], s[6][i], s[7][i]);
;         w.z = pk4_fp8w(s[8][i], s[9][i], s[10][i], s[11][i]); w.w = pk4_fp8w(s[12][i], s[13][i], s[14][i], s[15][i]);
;         GAS v4u* p = (GAS v4u*)(base + (size_t)i * (size_t)d.ldk + lo);
;         if (NT) __builtin_nontemporal_store(w, p); else *p = w; }
	v_pk_mul_f32 v[130:131], v[130:131], s[30:31] op_sel_hi:[1,0]
	v_pk_mul_f32 v[132:133], v[132:133], s[30:31] op_sel_hi:[1,0]
	v_pk_mul_f32 v[134:135], v[134:135], s[30:31] op_sel_hi:[1,0]
	v_pk_mul_f32 v[136:137], v[136:137], s[30:31] op_sel_hi:[1,0]
	v_pk_mul_f32 v[138:139], v[138:139], s[30:31] op_sel_hi:[1,0]
	v_pk_mul_f32 v[140:141], v[140:141], s[30:31] op_sel_hi:[1,0]
	v_pk_mul_f32 v[142:143], v[142:143], s[30:31] op_sel_hi:[1,0]
	v_pk_mul_f32 v[144:145], v[144:145], s[30:31] op_sel_hi:[1,0]
	v_pk_mul_f32 v[146:147], v[146:147], s[30:31] op_sel_hi:[1,0]
	v_pk_mul_f32 v[148:149], v[148:149], s[30:31] op_sel_hi:[1,0]
	v_pk_mul_f32 v[150:151], v[150:151], s[30:31] op_sel_hi:[1,0]
	v_pk_mul_f32 v[152:153], v[152:153], s[30:31] op_sel_hi:[1,0]
	v_pk_mul_f32 v[154:155], v[154:155], s[30:31] op_sel_hi:[1,0]
	v_pk_mul_f32 v[156:157], v[156:157], s[30:31] op_sel_hi:[1,0]
	v_pk_mul_f32 v[158:159], v[158:159], s[30:31] op_sel_hi:[1,0]
	v_pk_mul_f32 v[160:161], v[160:161], s[30:31] op_sel_hi:[1,0]
	v_pk_mul_f32 v[162:163], v[162:163], s[30:31] op_sel_hi:[1,0]
	v_pk_mul_f32 v[164:165], v[164:165], s[30:31] op_sel_hi:[1,0]
	v_pk_mul_f32 v[166:167], v[166:167], s[30:31] op_sel_hi:[1,0]
	v_pk_mul_f32 v[168:169], v[168:169], s[30:31] op_sel_hi:[1,0]
	v_pk_mul_f32 v[170:171], v[170:171], s[30:31] op_sel_hi:[1,0]
	v_pk_mul_f32 v[172:173], v[172:173], s[30:31] op_sel_hi:[1,0]
	v_pk_mul_f32 v[174:175], v[174:175], s[30:31] op_sel_hi:[1,0]
	v_pk_mul_f32 v[176:177], v[176:177], s[30:31] op_sel_hi:[1,0]
	v_pk_mul_f32 v[178:179], v[178:179], s[30:31] op_sel_hi:[1,0]
	v_pk_mul_f32 v[180:181], v[180:181], s[30:31] op_sel_hi:[1,0]
	v_pk_mul_f32 v[182:183], v[182:183], s[30:31] op_sel_hi:[1,0]
	v_pk_mul_f32 v[184:185], v[184:185], s[30:31] op_sel_hi:[1,0]
	v_pk_mul_f32 v[186:187], v[186:187], s[30:31] op_sel_hi:[1,0]
	v_pk_mul_f32 v[188:189], v[188:189], s[30:31] op_sel_hi:[1,0]
	v_pk_mul_f32 v[190:191], v[190:191], s[30:31] op_sel_hi:[1,0]
	v_pk_mul_f32 v[192:193], v[192:193], s[30:31] op_sel_hi:[1,0]
	v_med3_f32 v130, v130, s24, v237
	v_med3_f32 v131, v131, s24, v237
	v_med3_f32 v132, v132, s24, v237
	v_med3_f32 v133, v133, s24, v237
	v_med3_f32 v134, v134, s24, v237
	v_med3_f32 v135, v135, s24, v237
	v_med3_f32 v136, v136, s24, v237
	v_med3_f32 v137, v137, s24, v237
	v_med3_f32 v138, v138, s24, v237
	v_med3_f32 v139, v139, s24, v237
	v_med3_f32 v140, v140, s24, v237
	v_med3_f32 v141, v141, s24, v237
	v_med3_f32 v142, v142, s24, v237
	v_med3_f32 v143, v143, s24, v237
	v_med3_f32 v144, v144, s24, v237
	v_med3_f32 v145, v145, s24, v237
	v_med3_f32 v146, v146, s24, v237
	v_med3_f32 v147, v147, s24, v237
	v_med3_f32 v148, v148, s24, v237
	v_med3_f32 v149, v149, s24, v237
	v_med3_f32 v150, v150, s24, v237
	v_med3_f32 v151, v151, s24, v237
	v_med3_f32 v152, v152, s24, v237
	v_med3_f32 v153, v153, s24, v237
	v_med3_f32 v154, v154, s24, v237
	v_med3_f32 v155, v155, s24, v237
	v_med3_f32 v156, v156, s24, v237
	v_med3_f32 v157, v157, s24, v237
	v_med3_f32 v158, v158, s24, v237
	v_med3_f32 v159, v159, s24, v237
	v_med3_f32 v160, v160, s24, v237
	v_med3_f32 v161, v161, s24, v237
	v_med3_f32 v162, v162, s24, v237
	v_med3_f32 v163, v163, s24, v237
	v_med3_f32 v164, v164, s24, v237
	v_med3_f32 v165, v165, s24, v237
	v_med3_f32 v166, v166, s24, v237
	v_med3_f32 v167, v167, s24, v237
	v_med3_f32 v168, v168, s24, v237
	v_med3_f32 v169, v169, s24, v237
	v_med3_f32 v170, v170, s24, v237
	v_med3_f32 v171, v171, s24, v237
	v_med3_f32 v172, v172, s24, v237
	v_med3_f32 v173, v173, s24, v237
	v_med3_f32 v174, v174, s24, v237
	v_med3_f32 v175, v175, s24, v237
	v_med3_f32 v176, v176, s24, v237
	v_med3_f32 v177, v177, s24, v237
	v_med3_f32 v178, v178, s24, v237
	v_med3_f32 v179, v179, s24, v237
	v_med3_f32 v180, v180, s24, v237
	v_med3_f32 v181, v181, s24, v237
	v_med3_f32 v182, v182, s24, v237
	v_med3_f32 v183, v183, s24, v237
	v_med3_f32 v184, v184, s24, v237
	v_med3_f32 v185, v185, s24, v237
	v_med3_f32 v186, v186, s24, v237
	v_med3_f32 v187, v187, s24, v237
	v_med3_f32 v188, v188, s24, v237
	v_med3_f32 v189, v189, s24, v237
	v_med3_f32 v190, v190, s24, v237
	v_med3_f32 v191, v191, s24, v237
	v_med3_f32 v192, v192, s24, v237
	v_med3_f32 v193, v193, s24, v237
	v_cvt_pk_fp8_f32 v130, v130, v134
	v_cvt_pk_fp8_f32 v130, v138, v142 op_sel:[0,0,1]
	v_cvt_pk_fp8_f32 v134, v131, v135
	v_cvt_pk_fp8_f32 v134, v139, v143 op_sel:[0,0,1]
	v_cvt_pk_fp8_f32 v138, v132, v136
	v_cvt_pk_fp8_f32 v138, v140, v144 op_sel:[0,0,1]
	v_cvt_pk_fp8_f32 v142, v133, v137
	v_cvt_pk_fp8_f32 v142, v141, v145 op_sel:[0,0,1]
	v_cvt_pk_fp8_f32 v131, v146, v150
	v_cvt_pk_fp8_f32 v131, v154, v158 op_sel:[0,0,1]
	v_cvt_pk_fp8_f32 v135, v147, v151
	v_cvt_pk_fp8_f32 v135, v155, v159 op_sel:[0,0,1]
	v_cvt_pk_fp8_f32 v139, v148, v152
	v_cvt_pk_fp8_f32 v139, v156, v160 op_sel:[0,0,1]
	v_cvt_pk_fp8_f32 v143, v149, v153
	v_cvt_pk_fp8_f32 v143, v157, v161 op_sel:[0,0,1]
	v_cvt_pk_fp8_f32 v132, v162, v166
	v_cvt_pk_fp8_f32 v132, v170, v174 op_sel:[0,0,1]
	v_cvt_pk_fp8_f32 v136, v163, v167
	v_cvt_pk_fp8_f32 v136, v171, v175 op_sel:[0,0,1]
	v_cvt_pk_fp8_f32 v140, v164, v168
	v_cvt_pk_fp8_f32 v140, v172, v176 op_sel:[0,0,1]
	v_cvt_pk_fp8_f32 v144, v165, v169
	v_cvt_pk_fp8_f32 v144, v173, v177 op_sel:[0,0,1]
	v_cvt_pk_fp8_f32 v133, v178, v182
	v_cvt_pk_fp8_f32 v133, v186, v190 op_sel:[0,0,1]
	v_cvt_pk_fp8_f32 v137, v179, v183
	v_cvt_pk_fp8_f32 v137, v187, v191 op_sel:[0,0,1]
	v_cvt_pk_fp8_f32 v141, v180, v184
	v_cvt_pk_fp8_f32 v141, v188, v192 op_sel:[0,0,1]
	v_cvt_pk_fp8_f32 v145, v181, v185
	v_cvt_pk_fp8_f32 v145, v189, v193 op_sel:[0,0,1]
	global_store_dwordx4 v250, v[130:133], s[42:43] nt
	global_store_dwordx4 v250, v[134:137], s[42:43] offset:2048 nt
	global_store_dwordx4 v251, v[138:141], s[42:43] nt
	global_store_dwordx4 v251, v[142:145], s[42:43] offset:2048 nt
	s_add_u32 s42, s42, 0x800000
	s_addc_u32 s43, s43, 0
	global_load_dwordx4 v[130:133], v246, s[4:5] nt
	global_load_dwordx4 v[134:137], v247, s[4:5] nt
	global_load_dwordx4 v[138:141], v248, s[4:5] nt
	global_load_dwordx4 v[142:145], v249, s[4:5] nt
	global_load_dwordx4 v[146:149], v246, s[6:7] nt
	global_load_dwordx4 v[150:153], v247, s[6:7] nt
	global_load_dwordx4 v[154:157], v248, s[6:7] nt
	global_load_dwordx4 v[158:161], v249, s[6:7] nt
	global_load_dwordx4 v[162:165], v246, s[8:9] nt
	global_load_dwordx4 v[166:169], v247, s[8:9] nt
	global_load_dwordx4 v[170:173], v248, s[8:9] nt
	global_load_dwordx4 v[174:177], v249, s[8:9] nt
	global_load_dwordx4 v[178:181], v246, s[38:39] nt
	global_load_dwordx4 v[182:185], v247, s[38:39] nt
	global_load_dwordx4 v[186:189], v248, s[38:39] nt
	global_load_dwordx4 v[190:193], v249, s[38:39] nt
	s_add_u32 s4, s4, 0x2000000
	s_addc_u32 s5, s5, 0
	s_add_u32 s6, s6, 0x2000000
	s_addc_u32 s7, s7, 0
	s_add_u32 s8, s8, 0x2000000
	s_addc_u32 s9, s9, 0
	s_add_u32 s38, s38, 0x2000000
	s_addc_u32 s39, s39, 0
	s_waitcnt vmcnt(40)
; #define GAS __attribute__((address_space(1)))
; template <bool GAIN, bool NT = false> __device__ __forceinline__ void titem8_load(const TItem& d, int lane, f32x4 (&r)[16], f32x4 (&g)[4]) {
;     const int q = lane & 7, kg = lane >> 3; const unsigned lo = (unsigned)((16 * kg) * d.N + 4 * q) * 4u;
;     const GAS char* base = (const GAS char*)d.src;
; #pragma unroll
;     for (int j = 0; j < 16; ++j) { const GAS f32x4* p = (const GAS f32x4*)(base + (size_t)j * (size_t)d.N * 4 + lo); r[j] = NT ? __builtin_nontemporal_load(p) : *p; }
; template <bool GAIN, bool NT = false> __device__ __forceinline__ void titem8_store(const TItem& d, int lane, const f32x4 (&r)[16], const f32x4 (&g)[4]) {
;     const int q = lane & 7, kg = lane >> 3; const unsigned lo = (unsigned)((4 * q) * d.ldk + 16 * kg);
;     GAS char* base = (GAS char*)d.dst;
;     f32x4 s[16];
; #pragma unroll
;     for (int j = 0; j < 16; ++j) s[j] = r[j] * ((GAIN ? g[j >> 2][j & 3] : 1.0f) * W8_SCALE);
; #pragma unroll
;     for (int i = 0; i < 4; ++i) { v4u w;
;         w.x = pk4_fp8w(s[0][i], s[1][i], s[2][i], s[3][i]); w.y = pk4_fp8w(s[4][i], s[5][i], s[6][i], s[7][i]);
;         w.z = pk4_fp8w(s[8][i], s[9][i], s[10][i], s[11][i]); w.w = pk4_fp8w(s[12][i], s[13][i], s[14][i], s[15][i]);
;         GAS v4u* p = (GAS v4u*)(base + (size_t)i * (size_t)d.ldk + lo);
;         if (NT) __builtin_nontemporal_store(w, p); else *p = w; }
	v_pk_mul_f32 v[0:1], v[0:1], s[30:31] op_sel_hi:[1,0]
	v_pk_mul_f32 v[2:3], v[2:3], s[30:31] op_sel_hi:[1,0]
	v_pk_mul_f32 v[4:5], v[4:5], s[30:31] op_sel_hi:[1,0]
	v_pk_mul_f32 v[6:7], v[6:7], s[30:31] op_sel_hi:[1,0]
	v_pk_mul_f32 v[8:9], v[8:9], s[30:31] op_sel_hi:[1,0]
	v_pk_mul_f32 v[10:11], v[10:11], s[30:31] op_sel_hi:[1,0]
	v_pk_mul_f32 v[12:13], v[12:13], s[30:31] op_sel_hi:[1,0]
	v_pk_mul_f32 v[14:15], v[14:15], s[30:31] op_sel_hi:[1,0]
	v_pk_mul_f32 v[16:17], v[16:17], s[30:31] op_sel_hi:[1,0]
	v_pk_mul_f32 v[18:19], v[18:19], s[30:31] op_sel_hi:[1,0]
	v_pk_mul_f32 v[20:21], v[20:21], s[30:31] op_sel_hi:[1,0]
	v_pk_mul_f32 v[22:23], v[22:23], s[30:31] op_sel_hi:[1,0]
	v_pk_mul_f32 v[24:25], v[24:25], s[30:31] op_sel_hi:[1,0]
	v_pk_mul_f32 v[26:27], v[26:27], s[30:31] op_sel_hi:[1,0]
	v_pk_mul_f32 v[28:29], v[28:29], s[30:31] op_sel_hi:[1,0]
	v_pk_mul_f32 v[30:31], v[30:31], s[30:31] op_sel_hi:[1,0]
	v_pk_mul_f32 v[32:33], v[32:33], s[30:31] op_sel_hi:[1,0]
	v_pk_mul_f32 v[34:35], v[34:35], s[30:31] op_sel_hi:[1,0]
	v_pk_mul_f32 v[36:37], v[36:37], s[30:31] op_sel_hi:[1,0]
	v_pk_mul_f32 v[38:39], v[38:39], s[30:31] op_sel_hi:[1,0]
	v_pk_mul_f32 v[40:41], v[40:41], s[30:31] op_sel_hi:[1,0]
	v_pk_mul_f32 v[42:43], v[42:43], s[30:31] op_sel_hi:[1,0]
	v_pk_mul_f32 v[44:45], v[44:45], s[30:31] op_sel_hi:[1,0]
	v_pk_mul_f32 v[46:47], v[46:47], s[30:31] op_sel_hi:[1,0]
	v_pk_mul_f32 v[48:49], v[48:49], s[30:31] op_sel_hi:[1,0]
	v_pk_mul_f32 v[50:51], v[50:51], s[30:31] op_sel_hi:[1,0]
	v_pk_mul_f32 v[52:53], v[52:53], s[30:31] op_sel_hi:[1,0]
	v_pk_mul_f32 v[54:55], v[54:55], s[30:31] op_sel_hi:[1,0]
	v_pk_mul_f32 v[56:57], v[56:57], s[30:31] op_sel_hi:[1,0]
	v_pk_mul_f32 v[58:59], v[58:59], s[30:31] op_sel_hi:[1,0]
	v_pk_mul_f32 v[60:61], v[60:61], s[30:31] op_sel_hi:[1,0]
	v_pk_mul_f32 v[62:63], v[62:63], s[30:31] op_sel_hi:[1,0]
	v_med3_f32 v0, v0, s24, v237
	v_med3_f32 v1, v1, s24, v237
	v_med3_f32 v2, v2, s24, v237
	v_med3_f32 v3, v3, s24, v237
	v_med3_f32 v4, v4, s24, v237
	v_med3_f32 v5, v5, s24, v237
	v_med3_f32 v6, v6, s24, v237
	v_med3_f32 v7, v7, s24, v237
	v_med3_f32 v8, v8, s24, v237
	v_med3_f32 v9, v9, s24, v237
	v_med3_f32 v10, v10, s24, v237
	v_med3_f32 v11, v11, s24, v237
	v_med3_f32 v12, v12, s24, v237
	v_med3_f32 v13, v13, s24, v237
	v_med3_f32 v14, v14, s24, v237
	v_med3_f32 v15, v15, s24, v237
	v_med3_f32 v16, v16, s24, v237
	v_med3_f32 v17, v17, s24, v237
	v_med3_f32 v18, v18, s24, v237
	v_med3_f32 v19, v19, s24, v237
	v_med3_f32 v20, v20, s24, v237
	v_med3_f32 v21, v21, s24, v237
	v_med3_f32 v22, v22, s24, v237
	v_med3_f32 v23, v23, s24, v237
	v_med3_f32 v24, v24, s24, v237
	v_med3_f32 v25, v25, s24, v237
	v_med3_f32 v26, v26, s24, v237
	v_med3_f32 v27, v27, s24, v237
	v_med3_f32 v28, v28, s24, v237
	v_med3_f32 v29, v29, s24, v237
	v_med3_f32 v30, v30, s24, v237
	v_med3_f32 v31, v31, s24, v237
	v_med3_f32 v32, v32, s24, v237
	v_med3_f32 v33, v33, s24, v237
	v_med3_f32 v34, v34, s24, v237
	v_med3_f32 v35, v35, s24, v237
	v_med3_f32 v36, v36, s24, v237
	v_med3_f32 v37, v37, s24, v237
	v_med3_f32 v38, v38, s24, v237
	v_med3_f32 v39, v39, s24, v237
	v_med3_f32 v40, v40, s24, v237
	v_med3_f32 v41, v41, s24, v237
	v_med3_f32 v42, v42, s24, v237
	v_med3_f32 v43, v43, s24, v237
	v_med3_f32 v44, v44, s24, v237
	v_med3_f32 v45, v45, s24, v237
	v_med3_f32 v46, v46, s24, v237
	v_med3_f32 v47, v47, s24, v237
	v_med3_f32 v48, v48, s24, v237
	v_med3_f32 v49, v49, s24, v237
	v_med3_f32 v50, v50, s24, v237
	v_med3_f32 v51, v51, s24, v237
	v_med3_f32 v52, v52, s24, v237
	v_med3_f32 v53, v53, s24, v237
	v_med3_f32 v54, v54, s24, v237
	v_med3_f32 v55, v55, s24, v237
	v_med3_f32 v56, v56, s24, v237
	v_med3_f32 v57, v57, s24, v237
	v_med3_f32 v58, v58, s24, v237
	v_med3_f32 v59, v59, s24, v237
	v_med3_f32 v60, v60, s24, v237
	v_med3_f32 v61, v61, s24, v237
	v_med3_f32 v62, v62, s24, v237
	v_med3_f32 v63, v63, s24, v237
	v_cvt_pk_fp8_f32 v0, v0, v4
	v_cvt_pk_fp8_f32 v0, v8, v12 op_sel:[0,0,1]
	v_cvt_pk_fp8_f32 v4, v1, v5
	v_cvt_pk_fp8_f32 v4, v9, v13 op_sel:[0,0,1]
	v_cvt_pk_fp8_f32 v8, v2, v6
	v_cvt_pk_fp8_f32 v8, v10, v14 op_sel:[0,0,1]
	v_cvt_pk_fp8_f32 v12, v3, v7
	v_cvt_pk_fp8_f32 v12, v11, v15 op_sel:[0,0,1]
	v_cvt_pk_fp8_f32 v1, v16, v20
	v_cvt_pk_fp8_f32 v1, v24, v28 op_sel:[0,0,1]
	v_cvt_pk_fp8_f32 v5, v17, v21
	v_cvt_pk_fp8_f32 v5, v25, v29 op_sel:[0,0,1]
	v_cvt_pk_fp8_f32 v9, v18, v22
	v_cvt_pk_fp8_f32 v9, v26, v30 op_sel:[0,0,1]
	v_cvt_pk_fp8_f32 v13, v19, v23
	v_cvt_pk_fp8_f32 v13, v27, v31 op_sel:[0,0,1]
	v_cvt_pk_fp8_f32 v2, v32, v36
	v_cvt_pk_fp8_f32 v2, v40, v44 op_sel:[0,0,1]
	v_cvt_pk_fp8_f32 v6, v33, v37
	v_cvt_pk_fp8_f32 v6, v41, v45 op_sel:[0,0,1]
	v_cvt_pk_fp8_f32 v10, v34, v38
	v_cvt_pk_fp8_f32 v10, v42, v46 op_sel:[0,0,1]
	v_cvt_pk_fp8_f32 v14, v35, v39
	v_cvt_pk_fp8_f32 v14, v43, v47 op_sel:[0,0,1]
	v_cvt_pk_fp8_f32 v3, v48, v52
	v_cvt_pk_fp8_f32 v3, v56, v60 op_sel:[0,0,1]
	v_cvt_pk_fp8_f32 v7, v49, v53
	v_cvt_pk_fp8_f32 v7, v57, v61 op_sel:[0,0,1]
	v_cvt_pk_fp8_f32 v11, v50, v54
	v_cvt_pk_fp8_f32 v11, v58, v62 op_sel:[0,0,1]
	v_cvt_pk_fp8_f32 v15, v51, v55
	v_cvt_pk_fp8_f32 v15, v59, v63 op_sel:[0,0,1]
	global_store_dwordx4 v250, v[0:3], s[42:43] nt
	global_store_dwordx4 v250, v[4:7], s[42:43] offset:2048 nt
	global_store_dwordx4 v251, v[8:11], s[42:43] nt
	global_store_dwordx4 v251, v[12:15], s[42:43] offset:2048 nt
	s_add_u32 s42, s42, 0x800000
	s_addc_u32 s43, s43, 0
	global_load_dwordx4 v[0:3], v246, s[4:5] nt
	global_load_dwordx4 v[4:7], v247, s[4:5] nt
	global_load_dwordx4 v[8:11], v248, s[4:5] nt
	global_load_dwordx4 v[12:15], v249, s[4:5] nt
	global_load_dwordx4 v[16:19], v246, s[6:7] nt
	global_load_dwordx4 v[20:23], v247, s[6:7] nt
	global_load_dwordx4 v[24:27], v248, s[6:7] nt
	global_load_dwordx4 v[28:31], v249, s[6:7] nt
	global_load_dwordx4 v[32:35], v246, s[8:9] nt
	global_load_dwordx4 v[36:39], v247, s[8:9] nt
	global_load_dwordx4 v[40:43], v248, s[8:9] nt
	global_load_dwordx4 v[44:47], v249, s[8:9] nt
	global_load_dwordx4 v[48:51], v246, s[38:39] nt
	global_load_dwordx4 v[52:55], v247, s[38:39] nt
	global_load_dwordx4 v[56:59], v248, s[38:39] nt
	global_load_dwordx4 v[60:63], v249, s[38:39] nt
	s_add_u32 s4, s4, 0x2000000
	s_addc_u32 s5, s5, 0
	s_add_u32 s6, s6, 0x2000000
	s_addc_u32 s7, s7, 0
	s_add_u32 s8, s8, 0x2000000
	s_addc_u32 s9, s9, 0
	s_add_u32 s38, s38, 0x2000000
	s_addc_u32 s39, s39, 0
	s_waitcnt vmcnt(40)
; #define GAS __attribute__((address_space(1)))
; template <bool GAIN, bool NT = false> __device__ __forceinline__ void titem8_store(const TItem& d, int lane, const f32x4 (&r)[16], const f32x4 (&g)[4]) {
;     const int q = lane & 7, kg = lane >> 3; const unsigned lo = (unsigned)((4 * q) * d.ldk + 16 * kg);
;     GAS char* base = (GAS char*)d.dst;
;     f32x4 s[16];
; #pragma unroll
;     for (int j = 0; j < 16; ++j) s[j] = r[j] * ((GAIN ? g[j >> 2][j & 3] : 1.0f) * W8_SCALE);
; #pragma unroll
;     for (int i = 0; i < 4; ++i) { v4u w;
;         w.x = pk4_fp8w(s[0][i], s[1][i], s[2][i], s[3][i]); w.y = pk4_fp8w(s[4][i], s[5][i], s[6][i], s[7][i]);
;         w.z = pk4_fp8w(s[8][i], s[9][i], s[10][i], s[11][i]); w.w = pk4_fp8w(s[12][i], s[13][i], s[14][i], s[15][i]);
;         GAS v4u* p = (GAS v4u*)(base + (size_t)i * (size_t)d.ldk + lo);
;         if (NT) __builtin_nontemporal_store(w, p); else *p = w; }
	v_pk_mul_f32 v[66:67], v[66:67], s[30:31] op_sel_hi:[1,0]
	v_pk_mul_f32 v[68:69], v[68:69], s[30:31] op_sel_hi:[1,0]
	v_pk_mul_f32 v[70:71], v[70:71], s[30:31] op_sel_hi:[1,0]
	v_pk_mul_f32 v[72:73], v[72:73], s[30:31] op_sel_hi:[1,0]
	v_pk_mul_f32 v[74:75], v[74:75], s[30:31] op_sel_hi:[1,0]
	v_pk_mul_f32 v[76:77], v[76:77], s[30:31] op_sel_hi:[1,0]
	v_pk_mul_f32 v[78:79], v[78:79], s[30:31] op_sel_hi:[1,0]
	v_pk_mul_f32 v[80:81], v[80:81], s[30:31] op_sel_hi:[1,0]
	v_pk_mul_f32 v[82:83], v[82:83], s[30:31] op_sel_hi:[1,0]
	v_pk_mul_f32 v[84:85], v[84:85], s[30:31] op_sel_hi:[1,0]
	v_pk_mul_f32 v[86:87], v[86:87], s[30:31] op_sel_hi:[1,0]
	v_pk_mul_f32 v[88:89], v[88:89], s[30:31] op_sel_hi:[1,0]
	v_pk_mul_f32 v[90:91], v[90:91], s[30:31] op_sel_hi:[1,0]
	v_pk_mul_f32 v[92:93], v[92:93], s[30:31] op_sel_hi:[1,0]
	v_pk_mul_f32 v[94:95], v[94:95], s[30:31] op_sel_hi:[1,0]
	v_pk_mul_f32 v[96:97], v[96:97], s[30:31] op_sel_hi:[1,0]
	v_pk_mul_f32 v[98:99], v[98:99], s[30:31] op_sel_hi:[1,0]
	v_pk_mul_f32 v[100:101], v[100:101], s[30:31] op_sel_hi:[1,0]
	v_pk_mul_f32 v[102:103], v[102:103], s[30:31] op_sel_hi:[1,0]
	v_pk_mul_f32 v[104:105], v[104:105], s[30:31] op_sel_hi:[1,0]
	v_pk_mul_f32 v[106:107], v[106:107], s[30:31] op_sel_hi:[1,0]
	v_pk_mul_f32 v[108:109], v[108:109], s[30:31] op_sel_hi:[1,0]
	v_pk_mul_f32 v[110:111], v[110:111], s[30:31] op_sel_hi:[1,0]
	v_pk_mul_f32 v[112:113], v[112:113], s[30:31] op_sel_hi:[1,0]
	v_pk_mul_f32 v[114:115], v[114:115], s[30:31] op_sel_hi:[1,0]
	v_pk_mul_f32 v[116:117], v[116:117], s[30:31] op_sel_hi:[1,0]
	v_pk_mul_f32 v[118:119], v[118:119], s[30:31] op_sel_hi:[1,0]
	v_pk_mul_f32 v[120:121], v[120:121], s[30:31] op_sel_hi:[1,0]
	v_pk_mul_f32 v[122:123], v[122:123], s[30:31] op_sel_hi:[1,0]
	v_pk_mul_f32 v[124:125], v[124:125], s[30:31] op_sel_hi:[1,0]
	v_pk_mul_f32 v[126:127], v[126:127], s[30:31] op_sel_hi:[1,0]
	v_pk_mul_f32 v[128:129], v[128:129], s[30:31] op_sel_hi:[1,0]
	v_med3_f32 v66, v66, s24, v237
	v_med3_f32 v67, v67, s24, v237
	v_med3_f32 v68, v68, s24, v237
	v_med3_f32 v69, v69, s24, v237
	v_med3_f32 v70, v70, s24, v237
	v_med3_f32 v71, v71, s24, v237
	v_med3_f32 v72, v72, s24, v237
	v_med3_f32 v73, v73, s24, v237
	v_med3_f32 v74, v74, s24, v237
	v_med3_f32 v75, v75, s24, v237
	v_med3_f32 v76, v76, s24, v237
	v_med3_f32 v77, v77, s24, v237
	v_med3_f32 v78, v78, s24, v237
	v_med3_f32 v79, v79, s24, v237
	v_med3_f32 v80, v80, s24, v237
	v_med3_f32 v81, v81, s24, v237
	v_med3_f32 v82, v82, s24, v237
	v_med3_f32 v83, v83, s24, v237
	v_med3_f32 v84, v84, s24, v237
	v_med3_f32 v85, v85, s24, v237
	v_med3_f32 v86, v86, s24, v237
	v_med3_f32 v87, v87, s24, v237
	v_med3_f32 v88, v88, s24, v237
	v_med3_f32 v89, v89, s24, v237
	v_med3_f32 v90, v90, s24, v237
	v_med3_f32 v91, v91, s24, v237
	v_med3_f32 v92, v92, s24, v237
	v_med3_f32 v93, v93, s24, v237
	v_med3_f32 v94, v94, s24, v237
	v_med3_f32 v95, v95, s24, v237
	v_med3_f32 v96, v96, s24, v237
	v_med3_f32 v97, v97, s24, v237
	v_med3_f32 v98, v98, s24, v237
	v_med3_f32 v99, v99, s24, v237
	v_med3_f32 v100, v100, s24, v237
	v_med3_f32 v101, v101, s24, v237
	v_med3_f32 v102, v102, s24, v237
	v_med3_f32 v103, v103, s24, v237
	v_med3_f32 v104, v104, s24, v237
	v_med3_f32 v105, v105, s24, v237
	v_med3_f32 v106, v106, s24, v237
	v_med3_f32 v107, v107, s24, v237
	v_med3_f32 v108, v108, s24, v237
	v_med3_f32 v109, v109, s24, v237
	v_med3_f32 v110, v110, s24, v237
	v_med3_f32 v111, v111, s24, v237
	v_med3_f32 v112, v112, s24, v237
	v_med3_f32 v113, v113, s24, v237
	v_med3_f32 v114, v114, s24, v237
	v_med3_f32 v115, v115, s24, v237
	v_med3_f32 v116, v116, s24, v237
	v_med3_f32 v117, v117, s24, v237
	v_med3_f32 v118, v118, s24, v237
	v_med3_f32 v119, v119, s24, v237
	v_med3_f32 v120, v120, s24, v237
	v_med3_f32 v121, v121, s24, v237
	v_med3_f32 v122, v122, s24, v237
	v_med3_f32 v123, v123, s24, v237
	v_med3_f32 v124, v124, s24, v237
	v_med3_f32 v125, v125, s24, v237
	v_med3_f32 v126, v126, s24, v237
	v_med3_f32 v127, v127, s24, v237
	v_med3_f32 v128, v128, s24, v237
	v_med3_f32 v129, v129, s24, v237
	v_cvt_pk_fp8_f32 v66, v66, v70
	v_cvt_pk_fp8_f32 v66, v74, v78 op_sel:[0,0,1]
	v_cvt_pk_fp8_f32 v70, v67, v71
	v_cvt_pk_fp8_f32 v70, v75, v79 op_sel:[0,0,1]
	v_cvt_pk_fp8_f32 v74, v68, v72
	v_cvt_pk_fp8_f32 v74, v76, v80 op_sel:[0,0,1]
	v_cvt_pk_fp8_f32 v78, v69, v73
	v_cvt_pk_fp8_f32 v78, v77, v81 op_sel:[0,0,1]
	v_cvt_pk_fp8_f32 v67, v82, v86
	v_cvt_pk_fp8_f32 v67, v90, v94 op_sel:[0,0,1]
	v_cvt_pk_fp8_f32 v71, v83, v87
	v_cvt_pk_fp8_f32 v71, v91, v95 op_sel:[0,0,1]
	v_cvt_pk_fp8_f32 v75, v84, v88
	v_cvt_pk_fp8_f32 v75, v92, v96 op_sel:[0,0,1]
	v_cvt_pk_fp8_f32 v79, v85, v89
	v_cvt_pk_fp8_f32 v79, v93, v97 op_sel:[0,0,1]
	v_cvt_pk_fp8_f32 v68, v98, v102
	v_cvt_pk_fp8_f32 v68, v106, v110 op_sel:[0,0,1]
	v_cvt_pk_fp8_f32 v72, v99, v103
	v_cvt_pk_fp8_f32 v72, v107, v111 op_sel:[0,0,1]
	v_cvt_pk_fp8_f32 v76, v100, v104
	v_cvt_pk_fp8_f32 v76, v108, v112 op_sel:[0,0,1]
	v_cvt_pk_fp8_f32 v80, v101, v105
	v_cvt_pk_fp8_f32 v80, v109, v113 op_sel:[0,0,1]
	v_cvt_pk_fp8_f32 v69, v114, v118
	v_cvt_pk_fp8_f32 v69, v122, v126 op_sel:[0,0,1]
	v_cvt_pk_fp8_f32 v73, v115, v119
	v_cvt_pk_fp8_f32 v73, v123, v127 op_sel:[0,0,1]
	v_cvt_pk_fp8_f32 v77, v116, v120
	v_cvt_pk_fp8_f32 v77, v124, v128 op_sel:[0,0,1]
	v_cvt_pk_fp8_f32 v81, v117, v121
	v_cvt_pk_fp8_f32 v81, v125, v129 op_sel:[0,0,1]
	global_store_dwordx4 v250, v[66:69], s[42:43] nt
	global_store_dwordx4 v250, v[70:73], s[42:43] offset:2048 nt
	global_store_dwordx4 v251, v[74:77], s[42:43] nt
	global_store_dwordx4 v251, v[78:81], s[42:43] offset:2048 nt
	s_add_u32 s42, s42, 0x800000
	s_addc_u32 s43, s43, 0
	s_waitcnt vmcnt(24)
; #define GAS __attribute__((address_space(1)))
; template <bool GAIN, bool NT = false> __device__ __forceinline__ void titem8_store(const TItem& d, int lane, const f32x4 (&r)[16], const f32x4 (&g)[4]) {
;     const int q = lane & 7, kg = lane >> 3; const unsigned lo = (unsigned)((4 * q) * d.ldk + 16 * kg);
;     GAS char* base = (GAS char*)d.dst;
;     f32x4 s[16];
; #pragma unroll
;     for (int j = 0; j < 16; ++j) s[j] = r[j] * ((GAIN ? g[j >> 2][j & 3] : 1.0f) * W8_SCALE);
; #pragma unroll
;     for (int i = 0; i < 4; ++i) { v4u w;
;         w.x = pk4_fp8w(s[0][i], s[1][i], s[2][i], s[3][i]); w.y = pk4_fp8w(s[4][i], s[5][i], s[6][i], s[7][i]);
;         w.z = pk4_fp8w(s[8][i], s[9][i], s[10][i], s[11][i]); w.w = pk4_fp8w(s[12][i], s[13][i], s[14][i], s[15][i]);
;         GAS v4u* p = (GAS v4u*)(base + (size_t)i * (size_t)d.ldk + lo);
;         if (NT) __builtin_nontemporal_store(w, p); else *p = w; }
	v_pk_mul_f32 v[130:131], v[130:131], s[30:31] op_sel_hi:[1,0]
	v_pk_mul_f32 v[132:133], v[132:133], s[30:31] op_sel_hi:[1,0]
	v_pk_mul_f32 v[134:135], v[134:135], s[30:31] op_sel_hi:[1,0]
	v_pk_mul_f32 v[136:137], v[136:137], s[30:31] op_sel_hi:[1,0]
	v_pk_mul_f32 v[138:139], v[138:139], s[30:31] op_sel_hi:[1,0]
	v_pk_mul_f32 v[140:141], v[140:141], s[30:31] op_sel_hi:[1,0]
	v_pk_mul_f32 v[142:143], v[142:143], s[30:31] op_sel_hi:[1,0]
	v_pk_mul_f32 v[144:145], v[144:145], s[30:31] op_sel_hi:[1,0]
	v_pk_mul_f32 v[146:147], v[146:147], s[30:31] op_sel_hi:[1,0]
	v_pk_mul_f32 v[148:149], v[148:149], s[30:31] op_sel_hi:[1,0]
	v_pk_mul_f32 v[150:151], v[150:151], s[30:31] op_sel_hi:[1,0]
	v_pk_mul_f32 v[152:153], v[152:153], s[30:31] op_sel_hi:[1,0]
	v_pk_mul_f32 v[154:155], v[154:155], s[30:31] op_sel_hi:[1,0]
	v_pk_mul_f32 v[156:157], v[156:157], s[30:31] op_sel_hi:[1,0]
	v_pk_mul_f32 v[158:159], v[158:159], s[30:31] op_sel_hi:[1,0]
	v_pk_mul_f32 v[160:161], v[160:161], s[30:31] op_sel_hi:[1,0]
	v_pk_mul_f32 v[162:163], v[162:163], s[30:31] op_sel_hi:[1,0]
	v_pk_mul_f32 v[164:165], v[164:165], s[30:31] op_sel_hi:[1,0]
	v_pk_mul_f32 v[166:167], v[166:167], s[30:31] op_sel_hi:[1,0]
	v_pk_mul_f32 v[168:169], v[168:169], s[30:31] op_sel_hi:[1,0]
	v_pk_mul_f32 v[170:171], v[170:171], s[30:31] op_sel_hi:[1,0]
	v_pk_mul_f32 v[172:173], v[172:173], s[30:31] op_sel_hi:[1,0]
	v_pk_mul_f32 v[174:175], v[174:175], s[30:31] op_sel_hi:[1,0]
	v_pk_mul_f32 v[176:177], v[176:177], s[30:31] op_sel_hi:[1,0]
	v_pk_mul_f32 v[178:179], v[178:179], s[30:31] op_sel_hi:[1,0]
	v_pk_mul_f32 v[180:181], v[180:181], s[30:31] op_sel_hi:[1,0]
	v_pk_mul_f32 v[182:183], v[182:183], s[30:31] op_sel_hi:[1,0]
	v_pk_mul_f32 v[184:185], v[184:185], s[30:31] op_sel_hi:[1,0]
	v_pk_mul_f32 v[186:187], v[186:187], s[30:31] op_sel_hi:[1,0]
	v_pk_mul_f32 v[188:189], v[188:189], s[30:31] op_sel_hi:[1,0]
	v_pk_mul_f32 v[190:191], v[190:191], s[30:31] op_sel_hi:[1,0]
	v_pk_mul_f32 v[192:193], v[192:193], s[30:31] op_sel_hi:[1,0]
	v_med3_f32 v130, v130, s24, v237
	v_med3_f32 v131, v131, s24, v237
	v_med3_f32 v132, v132, s24, v237
	v_med3_f32 v133, v133, s24, v237
	v_med3_f32 v134, v134, s24, v237
	v_med3_f32 v135, v135, s24, v237
	v_med3_f32 v136, v136, s24, v237
	v_med3_f32 v137, v137, s24, v237
	v_med3_f32 v138, v138, s24, v237
	v_med3_f32 v139, v139, s24, v237
	v_med3_f32 v140, v140, s24, v237
	v_med3_f32 v141, v141, s24, v237
	v_med3_f32 v142, v142, s24, v237
	v_med3_f32 v143, v143, s24, v237
	v_med3_f32 v144, v144, s24, v237
	v_med3_f32 v145, v145, s24, v237
	v_med3_f32 v146, v146, s24, v237
	v_med3_f32 v147, v147, s24, v237
	v_med3_f32 v148, v148, s24, v237
	v_med3_f32 v149, v149, s24, v237
	v_med3_f32 v150, v150, s24, v237
	v_med3_f32 v151, v151, s24, v237
	v_med3_f32 v152, v152, s24, v237
	v_med3_f32 v153, v153, s24, v237
	v_med3_f32 v154, v154, s24, v237
	v_med3_f32 v155, v155, s24, v237
	v_med3_f32 v156, v156, s24, v237
	v_med3_f32 v157, v157, s24, v237
	v_med3_f32 v158, v158, s24, v237
	v_med3_f32 v159, v159, s24, v237
	v_med3_f32 v160, v160, s24, v237
	v_med3_f32 v161, v161, s24, v237
	v_med3_f32 v162, v162, s24, v237
	v_med3_f32 v163, v163, s24, v237
	v_med3_f32 v164, v164, s24, v237
	v_med3_f32 v165, v165, s24, v237
	v_med3_f32 v166, v166, s24, v237
	v_med3_f32 v167, v167, s24, v237
	v_med3_f32 v168, v168, s24, v237
	v_med3_f32 v169, v169, s24, v237
	v_med3_f32 v170, v170, s24, v237
	v_med3_f32 v171, v171, s24, v237
	v_med3_f32 v172, v172, s24, v237
	v_med3_f32 v173, v173, s24, v237
	v_med3_f32 v174, v174, s24, v237
	v_med3_f32 v175, v175, s24, v237
	v_med3_f32 v176, v176, s24, v237
	v_med3_f32 v177, v177, s24, v237
	v_med3_f32 v178, v178, s24, v237
	v_med3_f32 v179, v179, s24, v237
	v_med3_f32 v180, v180, s24, v237
	v_med3_f32 v181, v181, s24, v237
	v_med3_f32 v182, v182, s24, v237
	v_med3_f32 v183, v183, s24, v237
	v_med3_f32 v184, v184, s24, v237
	v_med3_f32 v185, v185, s24, v237
	v_med3_f32 v186, v186, s24, v237
	v_med3_f32 v187, v187, s24, v237
	v_med3_f32 v188, v188, s24, v237
	v_med3_f32 v189, v189, s24, v237
	v_med3_f32 v190, v190, s24, v237
	v_med3_f32 v191, v191, s24, v237
	v_med3_f32 v192, v192, s24, v237
	v_med3_f32 v193, v193, s24, v237
	v_cvt_pk_fp8_f32 v130, v130, v134
	v_cvt_pk_fp8_f32 v130, v138, v142 op_sel:[0,0,1]
	v_cvt_pk_fp8_f32 v134, v131, v135
	v_cvt_pk_fp8_f32 v134, v139, v143 op_sel:[0,0,1]
	v_cvt_pk_fp8_f32 v138, v132, v136
	v_cvt_pk_fp8_f32 v138, v140, v144 op_sel:[0,0,1]
	v_cvt_pk_fp8_f32 v142, v133, v137
	v_cvt_pk_fp8_f32 v142, v141, v145 op_sel:[0,0,1]
	v_cvt_pk_fp8_f32 v131, v146, v150
	v_cvt_pk_fp8_f32 v131, v154, v158 op_sel:[0,0,1]
	v_cvt_pk_fp8_f32 v135, v147, v151
	v_cvt_pk_fp8_f32 v135, v155, v159 op_sel:[0,0,1]
	v_cvt_pk_fp8_f32 v139, v148, v152
	v_cvt_pk_fp8_f32 v139, v156, v160 op_sel:[0,0,1]
	v_cvt_pk_fp8_f32 v143, v149, v153
	v_cvt_pk_fp8_f32 v143, v157, v161 op_sel:[0,0,1]
	v_cvt_pk_fp8_f32 v132, v162, v166
	v_cvt_pk_fp8_f32 v132, v170, v174 op_sel:[0,0,1]
	v_cvt_pk_fp8_f32 v136, v163, v167
	v_cvt_pk_fp8_f32 v136, v171, v175 op_sel:[0,0,1]
	v_cvt_pk_fp8_f32 v140, v164, v168
	v_cvt_pk_fp8_f32 v140, v172, v176 op_sel:[0,0,1]
	v_cvt_pk_fp8_f32 v144, v165, v169
	v_cvt_pk_fp8_f32 v144, v173, v177 op_sel:[0,0,1]
	v_cvt_pk_fp8_f32 v133, v178, v182
	v_cvt_pk_fp8_f32 v133, v186, v190 op_sel:[0,0,1]
	v_cvt_pk_fp8_f32 v137, v179, v183
	v_cvt_pk_fp8_f32 v137, v187, v191 op_sel:[0,0,1]
	v_cvt_pk_fp8_f32 v141, v180, v184
	v_cvt_pk_fp8_f32 v141, v188, v192 op_sel:[0,0,1]
	v_cvt_pk_fp8_f32 v145, v181, v185
	v_cvt_pk_fp8_f32 v145, v189, v193 op_sel:[0,0,1]
	global_store_dwordx4 v250, v[130:133], s[42:43] nt
	global_store_dwordx4 v250, v[134:137], s[42:43] offset:2048 nt
	global_store_dwordx4 v251, v[138:141], s[42:43] nt
	global_store_dwordx4 v251, v[142:145], s[42:43] offset:2048 nt
	s_add_u32 s42, s42, 0x800000
	s_addc_u32 s43, s43, 0
	s_waitcnt vmcnt(8)
; #define GAS __attribute__((address_space(1)))
; template <bool GAIN, bool NT = false> __device__ __forceinline__ void titem8_store(const TItem& d, int lane, const f32x4 (&r)[16], const f32x4 (&g)[4]) {
;     const int q = lane & 7, kg = lane >> 3; const unsigned lo = (unsigned)((4 * q) * d.ldk + 16 * kg);
;     GAS char* base = (GAS char*)d.dst;
;     f32x4 s[16];
; #pragma unroll
;     for (int j = 0; j < 16; ++j) s[j] = r[j] * ((GAIN ? g[j >> 2][j & 3] : 1.0f) * W8_SCALE);
; #pragma unroll
;     for (int i = 0; i < 4; ++i) { v4u w;
;         w.x = pk4_fp8w(s[0][i], s[1][i], s[2][i], s[3][i]); w.y = pk4_fp8w(s[4][i], s[5][i], s[6][i], s[7][i]);
;         w.z = pk4_fp8w(s[8][i], s[9][i], s[10][i], s[11][i]); w.w = pk4_fp8w(s[12][i], s[13][i], s[14][i], s[15][i]);
;         GAS v4u* p = (GAS v4u*)(base + (size_t)i * (size_t)d.ldk + lo);
;         if (NT) __builtin_nontemporal_store(w, p); else *p = w; }
	v_pk_mul_f32 v[0:1], v[0:1], s[30:31] op_sel_hi:[1,0]
	v_pk_mul_f32 v[2:3], v[2:3], s[30:31] op_sel_hi:[1,0]
	v_pk_mul_f32 v[4:5], v[4:5], s[30:31] op_sel_hi:[1,0]
	v_pk_mul_f32 v[6:7], v[6:7], s[30:31] op_sel_hi:[1,0]
	v_pk_mul_f32 v[8:9], v[8:9], s[30:31] op_sel_hi:[1,0]
	v_pk_mul_f32 v[10:11], v[10:11], s[30:31] op_sel_hi:[1,0]
	v_pk_mul_f32 v[12:13], v[12:13], s[30:31] op_sel_hi:[1,0]
	v_pk_mul_f32 v[14:15], v[14:15], s[30:31] op_sel_hi:[1,0]
	v_pk_mul_f32 v[16:17], v[16:17], s[30:31] op_sel_hi:[1,0]
	v_pk_mul_f32 v[18:19], v[18:19], s[30:31] op_sel_hi:[1,0]
	v_pk_mul_f32 v[20:21], v[20:21], s[30:31] op_sel_hi:[1,0]
	v_pk_mul_f32 v[22:23], v[22:23], s[30:31] op_sel_hi:[1,0]
	v_pk_mul_f32 v[24:25], v[24:25], s[30:31] op_sel_hi:[1,0]
	v_pk_mul_f32 v[26:27], v[26:27], s[30:31] op_sel_hi:[1,0]
	v_pk_mul_f32 v[28:29], v[28:29], s[30:31] op_sel_hi:[1,0]
	v_pk_mul_f32 v[30:31], v[30:31], s[30:31] op_sel_hi:[1,0]
	v_pk_mul_f32 v[32:33], v[32:33], s[30:31] op_sel_hi:[1,0]
	v_pk_mul_f32 v[34:35], v[34:35], s[30:31] op_sel_hi:[1,0]
	v_pk_mul_f32 v[36:37], v[36:37], s[30:31] op_sel_hi:[1,0]
	v_pk_mul_f32 v[38:39], v[38:39], s[30:31] op_sel_hi:[1,0]
	v_pk_mul_f32 v[40:41], v[40:41], s[30:31] op_sel_hi:[1,0]
	v_pk_mul_f32 v[42:43], v[42:43], s[30:31] op_sel_hi:[1,0]
	v_pk_mul_f32 v[44:45], v[44:45], s[30:31] op_sel_hi:[1,0]
	v_pk_mul_f32 v[46:47], v[46:47], s[30:31] op_sel_hi:[1,0]
	v_pk_mul_f32 v[48:49], v[48:49], s[30:31] op_sel_hi:[1,0]
	v_pk_mul_f32 v[50:51], v[50:51], s[30:31] op_sel_hi:[1,0]
	v_pk_mul_f32 v[52:53], v[52:53], s[30:31] op_sel_hi:[1,0]
	v_pk_mul_f32 v[54:55], v[54:55], s[30:31] op_sel_hi:[1,0]
	v_pk_mul_f32 v[56:57], v[56:57], s[30:31] op_sel_hi:[1,0]
	v_pk_mul_f32 v[58:59], v[58:59], s[30:31] op_sel_hi:[1,0]
	v_pk_mul_f32 v[60:61], v[60:61], s[30:31] op_sel_hi:[1,0]
	v_pk_mul_f32 v[62:63], v[62:63], s[30:31] op_sel_hi:[1,0]
	v_med3_f32 v0, v0, s24, v237
	v_med3_f32 v1, v1, s24, v237
	v_med3_f32 v2, v2, s24, v237
	v_med3_f32 v3, v3, s24, v237
	v_med3_f32 v4, v4, s24, v237
	v_med3_f32 v5, v5, s24, v237
	v_med3_f32 v6, v6, s24, v237
	v_med3_f32 v7, v7, s24, v237
	v_med3_f32 v8, v8, s24, v237
	v_med3_f32 v9, v9, s24, v237
	v_med3_f32 v10, v10, s24, v237
	v_med3_f32 v11, v11, s24, v237
	v_med3_f32 v12, v12, s24, v237
	v_med3_f32 v13, v13, s24, v237
	v_med3_f32 v14, v14, s24, v237
	v_med3_f32 v15, v15, s24, v237
	v_med3_f32 v16, v16, s24, v237
	v_med3_f32 v17, v17, s24, v237
	v_med3_f32 v18, v18, s24, v237
	v_med3_f32 v19, v19, s24, v237
	v_med3_f32 v20, v20, s24, v237
	v_med3_f32 v21, v21, s24, v237
	v_med3_f32 v22, v22, s24, v237
	v_med3_f32 v23, v23, s24, v237
	v_med3_f32 v24, v24, s24, v237
	v_med3_f32 v25, v25, s24, v237
	v_med3_f32 v26, v26, s24, v237
	v_med3_f32 v27, v27, s24, v237
	v_med3_f32 v28, v28, s24, v237
	v_med3_f32 v29, v29, s24, v237
	v_med3_f32 v30, v30, s24, v237
	v_med3_f32 v31, v31, s24, v237
	v_med3_f32 v32, v32, s24, v237
	v_med3_f32 v33, v33, s24, v237
	v_med3_f32 v34, v34, s24, v237
	v_med3_f32 v35, v35, s24, v237
	v_med3_f32 v36, v36, s24, v237
	v_med3_f32 v37, v37, s24, v237
	v_med3_f32 v38, v38, s24, v237
	v_med3_f32 v39, v39, s24, v237
	v_med3_f32 v40, v40, s24, v237
	v_med3_f32 v41, v41, s24, v237
	v_med3_f32 v42, v42, s24, v237
	v_med3_f32 v43, v43, s24, v237
	v_med3_f32 v44, v44, s24, v237
	v_med3_f32 v45, v45, s24, v237
	v_med3_f32 v46, v46, s24, v237
	v_med3_f32 v47, v47, s24, v237
	v_med3_f32 v48, v48, s24, v237
	v_med3_f32 v49, v49, s24, v237
	v_med3_f32 v50, v50, s24, v237
	v_med3_f32 v51, v51, s24, v237
	v_med3_f32 v52, v52, s24, v237
	v_med3_f32 v53, v53, s24, v237
	v_med3_f32 v54, v54, s24, v237
	v_med3_f32 v55, v55, s24, v237
	v_med3_f32 v56, v56, s24, v237
	v_med3_f32 v57, v57, s24, v237
	v_med3_f32 v58, v58, s24, v237
	v_med3_f32 v59, v59, s24, v237
	v_med3_f32 v60, v60, s24, v237
	v_med3_f32 v61, v61, s24, v237
	v_med3_f32 v62, v62, s24, v237
	v_med3_f32 v63, v63, s24, v237
	v_cvt_pk_fp8_f32 v0, v0, v4
	v_cvt_pk_fp8_f32 v0, v8, v12 op_sel:[0,0,1]
	v_cvt_pk_fp8_f32 v4, v1, v5
	v_cvt_pk_fp8_f32 v4, v9, v13 op_sel:[0,0,1]
	v_cvt_pk_fp8_f32 v8, v2, v6
	v_cvt_pk_fp8_f32 v8, v10, v14 op_sel:[0,0,1]
	v_cvt_pk_fp8_f32 v12, v3, v7
	v_cvt_pk_fp8_f32 v12, v11, v15 op_sel:[0,0,1]
	v_cvt_pk_fp8_f32 v1, v16, v20
	v_cvt_pk_fp8_f32 v1, v24, v28 op_sel:[0,0,1]
	v_cvt_pk_fp8_f32 v5, v17, v21
	v_cvt_pk_fp8_f32 v5, v25, v29 op_sel:[0,0,1]
	v_cvt_pk_fp8_f32 v9, v18, v22
	v_cvt_pk_fp8_f32 v9, v26, v30 op_sel:[0,0,1]
	v_cvt_pk_fp8_f32 v13, v19, v23
	v_cvt_pk_fp8_f32 v13, v27, v31 op_sel:[0,0,1]
	v_cvt_pk_fp8_f32 v2, v32, v36
	v_cvt_pk_fp8_f32 v2, v40, v44 op_sel:[0,0,1]
	v_cvt_pk_fp8_f32 v6, v33, v37
	v_cvt_pk_fp8_f32 v6, v41, v45 op_sel:[0,0,1]
	v_cvt_pk_fp8_f32 v10, v34, v38
	v_cvt_pk_fp8_f32 v10, v42, v46 op_sel:[0,0,1]
	v_cvt_pk_fp8_f32 v14, v35, v39
	v_cvt_pk_fp8_f32 v14, v43, v47 op_sel:[0,0,1]
	v_cvt_pk_fp8_f32 v3, v48, v52
	v_cvt_pk_fp8_f32 v3, v56, v60 op_sel:[0,0,1]
	v_cvt_pk_fp8_f32 v7, v49, v53
	v_cvt_pk_fp8_f32 v7, v57, v61 op_sel:[0,0,1]
	v_cvt_pk_fp8_f32 v11, v50, v54
	v_cvt_pk_fp8_f32 v11, v58, v62 op_sel:[0,0,1]
	v_cvt_pk_fp8_f32 v15, v51, v55
	v_cvt_pk_fp8_f32 v15, v59, v63 op_sel:[0,0,1]
	global_store_dwordx4 v250, v[0:3], s[42:43] nt
	global_store_dwordx4 v250, v[4:7], s[42:43] offset:2048 nt
	global_store_dwordx4 v251, v[8:11], s[42:43] nt
	global_store_dwordx4 v251, v[12:15], s[42:43] offset:2048 nt
	s_add_u32 s42, s42, 0x800000
	s_addc_u32 s43, s43, 0
	v_mov_b32_e32 v65, 0

; #define LAS __attribute__((address_space(3)))
; #define LANE_NOW() ({ int l_ = lane_id_now(); asm volatile("" : "+v"(l_)); l_; })
; __device__ __forceinline__ int moe_block_table(const unsigned* counts, LAS int* blkE, int tid) {
;     if (tid < 64) {
;         const int cnt = tid < E ? (int)counts[tid * CNT_STRIDE] : 0, nb = (cnt + 255) >> 8;
;         int inc = nb;
; #pragma unroll
;         for (int o = 1; o < 64; o <<= 1) { const int v = __shfl_up(inc, o); if (tid >= o) inc += v; }
;         const int base = inc - nb;
;         for (int j = 0; j < nb; ++j) { blkE[base + j] = tid; blkE[160 + base + j] = j; const int left = cnt - j * 256; blkE[320 + base + j] = left < 256 ? left : 256; }
;         if (tid == 63) blkE[480] = inc;
;     }
;     __syncthreads();
;     return blkE[480];
; }
; __global__ void __launch_bounds__(NTHR, 2) fwd(Args args) {
;     ...
;     if (IN(13)) {
;         const int lane = LANE_NOW(), tid = wave * 64 + lane; (void)tid; (void)lane;
;         LAS int* blkE = (LAS int*)(lds + BLK_OFF);
;         __syncthreads();
;         const int NBt = moe_block_table(ctl + CW_CNT, blkE, tid);
.LBB0_1586:
	s_cmp_gt_i32 s80, 13
	s_cselect_b64 s[0:1], -1, 0
	s_cmp_lt_i32 s81, 14
	s_cselect_b64 s[2:3], -1, 0
	s_or_b64 s[0:1], s[0:1], s[2:3]
	s_and_b64 vcc, exec, s[0:1]
	s_cbranch_vccnz .LBB0_1669
	s_waitcnt vmcnt(0)
	v_mov_b32_e32 v0, 0
	v_mov_b32_e32 v4, 0
	v_mbcnt_lo_u32_b32 v0, -1, v0
	v_mbcnt_hi_u32_b32 v0, -1, v0
	s_waitcnt lgkmcnt(0)
	v_add_u32_e32 v2, s94, v0
	v_cmp_gt_i32_e32 vcc, 64, v2
	s_barrier
	s_and_saveexec_b64 s[4:5], vcc
	s_branch .LBB0_1605
	v_cmp_gt_i32_e64 s[0:1], 32, v2
	s_and_saveexec_b64 s[6:7], s[0:1]
	s_cbranch_execz .LBB0_1590
	v_lshlrev_b32_e32 v0, 6, v2
	v_ashrrev_i32_e32 v1, 31, v0
	v_lshl_add_u64 v[0:1], v[0:1], 2, s[78:79]
	v_add_co_u32_e32 v0, vcc, 0x30000, v0
	s_nop 1
	v_addc_co_u32_e32 v1, vcc, 0, v1, vcc
	global_load_dword v4, v[0:1], off
